# v8 + 8-phase GEMM loops: LDS-DMA stage loads issued between the MFMAs (after the phase barrier) instead of in the read segment; counted vmcnt 6->4
# baseline (speedup 1.0000x reference)
.LBB0_249:
	s_add_u32 s31, s26, 0xfffc0080
	s_addc_u32 s33, s27, -1
	s_add_i32 s34, 0, 0x10000
	v_add_u32_e32 v0, s34, v138
	ds_read_b128 v[140:143], v0
	ds_read_b128 v[144:147], v0 offset:1024
	ds_read_b128 v[148:151], v0 offset:2048
	ds_read_b128 v[152:155], v0 offset:3072
	s_cmp_eq_u32 s30, 12
	s_cselect_b32 s49, s3, s33
	s_cselect_b32 s48, s5, s31
	s_cselect_b32 s47, s20, s25
	s_cselect_b32 s46, s21, s22
	v_mov_b32_e32 v0, v136
	ds_read_b128 v[156:159], v139
	ds_read_b128 v[160:163], v139 offset:1024
	ds_read_b128 v[172:175], v139 offset:2048
	ds_read_b128 v[176:179], v139 offset:3072
	ds_read_b128 v[180:183], v139 offset:4096
	ds_read_b128 v[184:187], v139 offset:5120
	ds_read_b128 v[188:191], v139 offset:6144
	ds_read_b128 v[192:195], v139 offset:7168
	s_nop 0
	v_mov_b32_e32 v0, v137
	s_nop 0
	s_waitcnt lgkmcnt(8)
	s_barrier
	s_waitcnt lgkmcnt(0)
	s_setprio 1
	v_mov_b64_e32 v[50:51], v[164:165]
	s_waitcnt lgkmcnt(0)
	v_mfma_scale_f32_16x16x128_f8f6f4 v[98:101], v[156:163], v[148:155], v[98:101], v202, v202 op_sel_hi:[0,0,0]
	v_mov_b64_e32 v[52:53], v[166:167]
	v_mfma_scale_f32_16x16x128_f8f6f4 v[164:167], v[172:179], v[140:147], v[118:121], v202, v202 op_sel_hi:[0,0,0]
	s_add_i32 m0, s1, 0xc000
	v_mfma_scale_f32_16x16x128_f8f6f4 v[90:93], v[180:187], v[148:155], v[90:93], v202, v202 op_sel_hi:[0,0,0]
	global_load_lds_dwordx4 v136, s[26:27]
	v_mfma_scale_f32_16x16x128_f8f6f4 v[130:133], v[156:163], v[140:147], v[126:129], v202, v202 op_sel_hi:[0,0,0]
	v_mfma_scale_f32_16x16x128_f8f6f4 v[168:171], v[172:179], v[148:155], v[86:89], v202, v202 op_sel_hi:[0,0,0]
	s_add_i32 m0, s1, 0xe000
	v_mfma_scale_f32_16x16x128_f8f6f4 v[196:199], v[180:187], v[140:147], v[122:125], v202, v202 op_sel_hi:[0,0,0]
	global_load_lds_dwordx4 v137, s[26:27]
	v_mfma_scale_f32_16x16x128_f8f6f4 v[206:209], v[188:195], v[140:147], v[114:117], v202, v202 op_sel_hi:[0,0,0]
	v_mfma_scale_f32_16x16x128_f8f6f4 v[210:213], v[188:195], v[148:155], v[82:85], v202, v202 op_sel_hi:[0,0,0]
	s_setprio 0
	s_barrier
	s_add_i32 s31, 0, 0x14000
	v_add_u32_e32 v0, s31, v138
	s_nop 2
	ds_read_b128 v[82:85], v0
	ds_read_b128 v[86:89], v0 offset:1024
	ds_read_b128 v[114:117], v0 offset:2048
	ds_read_b128 v[118:121], v0 offset:3072
	v_mov_b32_e32 v0, v136
	s_add_i32 s33, s34, s73
	s_nop 0
	v_mov_b32_e32 v0, v137
	s_nop 0
	s_barrier
	s_waitcnt lgkmcnt(0)
	s_setprio 1
	s_waitcnt lgkmcnt(0)
	v_mfma_scale_f32_16x16x128_f8f6f4 v[66:69], v[156:163], v[82:89], v[66:69], v202, v202 op_sel_hi:[0,0,0]
	v_mfma_scale_f32_16x16x128_f8f6f4 v[38:41], v[156:163], v[114:121], v[38:41], v202, v202 op_sel_hi:[0,0,0]
	s_mov_b32 m0, s33
	v_mfma_scale_f32_16x16x128_f8f6f4 v[58:61], v[180:187], v[82:89], v[58:61], v202, v202 op_sel_hi:[0,0,0]
	global_load_lds_dwordx4 v136, s[46:47]
	v_mfma_scale_f32_16x16x128_f8f6f4 v[214:217], v[172:179], v[82:89], v[54:57], v202, v202 op_sel_hi:[0,0,0]
	v_mfma_scale_f32_16x16x128_f8f6f4 v[172:175], v[172:179], v[114:121], v[22:25], v202, v202 op_sel_hi:[0,0,0]
	s_add_i32 m0, s33, 0x2000
	v_mfma_scale_f32_16x16x128_f8f6f4 v[176:179], v[180:187], v[114:121], v[30:33], v202, v202 op_sel_hi:[0,0,0]
	global_load_lds_dwordx4 v137, s[46:47]
	v_mfma_scale_f32_16x16x128_f8f6f4 v[180:183], v[188:195], v[82:89], v[18:21], v202, v202 op_sel_hi:[0,0,0]
	v_mfma_scale_f32_16x16x128_f8f6f4 v[184:187], v[188:195], v[114:121], v[50:53], v202, v202 op_sel_hi:[0,0,0]
	s_setprio 0
	v_mov_b32_e32 v0, v136
	s_barrier
	s_nop 1
	ds_read_b128 v[18:21], v139 offset:16384
	ds_read_b128 v[22:25], v139 offset:17408
	ds_read_b128 v[50:53], v139 offset:18432
	ds_read_b128 v[54:57], v139 offset:19456
	ds_read_b128 v[122:125], v139 offset:20480
	ds_read_b128 v[126:129], v139 offset:21504
	ds_read_b128 v[156:159], v139 offset:22528
	ds_read_b128 v[160:163], v139 offset:23552
	s_nop 0
	v_mov_b32_e32 v0, v137
	s_nop 0
	s_barrier
	s_waitcnt lgkmcnt(0)
	s_setprio 1
	s_waitcnt lgkmcnt(0)
	v_mfma_scale_f32_16x16x128_f8f6f4 v[110:113], v[18:25], v[140:147], v[110:113], v202, v202 op_sel_hi:[0,0,0]
	v_mfma_scale_f32_16x16x128_f8f6f4 v[78:81], v[18:25], v[148:155], v[78:81], v202, v202 op_sel_hi:[0,0,0]
	s_mov_b32 m0, s1
	v_mfma_scale_f32_16x16x128_f8f6f4 v[102:105], v[50:57], v[140:147], v[102:105], v202, v202 op_sel_hi:[0,0,0]
	global_load_lds_dwordx4 v136, s[48:49]
	v_mfma_scale_f32_16x16x128_f8f6f4 v[106:109], v[122:129], v[140:147], v[106:109], v202, v202 op_sel_hi:[0,0,0]
	v_mfma_scale_f32_16x16x128_f8f6f4 v[94:97], v[156:163], v[140:147], v[94:97], v202, v202 op_sel_hi:[0,0,0]
	s_mov_b32 m0, s13
	v_mfma_scale_f32_16x16x128_f8f6f4 v[62:65], v[156:163], v[148:155], v[62:65], v202, v202 op_sel_hi:[0,0,0]
	global_load_lds_dwordx4 v137, s[48:49]
	v_mfma_scale_f32_16x16x128_f8f6f4 v[218:221], v[50:57], v[148:155], v[70:73], v202, v202 op_sel_hi:[0,0,0]
	v_mfma_scale_f32_16x16x128_f8f6f4 v[222:225], v[122:129], v[148:155], v[74:77], v202, v202 op_sel_hi:[0,0,0]
	s_setprio 0
	s_barrier
	s_add_u32 s34, s46, 0x40000
	s_addc_u32 s35, s47, 0
	v_mov_b32_e32 v0, v136
	s_add_i32 s31, s31, s73
	s_mov_b32 s100, s31
	s_nop 0
	v_mov_b32_e32 v0, v137
	s_add_i32 s101, s31, 0x2000
	s_nop 0
	s_waitcnt vmcnt(4)
	s_barrier
	s_setprio 1
	v_mfma_scale_f32_16x16x128_f8f6f4 v[34:37], v[50:57], v[82:89], v[34:37], v202, v202 op_sel_hi:[0,0,0]
	v_mfma_scale_f32_16x16x128_f8f6f4 v[226:229], v[18:25], v[82:89], v[46:49], v202, v202 op_sel_hi:[0,0,0]
	s_mov_b32 m0, s100
	v_mfma_scale_f32_16x16x128_f8f6f4 v[230:233], v[18:25], v[114:121], v[14:17], v202, v202 op_sel_hi:[0,0,0]
	global_load_lds_dwordx4 v136, s[34:35]
	v_mfma_scale_f32_16x16x128_f8f6f4 v[234:237], v[50:57], v[114:121], v[6:9], v202, v202 op_sel_hi:[0,0,0]
	v_mfma_scale_f32_16x16x128_f8f6f4 v[238:241], v[122:129], v[82:89], v[42:45], v202, v202 op_sel_hi:[0,0,0]
	s_mov_b32 m0, s101
	v_mfma_scale_f32_16x16x128_f8f6f4 v[242:245], v[122:129], v[114:121], v[10:13], v202, v202 op_sel_hi:[0,0,0]
	global_load_lds_dwordx4 v137, s[34:35]
	v_mfma_scale_f32_16x16x128_f8f6f4 v[246:249], v[156:163], v[82:89], v[26:29], v202, v202 op_sel_hi:[0,0,0]
	v_mfma_scale_f32_16x16x128_f8f6f4 v[50:53], v[156:163], v[114:121], v[2:5], v202, v202 op_sel_hi:[0,0,0]
	s_setprio 0
	s_add_i32 s31, 0, 0x18000
	v_add_u32_e32 v0, s31, v138
	s_barrier
	s_nop 2
	ds_read_b128 v[2:5], v0
	ds_read_b128 v[6:9], v0 offset:1024
	ds_read_b128 v[10:13], v0 offset:2048
	ds_read_b128 v[14:17], v0 offset:3072
	s_add_u32 s34, s48, 0x40000
	v_mov_b32_e32 v0, v136
	ds_read_b128 v[18:21], v139 offset:32768
	ds_read_b128 v[22:25], v139 offset:33792
	ds_read_b128 v[26:29], v139 offset:34816
	ds_read_b128 v[30:33], v139 offset:35840
	ds_read_b128 v[42:45], v139 offset:36864
	ds_read_b128 v[46:49], v139 offset:37888
	ds_read_b128 v[70:73], v139 offset:38912
	ds_read_b128 v[74:77], v139 offset:39936
	s_addc_u32 s35, s49, 0
	s_nop 0
	v_mov_b32_e32 v0, v137
	s_nop 0
	s_waitcnt lgkmcnt(8)
	s_barrier
	s_waitcnt lgkmcnt(0)
	s_setprio 1
	s_waitcnt lgkmcnt(0)
	v_mfma_scale_f32_16x16x128_f8f6f4 v[126:129], v[18:25], v[2:9], v[130:133], v202, v202 op_sel_hi:[0,0,0]
	v_mfma_scale_f32_16x16x128_f8f6f4 v[98:101], v[18:25], v[10:17], v[98:101], v202, v202 op_sel_hi:[0,0,0]
	s_mov_b32 m0, s14
	v_mfma_scale_f32_16x16x128_f8f6f4 v[118:121], v[26:33], v[2:9], v[164:167], v202, v202 op_sel_hi:[0,0,0]
	global_load_lds_dwordx4 v136, s[34:35]
	v_mfma_scale_f32_16x16x128_f8f6f4 v[86:89], v[26:33], v[10:17], v[168:171], v202, v202 op_sel_hi:[0,0,0]
	v_mfma_scale_f32_16x16x128_f8f6f4 v[122:125], v[42:49], v[2:9], v[196:199], v202, v202 op_sel_hi:[0,0,0]
	s_mov_b32 m0, s15
	v_mfma_scale_f32_16x16x128_f8f6f4 v[90:93], v[42:49], v[10:17], v[90:93], v202, v202 op_sel_hi:[0,0,0]
	global_load_lds_dwordx4 v137, s[34:35]
	v_mfma_scale_f32_16x16x128_f8f6f4 v[114:117], v[70:77], v[2:9], v[206:209], v202, v202 op_sel_hi:[0,0,0]
	v_mfma_scale_f32_16x16x128_f8f6f4 v[82:85], v[70:77], v[10:17], v[210:213], v202, v202 op_sel_hi:[0,0,0]
	s_setprio 0
	s_barrier
	s_add_i32 s33, 0, 0x1c000
	v_add_u32_e32 v0, s33, v138
	ds_read_b128 v[140:143], v0
	ds_read_b128 v[144:147], v0 offset:1024
	ds_read_b128 v[148:151], v0 offset:2048
	ds_read_b128 v[152:155], v0 offset:3072
	v_mov_b32_e32 v0, v136
	s_add_i32 s31, s31, s73
	v_lshl_add_u64 v[54:55], s[46:47], 0, v[0:1]
	v_lshl_add_u64 v[54:55], v[54:55], 0, s[66:67]
	v_mov_b32_e32 v0, v137
	v_lshl_add_u64 v[54:55], s[46:47], 0, v[0:1]
	v_lshl_add_u64 v[54:55], v[54:55], 0, s[66:67]
	s_barrier
	s_waitcnt lgkmcnt(0)
	s_setprio 1
	s_waitcnt lgkmcnt(0)
	v_mfma_scale_f32_16x16x128_f8f6f4 v[66:69], v[18:25], v[140:147], v[66:69], v202, v202 op_sel_hi:[0,0,0]
	v_mfma_scale_f32_16x16x128_f8f6f4 v[38:41], v[18:25], v[148:155], v[38:41], v202, v202 op_sel_hi:[0,0,0]
	s_add_u32 s98, s46, s66
	s_addc_u32 s99, s47, s67
	s_mov_b32 m0, s31
	v_mfma_scale_f32_16x16x128_f8f6f4 v[54:57], v[26:33], v[140:147], v[214:217], v202, v202 op_sel_hi:[0,0,0]
	global_load_lds_dwordx4 v136, s[98:99]
	v_mfma_scale_f32_16x16x128_f8f6f4 v[22:25], v[26:33], v[148:155], v[172:175], v202, v202 op_sel_hi:[0,0,0]
	v_mfma_scale_f32_16x16x128_f8f6f4 v[58:61], v[42:49], v[140:147], v[58:61], v202, v202 op_sel_hi:[0,0,0]
	s_add_i32 m0, s31, 0x2000
	v_mfma_scale_f32_16x16x128_f8f6f4 v[30:33], v[42:49], v[148:155], v[176:179], v202, v202 op_sel_hi:[0,0,0]
	global_load_lds_dwordx4 v137, s[98:99]
	v_mfma_scale_f32_16x16x128_f8f6f4 v[18:21], v[70:77], v[140:147], v[180:183], v202, v202 op_sel_hi:[0,0,0]
	v_mfma_scale_f32_16x16x128_f8f6f4 v[164:167], v[70:77], v[148:155], v[184:187], v202, v202 op_sel_hi:[0,0,0]
	s_setprio 0
	v_mov_b32_e32 v0, v136
	s_barrier
	ds_read_b128 v[156:159], v139 offset:49152
	ds_read_b128 v[160:163], v139 offset:50176
	ds_read_b128 v[172:175], v139 offset:51200
	ds_read_b128 v[176:179], v139 offset:52224
	ds_read_b128 v[180:183], v139 offset:53248
	ds_read_b128 v[184:187], v139 offset:54272
	ds_read_b128 v[188:191], v139 offset:55296
	ds_read_b128 v[192:195], v139 offset:56320
	v_lshl_add_u64 v[26:27], s[48:49], 0, v[0:1]
	v_lshl_add_u64 v[26:27], v[26:27], 0, s[66:67]
	v_mov_b32_e32 v0, v137
	v_lshl_add_u64 v[26:27], s[48:49], 0, v[0:1]
	v_lshl_add_u64 v[26:27], v[26:27], 0, s[66:67]
	s_barrier
	s_waitcnt lgkmcnt(0)
	s_setprio 1
	s_waitcnt lgkmcnt(0)
	v_mfma_scale_f32_16x16x128_f8f6f4 v[110:113], v[156:163], v[2:9], v[110:113], v202, v202 op_sel_hi:[0,0,0]
	v_mfma_scale_f32_16x16x128_f8f6f4 v[78:81], v[156:163], v[10:17], v[78:81], v202, v202 op_sel_hi:[0,0,0]
	s_add_u32 s98, s48, s66
	s_addc_u32 s99, s49, s67
	s_mov_b32 m0, s17
	v_mfma_scale_f32_16x16x128_f8f6f4 v[102:105], v[172:179], v[2:9], v[102:105], v202, v202 op_sel_hi:[0,0,0]
	global_load_lds_dwordx4 v136, s[98:99]
	v_mfma_scale_f32_16x16x128_f8f6f4 v[70:73], v[172:179], v[10:17], v[218:221], v202, v202 op_sel_hi:[0,0,0]
	v_mfma_scale_f32_16x16x128_f8f6f4 v[106:109], v[180:187], v[2:9], v[106:109], v202, v202 op_sel_hi:[0,0,0]
	s_mov_b32 m0, s18
	v_mfma_scale_f32_16x16x128_f8f6f4 v[74:77], v[180:187], v[10:17], v[222:225], v202, v202 op_sel_hi:[0,0,0]
	global_load_lds_dwordx4 v137, s[98:99]
	v_mfma_scale_f32_16x16x128_f8f6f4 v[94:97], v[188:195], v[2:9], v[94:97], v202, v202 op_sel_hi:[0,0,0]
	v_mfma_scale_f32_16x16x128_f8f6f4 v[62:65], v[188:195], v[10:17], v[62:65], v202, v202 op_sel_hi:[0,0,0]
	s_setprio 0
	s_barrier
	s_add_u32 s34, s46, 0x40080
	s_addc_u32 s35, s47, 0
	v_mov_b32_e32 v0, v136
	s_add_i32 s31, s33, s73
	s_nop 0
	v_mov_b32_e32 v0, v137
	s_nop 0
	s_waitcnt vmcnt(4)
	s_barrier
	s_setprio 1
	v_mfma_scale_f32_16x16x128_f8f6f4 v[46:49], v[156:163], v[140:147], v[226:229], v202, v202 op_sel_hi:[0,0,0]
	v_mfma_scale_f32_16x16x128_f8f6f4 v[14:17], v[156:163], v[148:155], v[230:233], v202, v202 op_sel_hi:[0,0,0]
	s_mov_b32 m0, s31
	v_mfma_scale_f32_16x16x128_f8f6f4 v[34:37], v[172:179], v[140:147], v[34:37], v202, v202 op_sel_hi:[0,0,0]
	global_load_lds_dwordx4 v136, s[34:35]
	v_mfma_scale_f32_16x16x128_f8f6f4 v[6:9], v[172:179], v[148:155], v[234:237], v202, v202 op_sel_hi:[0,0,0]
	v_mfma_scale_f32_16x16x128_f8f6f4 v[42:45], v[180:187], v[140:147], v[238:241], v202, v202 op_sel_hi:[0,0,0]
	s_add_i32 m0, s31, 0x2000
	v_mfma_scale_f32_16x16x128_f8f6f4 v[10:13], v[180:187], v[148:155], v[242:245], v202, v202 op_sel_hi:[0,0,0]
	global_load_lds_dwordx4 v137, s[34:35]
	v_mfma_scale_f32_16x16x128_f8f6f4 v[26:29], v[188:195], v[140:147], v[246:249], v202, v202 op_sel_hi:[0,0,0]
	v_mfma_scale_f32_16x16x128_f8f6f4 v[2:5], v[188:195], v[148:155], v[50:53], v202, v202 op_sel_hi:[0,0,0]
	s_setprio 0
	s_add_i32 s30, s30, 2
	s_add_u32 s26, s26, 0x100
	s_addc_u32 s27, s27, 0
	s_add_u32 s22, s22, 0x100
	s_addc_u32 s25, s25, 0
	s_cmp_gt_u32 s30, 13
	s_barrier
	s_cbranch_scc0 .LBB0_249
	s_mul_hi_i32 s3, s24, 0x2aaaaaab
	s_lshr_b32 s5, s3, 31
	s_lshr_b32 s3, s3, 1
	s_add_i32 s3, s3, s5
	s_lshl_b32 s5, s24, 1
	s_and_b32 s5, s5, 6
	s_and_b32 s20, s12, -16
	s_lshl_b32 s3, s3, 3
	s_or_b32 s5, s5, s20
	s_add_i32 s24, s5, s3
	v_readlane_b32 s3, v252, 41
	v_mbcnt_lo_u32_b32 v0, -1, 0
	v_mbcnt_hi_u32_b32 v0, -1, v0
	s_ashr_i32 s25, s24, 31
	s_lshl_b64 s[20:21], s[24:25], 19
	v_and_or_b32 v51, v0, 15, s3
	s_lshl_b32 s3, s12, 8
	s_and_b32 s22, s3, 0xf00
	v_ashrrev_i32_e32 v50, 4, v0
	s_add_u32 s20, s87, s20
	v_readlane_b32 s3, v252, 59
	v_lshlrev_b32_e32 v0, 5, v50
	v_lshlrev_b32_e32 v50, 3, v50
	v_lshlrev_b32_e32 v132, 12, v51
	v_mov_b32_e32 v133, v1
	s_addc_u32 s21, s3, s21
	v_and_b32_e32 v130, -16, v50
	v_lshl_add_u64 v[50:51], s[20:21], 0, v[132:133]
	v_lshl_add_u64 v[50:51], v[50:51], 0, s[22:23]
	v_and_b32_e32 v0, 32, v0
	v_lshl_add_u64 v[50:51], v[50:51], 0, s[28:29]
	v_pk_mul_f32 v[52:53], v[126:127], s[68:69] op_sel_hi:[1,0]
	v_mov_b32_e32 v126, v1
	v_ashrrev_i32_e32 v131, 31, v130
	v_lshl_add_u64 v[50:51], v[50:51], 0, v[0:1]
	v_cvt_pk_fp8_f32 v126, v52, v53
	v_pk_mul_f32 v[52:53], v[122:123], s[68:69] op_sel_hi:[1,0]
	v_mov_b32_e32 v127, v1
	v_lshl_add_u64 v[134:135], v[50:51], 0, v[130:131]
	v_pk_mul_f32 v[50:51], v[128:129], s[68:69] op_sel_hi:[1,0]
	v_cvt_pk_fp8_f32 v127, v52, v53
	v_pk_mul_f32 v[52:53], v[118:119], s[68:69] op_sel_hi:[1,0]
	v_mov_b32_e32 v128, v1
	v_cvt_pk_fp8_f32 v128, v52, v53
	v_pk_mul_f32 v[52:53], v[114:115], s[68:69] op_sel_hi:[1,0]
	v_mov_b32_e32 v129, v1
	v_cvt_pk_fp8_f32 v129, v52, v53
	v_cvt_pk_fp8_f32 v126, v50, v51 op_sel:[0,0,1]
	v_pk_mul_f32 v[50:51], v[124:125], s[68:69] op_sel_hi:[1,0]
	v_pk_mul_f32 v[52:53], v[110:111], s[68:69] op_sel_hi:[1,0]
	v_cvt_pk_fp8_f32 v127, v50, v51 op_sel:[0,0,1]
	v_pk_mul_f32 v[50:51], v[120:121], s[68:69] op_sel_hi:[1,0]
	v_mov_b32_e32 v110, v1
	v_cvt_pk_fp8_f32 v128, v50, v51 op_sel:[0,0,1]
	v_pk_mul_f32 v[50:51], v[116:117], s[68:69] op_sel_hi:[1,0]
	v_cvt_pk_fp8_f32 v110, v52, v53
	v_pk_mul_f32 v[52:53], v[106:107], s[68:69] op_sel_hi:[1,0]
	v_mov_b32_e32 v111, v1
	v_cvt_pk_fp8_f32 v129, v50, v51 op_sel:[0,0,1]
	v_pk_mul_f32 v[50:51], v[112:113], s[68:69] op_sel_hi:[1,0]
	v_cvt_pk_fp8_f32 v111, v52, v53
	v_pk_mul_f32 v[52:53], v[102:103], s[68:69] op_sel_hi:[1,0]
	v_mov_b32_e32 v112, v1
	v_cvt_pk_fp8_f32 v112, v52, v53
	v_cvt_pk_fp8_f32 v110, v50, v51 op_sel:[0,0,1]
	v_pk_mul_f32 v[50:51], v[108:109], s[68:69] op_sel_hi:[1,0]
	v_pk_mul_f32 v[52:53], v[94:95], s[68:69] op_sel_hi:[1,0]
	v_cvt_pk_fp8_f32 v111, v50, v51 op_sel:[0,0,1]
	v_pk_mul_f32 v[50:51], v[104:105], s[68:69] op_sel_hi:[1,0]
	v_mov_b32_e32 v94, v1
	v_cvt_pk_fp8_f32 v112, v50, v51 op_sel:[0,0,1]
	v_pk_mul_f32 v[50:51], v[96:97], s[68:69] op_sel_hi:[1,0]
	v_pk_mul_f32 v[96:97], v[98:99], s[68:69] op_sel_hi:[1,0]
	v_pk_mul_f32 v[90:91], v[90:91], s[68:69] op_sel_hi:[1,0]
	v_cvt_pk_fp8_f32 v94, v96, v97
	v_mov_b32_e32 v95, v1
	v_cvt_pk_fp8_f32 v95, v90, v91
	v_pk_mul_f32 v[86:87], v[86:87], s[68:69] op_sel_hi:[1,0]
	v_mov_b32_e32 v96, v1
	v_mov_b32_e32 v113, v1
	v_cvt_pk_fp8_f32 v96, v86, v87
	v_pk_mul_f32 v[82:83], v[82:83], s[68:69] op_sel_hi:[1,0]
	v_mov_b32_e32 v97, v1
	v_cvt_pk_fp8_f32 v113, v52, v53
	v_pk_mul_f32 v[52:53], v[100:101], s[68:69] op_sel_hi:[1,0]
	v_cvt_pk_fp8_f32 v97, v82, v83
	v_cvt_pk_fp8_f32 v94, v52, v53 op_sel:[0,0,1]
	v_pk_mul_f32 v[52:53], v[92:93], s[68:69] op_sel_hi:[1,0]
	s_mov_b32 s5, 0x10000
	v_cvt_pk_fp8_f32 v95, v52, v53 op_sel:[0,0,1]
	v_pk_mul_f32 v[52:53], v[88:89], s[68:69] op_sel_hi:[1,0]
	v_pk_mul_f32 v[74:75], v[74:75], s[68:69] op_sel_hi:[1,0]
	v_cvt_pk_fp8_f32 v96, v52, v53 op_sel:[0,0,1]
	v_pk_mul_f32 v[52:53], v[84:85], s[68:69] op_sel_hi:[1,0]
	v_permlane32_swap_b32_e32 v94, v95
	v_cvt_pk_fp8_f32 v97, v52, v53 op_sel:[0,0,1]
	v_add_co_u32_e32 v52, vcc, s5, v134
	v_pk_mul_f32 v[70:71], v[70:71], s[68:69] op_sel_hi:[1,0]
	v_permlane32_swap_b32_e32 v96, v97
	v_addc_co_u32_e32 v53, vcc, 0, v135, vcc
	global_store_dwordx4 v[52:53], v[94:97], off
	v_pk_mul_f32 v[52:53], v[80:81], s[68:69] op_sel_hi:[1,0]
	v_pk_mul_f32 v[80:81], v[78:79], s[68:69] op_sel_hi:[1,0]
	v_mov_b32_e32 v78, v1
	v_cvt_pk_fp8_f32 v78, v80, v81
	v_mov_b32_e32 v79, v1
	v_cvt_pk_fp8_f32 v79, v74, v75
	v_mov_b32_e32 v80, v1
	v_cvt_pk_fp8_f32 v80, v70, v71
	v_pk_mul_f32 v[62:63], v[62:63], s[68:69] op_sel_hi:[1,0]
	v_mov_b32_e32 v81, v1
	v_cvt_pk_fp8_f32 v81, v62, v63
	v_cvt_pk_fp8_f32 v78, v52, v53 op_sel:[0,0,1]
	v_pk_mul_f32 v[52:53], v[76:77], s[68:69] op_sel_hi:[1,0]
	v_pk_mul_f32 v[18:19], v[18:19], s[68:69] op_sel_hi:[1,0]
	v_cvt_pk_fp8_f32 v79, v52, v53 op_sel:[0,0,1]
	v_pk_mul_f32 v[52:53], v[72:73], s[68:69] op_sel_hi:[1,0]
	v_pk_mul_f32 v[20:21], v[20:21], s[68:69] op_sel_hi:[1,0]
	v_cvt_pk_fp8_f32 v80, v52, v53 op_sel:[0,0,1]
	v_pk_mul_f32 v[52:53], v[64:65], s[68:69] op_sel_hi:[1,0]
	s_or_b32 s20, s24, 1
	v_cvt_pk_fp8_f32 v81, v52, v53 op_sel:[0,0,1]
	v_pk_mul_f32 v[52:53], v[66:67], s[68:69] op_sel_hi:[1,0]
	v_mov_b32_e32 v67, v1
	v_cvt_pk_fp8_f32 v67, v18, v19
	v_pk_mul_f32 v[18:19], v[48:49], s[68:69] op_sel_hi:[1,0]
	v_mov_b32_e32 v48, v1
	s_ashr_i32 s21, s20, 31
	v_cvt_pk_fp8_f32 v67, v20, v21 op_sel:[0,0,1]
	v_pk_mul_f32 v[20:21], v[46:47], s[68:69] op_sel_hi:[1,0]
	v_mov_b32_e32 v46, v1
	v_cvt_pk_fp8_f32 v46, v20, v21
	v_pk_mul_f32 v[20:21], v[42:43], s[68:69] op_sel_hi:[1,0]
	v_mov_b32_e32 v47, v1
	v_cvt_pk_fp8_f32 v47, v20, v21
	v_pk_mul_f32 v[20:21], v[34:35], s[68:69] op_sel_hi:[1,0]
	v_cvt_pk_fp8_f32 v46, v18, v19 op_sel:[0,0,1]
	v_cvt_pk_fp8_f32 v48, v20, v21
	v_pk_mul_f32 v[18:19], v[44:45], s[68:69] op_sel_hi:[1,0]
	v_pk_mul_f32 v[20:21], v[26:27], s[68:69] op_sel_hi:[1,0]
	v_cvt_pk_fp8_f32 v47, v18, v19 op_sel:[0,0,1]
	v_pk_mul_f32 v[18:19], v[36:37], s[68:69] op_sel_hi:[1,0]
	v_mov_b32_e32 v26, v1
	v_cvt_pk_fp8_f32 v48, v18, v19 op_sel:[0,0,1]
	v_pk_mul_f32 v[18:19], v[28:29], s[68:69] op_sel_hi:[1,0]
	v_pk_mul_f32 v[28:29], v[38:39], s[68:69] op_sel_hi:[1,0]
	v_mov_b32_e32 v27, v1
	v_cvt_pk_fp8_f32 v26, v28, v29
	v_pk_mul_f32 v[28:29], v[30:31], s[68:69] op_sel_hi:[1,0]
	v_pk_mul_f32 v[22:23], v[22:23], s[68:69] op_sel_hi:[1,0]
	v_cvt_pk_fp8_f32 v27, v28, v29
	v_mov_b32_e32 v28, v1
	s_lshl_b64 s[20:21], s[20:21], 19
	v_mov_b32_e32 v49, v1
	v_cvt_pk_fp8_f32 v28, v22, v23
	v_pk_mul_f32 v[22:23], v[164:165], s[68:69] op_sel_hi:[1,0]
	v_mov_b32_e32 v29, v1
	s_mov_b64 s[26:27], 0x10000
	s_add_u32 s20, s87, s20
	v_cvt_pk_fp8_f32 v49, v20, v21
	v_pk_mul_f32 v[20:21], v[40:41], s[68:69] op_sel_hi:[1,0]
	v_cvt_pk_fp8_f32 v29, v22, v23
	v_cvt_pk_fp8_f32 v113, v50, v51 op_sel:[0,0,1]
	v_lshl_add_u64 v[50:51], v[134:135], 0, s[26:27]
	v_permlane32_swap_b32_e32 v78, v79
	v_permlane32_swap_b32_e32 v80, v81
	s_addc_u32 s21, s3, s21
	v_cvt_pk_fp8_f32 v26, v20, v21 op_sel:[0,0,1]
	v_pk_mul_f32 v[20:21], v[32:33], s[68:69] op_sel_hi:[1,0]
	global_store_dwordx4 v[50:51], v[78:81], off offset:128
	v_lshl_add_u64 v[50:51], s[20:21], 0, v[132:133]
	v_cvt_pk_fp8_f32 v27, v20, v21 op_sel:[0,0,1]
	v_pk_mul_f32 v[20:21], v[24:25], s[68:69] op_sel_hi:[1,0]
	v_lshl_add_u64 v[50:51], v[50:51], 0, s[22:23]
	v_cvt_pk_fp8_f32 v28, v20, v21 op_sel:[0,0,1]
	v_pk_mul_f32 v[20:21], v[166:167], s[68:69] op_sel_hi:[1,0]
	v_lshl_add_u64 v[50:51], v[50:51], 0, s[28:29]
	v_cvt_pk_fp8_f32 v29, v20, v21 op_sel:[0,0,1]
	v_lshl_add_u64 v[50:51], v[50:51], 0, v[0:1]
	v_lshl_add_u64 v[62:63], v[50:51], 0, v[130:131]
	v_add_co_u32_e32 v20, vcc, s5, v62
	v_permlane32_swap_b32_e32 v26, v27
	v_permlane32_swap_b32_e32 v28, v29
	v_addc_co_u32_e32 v21, vcc, 0, v63, vcc
	global_store_dwordx4 v[20:21], v[26:29], off
	v_pk_mul_f32 v[20:21], v[14:15], s[68:69] op_sel_hi:[1,0]
	v_mov_b32_e32 v14, v1
	v_cvt_pk_fp8_f32 v14, v20, v21
	v_mov_b32_e32 v64, v1
	v_cvt_pk_fp8_f32 v64, v52, v53
	v_pk_mul_f32 v[52:53], v[58:59], s[68:69] op_sel_hi:[1,0]
	v_mov_b32_e32 v65, v1
	v_pk_mul_f32 v[16:17], v[16:17], s[68:69] op_sel_hi:[1,0]
	v_cvt_pk_fp8_f32 v65, v52, v53
	v_pk_mul_f32 v[52:53], v[54:55], s[68:69] op_sel_hi:[1,0]
	v_mov_b32_e32 v66, v1
	v_cvt_pk_fp8_f32 v14, v16, v17 op_sel:[0,0,1]
	v_pk_mul_f32 v[10:11], v[10:11], s[68:69] op_sel_hi:[1,0]
	v_mov_b32_e32 v15, v1
	v_pk_mul_f32 v[6:7], v[6:7], s[68:69] op_sel_hi:[1,0]
	v_mov_b32_e32 v16, v1
	v_pk_mul_f32 v[2:3], v[2:3], s[68:69] op_sel_hi:[1,0]
	v_mov_b32_e32 v17, v1
	v_cvt_pk_fp8_f32 v66, v52, v53
	v_cvt_pk_fp8_f32 v15, v10, v11
	v_cvt_pk_fp8_f32 v16, v6, v7
	v_cvt_pk_fp8_f32 v17, v2, v3
	v_pk_mul_f32 v[50:51], v[68:69], s[68:69] op_sel_hi:[1,0]
	v_pk_mul_f32 v[12:13], v[12:13], s[68:69] op_sel_hi:[1,0]
	v_cvt_pk_fp8_f32 v64, v50, v51 op_sel:[0,0,1]
	v_pk_mul_f32 v[50:51], v[60:61], s[68:69] op_sel_hi:[1,0]
	v_pk_mul_f32 v[8:9], v[8:9], s[68:69] op_sel_hi:[1,0]
	v_cvt_pk_fp8_f32 v65, v50, v51 op_sel:[0,0,1]
	v_pk_mul_f32 v[50:51], v[56:57], s[68:69] op_sel_hi:[1,0]
	v_pk_mul_f32 v[4:5], v[4:5], s[68:69] op_sel_hi:[1,0]
	v_cvt_pk_fp8_f32 v66, v50, v51 op_sel:[0,0,1]
	v_cvt_pk_fp8_f32 v49, v18, v19 op_sel:[0,0,1]
	v_cvt_pk_fp8_f32 v15, v12, v13 op_sel:[0,0,1]
	v_cvt_pk_fp8_f32 v16, v8, v9 op_sel:[0,0,1]
	v_cvt_pk_fp8_f32 v17, v4, v5 op_sel:[0,0,1]
	v_permlane32_swap_b32_e32 v126, v127
	v_permlane32_swap_b32_e32 v128, v129
	v_permlane32_swap_b32_e32 v110, v111
	v_permlane32_swap_b32_e32 v112, v113
	v_permlane32_swap_b32_e32 v64, v65
	v_permlane32_swap_b32_e32 v66, v67
	v_permlane32_swap_b32_e32 v46, v47
	v_permlane32_swap_b32_e32 v48, v49
	v_lshl_add_u64 v[18:19], v[62:63], 0, s[26:27]
	v_permlane32_swap_b32_e32 v14, v15
	v_permlane32_swap_b32_e32 v16, v17
	s_and_b64 vcc, exec, s[10:11]
	s_mov_b32 s12, s2
	s_mov_b32 s24, s4
	s_mov_b64 s[46:47], s[8:9]
	s_mov_b64 s[26:27], s[6:7]
	global_store_dwordx4 v[134:135], v[126:129], off
	global_store_dwordx4 v[134:135], v[110:113], off offset:128
	global_store_dwordx4 v[62:63], v[64:67], off
	global_store_dwordx4 v[62:63], v[46:49], off offset:128
	global_store_dwordx4 v[18:19], v[14:17], off offset:128
	s_cbranch_vccz .LBB0_241
	v_readlane_b32 s0, v252, 50
	s_waitcnt vmcnt(0)
	v_readlane_b32 s1, v252, 51
	s_andn2_b64 vcc, exec, s[0:1]
	s_cbranch_vccnz .LBB0_253
	s_barrier

.LBB0_278:
	s_add_u32 s6, s4, 0xfffc0080
	s_addc_u32 s7, s5, -1
	s_add_i32 s25, 0, 0x10000
	v_add_u32_e32 v0, s25, v207
	ds_read_b128 v[52:55], v0
	ds_read_b128 v[56:59], v0 offset:1024
	ds_read_b128 v[68:71], v0 offset:2048
	ds_read_b128 v[72:75], v0 offset:3072
	s_cmp_eq_u32 s17, 12
	s_cselect_b32 s11, s3, s7
	s_cselect_b32 s10, s9, s6
	s_cselect_b32 s7, s12, s16
	s_cselect_b32 s6, s13, s15
	v_mov_b32_e32 v0, v205
	ds_read_b128 v[84:87], v208
	ds_read_b128 v[88:91], v208 offset:1024
	ds_read_b128 v[92:95], v208 offset:2048
	ds_read_b128 v[96:99], v208 offset:3072
	ds_read_b128 v[172:175], v208 offset:4096
	ds_read_b128 v[176:179], v208 offset:5120
	ds_read_b128 v[180:183], v208 offset:6144
	ds_read_b128 v[184:187], v208 offset:7168
	s_nop 0
	v_mov_b32_e32 v0, v206
	s_nop 0
	s_waitcnt lgkmcnt(8)
	s_barrier
	s_waitcnt lgkmcnt(0)
	s_setprio 1
	s_waitcnt lgkmcnt(0)
	v_mfma_scale_f32_16x16x128_f8f6f4 v[164:167], v[52:59], v[84:91], v[164:167], v202, v202 op_sel_hi:[0,0,0]
	v_mfma_scale_f32_16x16x128_f8f6f4 v[160:163], v[68:75], v[84:91], v[160:163], v202, v202 op_sel_hi:[0,0,0]
	s_add_i32 m0, s18, 0xc000
	v_mfma_scale_f32_16x16x128_f8f6f4 v[156:159], v[52:59], v[92:99], v[156:159], v202, v202 op_sel_hi:[0,0,0]
	global_load_lds_dwordx4 v205, s[4:5]
	v_mfma_scale_f32_16x16x128_f8f6f4 v[152:155], v[68:75], v[92:99], v[152:155], v202, v202 op_sel_hi:[0,0,0]
	v_mfma_scale_f32_16x16x128_f8f6f4 v[148:151], v[52:59], v[172:179], v[148:151], v202, v202 op_sel_hi:[0,0,0]
	s_add_i32 m0, s18, 0xe000
	v_mfma_scale_f32_16x16x128_f8f6f4 v[188:191], v[68:75], v[172:179], v[144:147], v202, v202 op_sel_hi:[0,0,0]
	global_load_lds_dwordx4 v206, s[4:5]
	v_mfma_scale_f32_16x16x128_f8f6f4 v[192:195], v[52:59], v[180:187], v[136:139], v202, v202 op_sel_hi:[0,0,0]
	v_mfma_scale_f32_16x16x128_f8f6f4 v[196:199], v[68:75], v[180:187], v[132:135], v202, v202 op_sel_hi:[0,0,0]
	s_setprio 0
	s_barrier
	s_add_i32 s30, 0, 0x14000
	v_add_u32_e32 v0, s30, v207
	s_nop 2
	ds_read_b128 v[132:135], v0
	ds_read_b128 v[136:139], v0 offset:1024
	ds_read_b128 v[140:143], v0 offset:2048
	ds_read_b128 v[144:147], v0 offset:3072
	v_mov_b32_e32 v0, v205
	s_add_i32 s25, s25, s73
	s_nop 0
	v_mov_b32_e32 v0, v206
	s_nop 0
	s_barrier
	s_waitcnt lgkmcnt(0)
	s_setprio 1
	s_waitcnt lgkmcnt(0)
	v_mfma_scale_f32_16x16x128_f8f6f4 v[128:131], v[132:139], v[84:91], v[128:131], v202, v202 op_sel_hi:[0,0,0]
	v_mfma_scale_f32_16x16x128_f8f6f4 v[124:127], v[140:147], v[84:91], v[124:127], v202, v202 op_sel_hi:[0,0,0]
	s_mov_b32 m0, s25
	v_mfma_scale_f32_16x16x128_f8f6f4 v[120:123], v[132:139], v[92:99], v[120:123], v202, v202 op_sel_hi:[0,0,0]
	global_load_lds_dwordx4 v205, s[6:7]
	v_mfma_scale_f32_16x16x128_f8f6f4 v[116:119], v[140:147], v[92:99], v[116:119], v202, v202 op_sel_hi:[0,0,0]
	v_mfma_scale_f32_16x16x128_f8f6f4 v[210:213], v[132:139], v[172:179], v[112:115], v202, v202 op_sel_hi:[0,0,0]
	s_add_i32 m0, s25, 0x2000
	v_mfma_scale_f32_16x16x128_f8f6f4 v[172:175], v[140:147], v[172:179], v[108:111], v202, v202 op_sel_hi:[0,0,0]
	global_load_lds_dwordx4 v206, s[6:7]
	v_mfma_scale_f32_16x16x128_f8f6f4 v[176:179], v[132:139], v[180:187], v[104:107], v202, v202 op_sel_hi:[0,0,0]
	v_mfma_scale_f32_16x16x128_f8f6f4 v[180:183], v[140:147], v[180:187], v[100:103], v202, v202 op_sel_hi:[0,0,0]
	s_setprio 0
	v_mov_b32_e32 v0, v205
	s_barrier
	ds_read_b128 v[84:87], v208 offset:16384
	ds_read_b128 v[88:91], v208 offset:17408
	ds_read_b128 v[92:95], v208 offset:18432
	ds_read_b128 v[96:99], v208 offset:19456
	ds_read_b128 v[100:103], v208 offset:20480
	ds_read_b128 v[104:107], v208 offset:21504
	ds_read_b128 v[108:111], v208 offset:22528
	ds_read_b128 v[112:115], v208 offset:23552
	s_nop 0
	v_mov_b32_e32 v0, v206
	s_nop 0
	s_barrier
	s_waitcnt lgkmcnt(0)
	s_setprio 1
	s_waitcnt lgkmcnt(0)
	v_mfma_scale_f32_16x16x128_f8f6f4 v[80:83], v[52:59], v[84:91], v[80:83], v202, v202 op_sel_hi:[0,0,0]
	v_mfma_scale_f32_16x16x128_f8f6f4 v[76:79], v[68:75], v[84:91], v[76:79], v202, v202 op_sel_hi:[0,0,0]
	s_mov_b32 m0, s18
	v_mfma_scale_f32_16x16x128_f8f6f4 v[64:67], v[52:59], v[92:99], v[64:67], v202, v202 op_sel_hi:[0,0,0]
	global_load_lds_dwordx4 v205, s[10:11]
	v_mfma_scale_f32_16x16x128_f8f6f4 v[60:63], v[68:75], v[92:99], v[60:63], v202, v202 op_sel_hi:[0,0,0]
	v_mfma_scale_f32_16x16x128_f8f6f4 v[184:187], v[52:59], v[100:107], v[48:51], v202, v202 op_sel_hi:[0,0,0]
	s_mov_b32 m0, s19
	v_mfma_scale_f32_16x16x128_f8f6f4 v[214:217], v[68:75], v[100:107], v[44:47], v202, v202 op_sel_hi:[0,0,0]
	global_load_lds_dwordx4 v206, s[10:11]
	v_mfma_scale_f32_16x16x128_f8f6f4 v[218:221], v[52:59], v[108:115], v[40:43], v202, v202 op_sel_hi:[0,0,0]
	v_mfma_scale_f32_16x16x128_f8f6f4 v[222:225], v[68:75], v[108:115], v[36:39], v202, v202 op_sel_hi:[0,0,0]
	s_setprio 0
	s_barrier
	s_add_u32 s26, s6, 0x40000
	s_addc_u32 s27, s7, 0
	v_mov_b32_e32 v0, v205
	s_add_i32 s25, s30, s73
	s_mov_b32 s100, s25
	s_nop 0
	v_mov_b32_e32 v0, v206
	s_add_i32 s101, s25, 0x2000
	s_nop 0
	s_waitcnt vmcnt(4)
	s_barrier
	s_setprio 1
	v_mfma_scale_f32_16x16x128_f8f6f4 v[226:229], v[132:139], v[84:91], v[32:35], v202, v202 op_sel_hi:[0,0,0]
	v_mfma_scale_f32_16x16x128_f8f6f4 v[230:233], v[140:147], v[84:91], v[28:31], v202, v202 op_sel_hi:[0,0,0]
	s_mov_b32 m0, s100
	v_mfma_scale_f32_16x16x128_f8f6f4 v[234:237], v[132:139], v[92:99], v[24:27], v202, v202 op_sel_hi:[0,0,0]
	global_load_lds_dwordx4 v205, s[26:27]
	v_mfma_scale_f32_16x16x128_f8f6f4 v[238:241], v[140:147], v[92:99], v[20:23], v202, v202 op_sel_hi:[0,0,0]
	v_mfma_scale_f32_16x16x128_f8f6f4 v[242:245], v[132:139], v[100:107], v[16:19], v202, v202 op_sel_hi:[0,0,0]
	s_mov_b32 m0, s101
	v_mfma_scale_f32_16x16x128_f8f6f4 v[246:249], v[140:147], v[100:107], v[12:15], v202, v202 op_sel_hi:[0,0,0]
	global_load_lds_dwordx4 v206, s[26:27]
	v_mfma_scale_f32_16x16x128_f8f6f4 v[168:171], v[132:139], v[108:115], v[8:11], v202, v202 op_sel_hi:[0,0,0]
	v_mfma_scale_f32_16x16x128_f8f6f4 v[140:143], v[140:147], v[108:115], v[4:7], v202, v202 op_sel_hi:[0,0,0]
	s_setprio 0
	s_add_i32 s25, 0, 0x18000
	v_add_u32_e32 v0, s25, v207
	s_barrier
	s_nop 2
	ds_read_b128 v[2:5], v0
	ds_read_b128 v[6:9], v0 offset:1024
	ds_read_b128 v[10:13], v0 offset:2048
	ds_read_b128 v[14:17], v0 offset:3072
	s_add_u32 s26, s10, 0x40000
	v_mov_b32_e32 v0, v205
	ds_read_b128 v[18:21], v208 offset:32768
	ds_read_b128 v[22:25], v208 offset:33792
	ds_read_b128 v[26:29], v208 offset:34816
	ds_read_b128 v[30:33], v208 offset:35840
	ds_read_b128 v[34:37], v208 offset:36864
	ds_read_b128 v[38:41], v208 offset:37888
	ds_read_b128 v[42:45], v208 offset:38912
	ds_read_b128 v[46:49], v208 offset:39936
	s_addc_u32 s27, s11, 0
	s_nop 0
	v_mov_b32_e32 v0, v206
	s_nop 0
	s_waitcnt lgkmcnt(8)
	s_barrier
	s_waitcnt lgkmcnt(0)
	s_setprio 1
	s_waitcnt lgkmcnt(0)
	v_mfma_scale_f32_16x16x128_f8f6f4 v[164:167], v[2:9], v[18:25], v[164:167], v202, v202 op_sel_hi:[0,0,0]
	v_mfma_scale_f32_16x16x128_f8f6f4 v[160:163], v[10:17], v[18:25], v[160:163], v202, v202 op_sel_hi:[0,0,0]
	s_mov_b32 m0, s20
	v_mfma_scale_f32_16x16x128_f8f6f4 v[156:159], v[2:9], v[26:33], v[156:159], v202, v202 op_sel_hi:[0,0,0]
	global_load_lds_dwordx4 v205, s[26:27]
	v_mfma_scale_f32_16x16x128_f8f6f4 v[152:155], v[10:17], v[26:33], v[152:155], v202, v202 op_sel_hi:[0,0,0]
	v_mfma_scale_f32_16x16x128_f8f6f4 v[148:151], v[2:9], v[34:41], v[148:151], v202, v202 op_sel_hi:[0,0,0]
	s_mov_b32 m0, s21
	v_mfma_scale_f32_16x16x128_f8f6f4 v[144:147], v[10:17], v[34:41], v[188:191], v202, v202 op_sel_hi:[0,0,0]
	global_load_lds_dwordx4 v206, s[26:27]
	v_mfma_scale_f32_16x16x128_f8f6f4 v[136:139], v[2:9], v[42:49], v[192:195], v202, v202 op_sel_hi:[0,0,0]
	v_mfma_scale_f32_16x16x128_f8f6f4 v[132:135], v[10:17], v[42:49], v[196:199], v202, v202 op_sel_hi:[0,0,0]
	s_setprio 0
	s_barrier
	s_add_i32 s26, 0, 0x1c000
	v_add_u32_e32 v0, s26, v207
	ds_read_b128 v[52:55], v0
	ds_read_b128 v[56:59], v0 offset:1024
	ds_read_b128 v[68:71], v0 offset:2048
	ds_read_b128 v[72:75], v0 offset:3072
	v_mov_b32_e32 v0, v205
	s_add_i32 s25, s25, s73
	v_lshl_add_u64 v[50:51], s[6:7], 0, v[0:1]
	v_lshl_add_u64 v[50:51], v[50:51], 0, s[66:67]
	v_mov_b32_e32 v0, v206
	v_lshl_add_u64 v[50:51], s[6:7], 0, v[0:1]
	v_lshl_add_u64 v[50:51], v[50:51], 0, s[66:67]
	s_barrier
	s_waitcnt lgkmcnt(0)
	s_setprio 1
	s_waitcnt lgkmcnt(0)
	v_mfma_scale_f32_16x16x128_f8f6f4 v[128:131], v[52:59], v[18:25], v[128:131], v202, v202 op_sel_hi:[0,0,0]
	v_mfma_scale_f32_16x16x128_f8f6f4 v[124:127], v[68:75], v[18:25], v[124:127], v202, v202 op_sel_hi:[0,0,0]
	s_add_u32 s98, s6, s66
	s_addc_u32 s99, s7, s67
	s_mov_b32 m0, s25
	v_mfma_scale_f32_16x16x128_f8f6f4 v[120:123], v[52:59], v[26:33], v[120:123], v202, v202 op_sel_hi:[0,0,0]
	global_load_lds_dwordx4 v205, s[98:99]
	v_mfma_scale_f32_16x16x128_f8f6f4 v[116:119], v[68:75], v[26:33], v[116:119], v202, v202 op_sel_hi:[0,0,0]
	v_mfma_scale_f32_16x16x128_f8f6f4 v[112:115], v[52:59], v[34:41], v[210:213], v202, v202 op_sel_hi:[0,0,0]
	s_add_i32 m0, s25, 0x2000
	v_mfma_scale_f32_16x16x128_f8f6f4 v[108:111], v[68:75], v[34:41], v[172:175], v202, v202 op_sel_hi:[0,0,0]
	global_load_lds_dwordx4 v206, s[98:99]
	v_mfma_scale_f32_16x16x128_f8f6f4 v[104:107], v[52:59], v[42:49], v[176:179], v202, v202 op_sel_hi:[0,0,0]
	v_mfma_scale_f32_16x16x128_f8f6f4 v[100:103], v[68:75], v[42:49], v[180:183], v202, v202 op_sel_hi:[0,0,0]
	s_setprio 0
	v_mov_b32_e32 v0, v205
	s_barrier
	ds_read_b128 v[18:21], v208 offset:49152
	ds_read_b128 v[22:25], v208 offset:50176
	ds_read_b128 v[84:87], v208 offset:51200
	ds_read_b128 v[88:91], v208 offset:52224
	ds_read_b128 v[92:95], v208 offset:53248
	ds_read_b128 v[96:99], v208 offset:54272
	ds_read_b128 v[172:175], v208 offset:55296
	ds_read_b128 v[176:179], v208 offset:56320
	v_lshl_add_u64 v[26:27], s[10:11], 0, v[0:1]
	v_lshl_add_u64 v[26:27], v[26:27], 0, s[66:67]
	v_mov_b32_e32 v0, v206
	v_lshl_add_u64 v[26:27], s[10:11], 0, v[0:1]
	v_lshl_add_u64 v[26:27], v[26:27], 0, s[66:67]
	s_barrier
	s_waitcnt lgkmcnt(0)
	s_setprio 1
	s_waitcnt lgkmcnt(0)
	v_mfma_scale_f32_16x16x128_f8f6f4 v[80:83], v[2:9], v[18:25], v[80:83], v202, v202 op_sel_hi:[0,0,0]
	v_mfma_scale_f32_16x16x128_f8f6f4 v[76:79], v[10:17], v[18:25], v[76:79], v202, v202 op_sel_hi:[0,0,0]
	s_add_u32 s98, s10, s66
	s_addc_u32 s99, s11, s67
	s_mov_b32 m0, s22
	v_mfma_scale_f32_16x16x128_f8f6f4 v[64:67], v[2:9], v[84:91], v[64:67], v202, v202 op_sel_hi:[0,0,0]
	global_load_lds_dwordx4 v205, s[98:99]
	v_mfma_scale_f32_16x16x128_f8f6f4 v[60:63], v[10:17], v[84:91], v[60:63], v202, v202 op_sel_hi:[0,0,0]
	v_mfma_scale_f32_16x16x128_f8f6f4 v[48:51], v[2:9], v[92:99], v[184:187], v202, v202 op_sel_hi:[0,0,0]
	s_mov_b32 m0, s34
	v_mfma_scale_f32_16x16x128_f8f6f4 v[44:47], v[10:17], v[92:99], v[214:217], v202, v202 op_sel_hi:[0,0,0]
	global_load_lds_dwordx4 v206, s[98:99]
	v_mfma_scale_f32_16x16x128_f8f6f4 v[40:43], v[2:9], v[172:179], v[218:221], v202, v202 op_sel_hi:[0,0,0]
	v_mfma_scale_f32_16x16x128_f8f6f4 v[36:39], v[10:17], v[172:179], v[222:225], v202, v202 op_sel_hi:[0,0,0]
	s_setprio 0
	s_barrier
	s_add_u32 s6, s6, 0x40080
	s_addc_u32 s7, s7, 0
	v_mov_b32_e32 v0, v205
	s_add_i32 s10, s26, s73
	s_nop 0
	v_mov_b32_e32 v0, v206
	s_nop 0
	s_waitcnt vmcnt(4)
	s_barrier
	s_setprio 1
	v_mfma_scale_f32_16x16x128_f8f6f4 v[32:35], v[52:59], v[18:25], v[226:229], v202, v202 op_sel_hi:[0,0,0]
	v_mfma_scale_f32_16x16x128_f8f6f4 v[28:31], v[68:75], v[18:25], v[230:233], v202, v202 op_sel_hi:[0,0,0]
	s_mov_b32 m0, s10
	v_mfma_scale_f32_16x16x128_f8f6f4 v[24:27], v[52:59], v[84:91], v[234:237], v202, v202 op_sel_hi:[0,0,0]
	global_load_lds_dwordx4 v205, s[6:7]
	v_mfma_scale_f32_16x16x128_f8f6f4 v[20:23], v[68:75], v[84:91], v[238:241], v202, v202 op_sel_hi:[0,0,0]
	v_mfma_scale_f32_16x16x128_f8f6f4 v[16:19], v[52:59], v[92:99], v[242:245], v202, v202 op_sel_hi:[0,0,0]
	s_add_i32 m0, s10, 0x2000
	v_mfma_scale_f32_16x16x128_f8f6f4 v[12:15], v[68:75], v[92:99], v[246:249], v202, v202 op_sel_hi:[0,0,0]
	global_load_lds_dwordx4 v206, s[6:7]
	v_mfma_scale_f32_16x16x128_f8f6f4 v[8:11], v[52:59], v[172:179], v[168:171], v202, v202 op_sel_hi:[0,0,0]
	v_mfma_scale_f32_16x16x128_f8f6f4 v[4:7], v[68:75], v[172:179], v[140:143], v202, v202 op_sel_hi:[0,0,0]
	s_setprio 0
	s_add_i32 s17, s17, 2
	s_add_u32 s4, s4, 0x100
	s_addc_u32 s5, s5, 0
	s_add_u32 s15, s15, 0x100
	s_addc_u32 s16, s16, 0
	s_cmp_gt_u32 s17, 13
	s_barrier
	s_cbranch_scc0 .LBB0_278
	s_ashr_i32 s3, s8, 2
	s_mul_hi_i32 s4, s3, 0x55555556
	s_lshr_b32 s5, s4, 31
	s_add_i32 s4, s4, s5
	s_mul_i32 s4, s4, 3
	s_sub_i32 s15, s3, s4
	s_add_i32 s3, s8, 11
	s_cmp_lt_u32 s3, 23
	s_cselect_b64 s[12:13], -1, 0
	s_cmp_lt_i32 s15, 2
	v_readlane_b32 s6, v252, 53
	s_cselect_b64 s[4:5], -1, 0
	v_readlane_b32 s7, v252, 54
	s_and_b64 s[4:5], s[6:7], s[4:5]
	v_mbcnt_lo_u32_b32 v211, -1, 0
	v_mbcnt_hi_u32_b32 v211, -1, v211
	s_and_b64 s[6:7], s[12:13], s[4:5]
	v_ashrrev_i32_e32 v210, 4, v211
	s_lshl_b32 s3, s74, 8
	v_lshlrev_b32_e32 v172, 2, v210
	v_mov_b32_e32 v140, 0
	v_cndmask_b32_e64 v0, 0, 1, s[6:7]
	v_and_b32_e32 v209, 15, v211
	s_add_i32 s46, s3, s28
	v_ashrrev_i32_e32 v173, 31, v172
	v_cmp_ne_u32_e64 s[10:11], 1, v0
	s_andn2_b64 vcc, exec, s[6:7]
	v_mov_b32_e32 v141, v140
	v_mov_b32_e32 v142, v140
	v_mov_b32_e32 v143, v140
	v_mov_b32_e32 v92, v140
	v_mov_b32_e32 v93, v140
	v_mov_b32_e32 v94, v140
	v_mov_b32_e32 v95, v140
	v_mov_b32_e32 v88, v140
	v_mov_b32_e32 v89, v140
	v_mov_b32_e32 v90, v140
	v_mov_b32_e32 v91, v140
	v_mov_b32_e32 v72, v140
	v_mov_b32_e32 v73, v140
	v_mov_b32_e32 v74, v140
	v_mov_b32_e32 v75, v140
	v_mov_b32_e32 v56, v140
	v_mov_b32_e32 v57, v140
	v_mov_b32_e32 v58, v140
	v_mov_b32_e32 v59, v140
	s_cbranch_vccnz .LBB0_281
	s_and_b32 s3, s46, 0xfc0
	v_readlane_b32 s4, v252, 31
	v_or_b32_e32 v0, s3, v209
	v_readlane_b32 s5, v252, 32
	v_lshlrev_b32_e32 v0, 7, v0
	s_movk_i32 s3, 0x1000
	v_lshl_add_u64 v[2:3], v[172:173], 2, s[4:5]
	v_lshl_add_u64 v[2:3], v[2:3], 0, v[0:1]
	global_load_dwordx4 v[92:95], v[2:3], off
	global_load_dwordx4 v[96:99], v[2:3], off offset:64
	v_add_co_u32_e32 v52, vcc, s3, v2
	s_nop 1
	v_addc_co_u32_e32 v53, vcc, 0, v3, vcc
	global_load_dwordx4 v[140:143], v[52:53], off offset:2048
	global_load_dwordx4 v[88:91], v[2:3], off offset:2048
	global_load_dwordx4 v[84:87], v[2:3], off offset:2112
	global_load_dwordx4 v[72:75], v[52:53], off
	global_load_dwordx4 v[68:71], v[52:53], off offset:64
	s_nop 0
	global_load_dwordx4 v[52:55], v[52:53], off offset:2112
	s_waitcnt vmcnt(0)
	v_mov_b32_e32 v56, v140
	v_mov_b32_e32 v57, v141
	v_mov_b32_e32 v58, v142
	v_mov_b32_e32 v59, v143

.LBB0_1503:
	s_add_u32 s24, s2, 0xfffc0080
	s_addc_u32 s25, s3, -1
	s_add_i32 s28, 0, 0x10000
	v_add_u32_e32 v128, s28, v150
	ds_read_b128 v[136:139], v128
	ds_read_b128 v[140:143], v128 offset:1024
	ds_read_b128 v[152:155], v128 offset:2048
	ds_read_b128 v[156:159], v128 offset:3072
	s_cmp_eq_u32 s22, 12
	s_cselect_b32 s41, s49, s25
	s_cselect_b32 s40, s48, s24
	s_cselect_b32 s39, s59, s20
	s_cselect_b32 s38, s58, s7
	v_mov_b32_e32 v128, v148
	ds_read_b128 v[160:163], v151
	ds_read_b128 v[164:167], v151 offset:1024
	ds_read_b128 v[168:171], v151 offset:2048
	ds_read_b128 v[172:175], v151 offset:3072
	ds_read_b128 v[176:179], v151 offset:4096
	ds_read_b128 v[180:183], v151 offset:5120
	ds_read_b128 v[184:187], v151 offset:6144
	ds_read_b128 v[188:191], v151 offset:7168
	s_nop 0
	v_mov_b32_e32 v128, v149
	s_nop 0
	s_waitcnt lgkmcnt(8)
	s_barrier
	s_waitcnt lgkmcnt(0)
	s_setprio 1
	s_waitcnt lgkmcnt(0)
	v_mfma_scale_f32_16x16x128_f8f6f4 v[124:127], v[136:143], v[160:167], v[124:127], v146, v146 op_sel_hi:[0,0,0]
	v_mfma_scale_f32_16x16x128_f8f6f4 v[120:123], v[152:159], v[160:167], v[120:123], v146, v146 op_sel_hi:[0,0,0]
	s_add_i32 m0, s0, 0xc000
	v_mfma_scale_f32_16x16x128_f8f6f4 v[116:119], v[136:143], v[168:175], v[116:119], v146, v146 op_sel_hi:[0,0,0]
	global_load_lds_dwordx4 v148, s[2:3]
	v_mfma_scale_f32_16x16x128_f8f6f4 v[112:115], v[152:159], v[168:175], v[112:115], v146, v146 op_sel_hi:[0,0,0]
	v_mfma_scale_f32_16x16x128_f8f6f4 v[128:131], v[136:143], v[176:183], v[108:111], v146, v146 op_sel_hi:[0,0,0]
	s_add_i32 m0, s0, 0xe000
	v_mfma_scale_f32_16x16x128_f8f6f4 v[192:195], v[152:159], v[176:183], v[104:107], v146, v146 op_sel_hi:[0,0,0]
	global_load_lds_dwordx4 v149, s[2:3]
	v_mfma_scale_f32_16x16x128_f8f6f4 v[196:199], v[136:143], v[184:191], v[100:103], v146, v146 op_sel_hi:[0,0,0]
	v_mfma_scale_f32_16x16x128_f8f6f4 v[200:203], v[152:159], v[184:191], v[96:99], v146, v146 op_sel_hi:[0,0,0]
	s_setprio 0
	s_barrier
	s_add_i32 s29, 0, 0x14000
	s_nop 0
	v_add_u32_e32 v108, s29, v150
	v_mov_b32_e32 v132, v148
	s_add_i32 s24, s28, s21
	ds_read_b128 v[96:99], v108
	ds_read_b128 v[100:103], v108 offset:1024
	ds_read_b128 v[104:107], v108 offset:2048
	ds_read_b128 v[108:111], v108 offset:3072
	s_nop 0
	v_mov_b32_e32 v132, v149
	s_nop 0
	s_barrier
	s_waitcnt lgkmcnt(0)
	s_setprio 1
	s_waitcnt lgkmcnt(0)
	v_mfma_scale_f32_16x16x128_f8f6f4 v[204:207], v[96:103], v[160:167], v[60:63], v146, v146 op_sel_hi:[0,0,0]
	v_mfma_scale_f32_16x16x128_f8f6f4 v[160:163], v[104:111], v[160:167], v[56:59], v146, v146 op_sel_hi:[0,0,0]
	s_mov_b32 m0, s24
	v_mfma_scale_f32_16x16x128_f8f6f4 v[164:167], v[96:103], v[168:175], v[52:55], v146, v146 op_sel_hi:[0,0,0]
	global_load_lds_dwordx4 v148, s[38:39]
	v_mfma_scale_f32_16x16x128_f8f6f4 v[168:171], v[104:111], v[168:175], v[48:51], v146, v146 op_sel_hi:[0,0,0]
	v_mfma_scale_f32_16x16x128_f8f6f4 v[172:175], v[96:103], v[176:183], v[44:47], v146, v146 op_sel_hi:[0,0,0]
	s_add_i32 m0, s24, 0x2000
	v_mfma_scale_f32_16x16x128_f8f6f4 v[176:179], v[104:111], v[176:183], v[40:43], v146, v146 op_sel_hi:[0,0,0]
	global_load_lds_dwordx4 v149, s[38:39]
	v_mfma_scale_f32_16x16x128_f8f6f4 v[180:183], v[96:103], v[184:191], v[36:39], v146, v146 op_sel_hi:[0,0,0]
	v_mfma_scale_f32_16x16x128_f8f6f4 v[184:187], v[104:111], v[184:191], v[32:35], v146, v146 op_sel_hi:[0,0,0]
	s_setprio 0
	v_mov_b32_e32 v132, v148
	s_barrier
	s_nop 2
	ds_read_b128 v[32:35], v151 offset:16384
	ds_read_b128 v[36:39], v151 offset:17408
	ds_read_b128 v[40:43], v151 offset:18432
	ds_read_b128 v[44:47], v151 offset:19456
	ds_read_b128 v[48:51], v151 offset:20480
	ds_read_b128 v[52:55], v151 offset:21504
	ds_read_b128 v[56:59], v151 offset:22528
	ds_read_b128 v[60:63], v151 offset:23552
	s_nop 0
	v_mov_b32_e32 v132, v149
	s_nop 0
	s_barrier
	s_waitcnt lgkmcnt(0)
	s_setprio 1
	s_waitcnt lgkmcnt(0)
	v_mfma_scale_f32_16x16x128_f8f6f4 v[92:95], v[136:143], v[32:39], v[92:95], v146, v146 op_sel_hi:[0,0,0]
	v_mfma_scale_f32_16x16x128_f8f6f4 v[88:91], v[152:159], v[32:39], v[88:91], v146, v146 op_sel_hi:[0,0,0]
	s_mov_b32 m0, s0
	v_mfma_scale_f32_16x16x128_f8f6f4 v[84:87], v[136:143], v[40:47], v[84:87], v146, v146 op_sel_hi:[0,0,0]
	global_load_lds_dwordx4 v148, s[40:41]
	v_mfma_scale_f32_16x16x128_f8f6f4 v[80:83], v[152:159], v[40:47], v[80:83], v146, v146 op_sel_hi:[0,0,0]
	v_mfma_scale_f32_16x16x128_f8f6f4 v[76:79], v[136:143], v[48:55], v[76:79], v146, v146 op_sel_hi:[0,0,0]
	s_mov_b32 m0, s1
	v_mfma_scale_f32_16x16x128_f8f6f4 v[72:75], v[152:159], v[48:55], v[72:75], v146, v146 op_sel_hi:[0,0,0]
	global_load_lds_dwordx4 v149, s[40:41]
	v_mfma_scale_f32_16x16x128_f8f6f4 v[188:191], v[136:143], v[56:63], v[68:71], v146, v146 op_sel_hi:[0,0,0]
	v_mfma_scale_f32_16x16x128_f8f6f4 v[208:211], v[152:159], v[56:63], v[64:67], v146, v146 op_sel_hi:[0,0,0]
	s_setprio 0
	s_barrier
	s_add_u32 s24, s38, 0x40000
	s_addc_u32 s25, s39, 0
	s_nop 2
	v_mov_b32_e32 v64, v148
	s_add_i32 s28, s29, s21
	s_mov_b32 s100, s28
	s_nop 0
	v_mov_b32_e32 v64, v149
	s_add_i32 s101, s28, 0x2000
	s_nop 0
	s_waitcnt vmcnt(4)
	s_barrier
	s_setprio 1
	v_mfma_scale_f32_16x16x128_f8f6f4 v[212:215], v[96:103], v[32:39], v[28:31], v146, v146 op_sel_hi:[0,0,0]
	v_mfma_scale_f32_16x16x128_f8f6f4 v[216:219], v[104:111], v[32:39], v[24:27], v146, v146 op_sel_hi:[0,0,0]
	s_mov_b32 m0, s100
	v_mfma_scale_f32_16x16x128_f8f6f4 v[220:223], v[96:103], v[40:47], v[20:23], v146, v146 op_sel_hi:[0,0,0]
	global_load_lds_dwordx4 v148, s[24:25]
	v_mfma_scale_f32_16x16x128_f8f6f4 v[224:227], v[104:111], v[40:47], v[16:19], v146, v146 op_sel_hi:[0,0,0]
	v_mfma_scale_f32_16x16x128_f8f6f4 v[228:231], v[96:103], v[48:55], v[12:15], v146, v146 op_sel_hi:[0,0,0]
	s_mov_b32 m0, s101
	v_mfma_scale_f32_16x16x128_f8f6f4 v[232:235], v[104:111], v[48:55], v[8:11], v146, v146 op_sel_hi:[0,0,0]
	global_load_lds_dwordx4 v149, s[24:25]
	v_mfma_scale_f32_16x16x128_f8f6f4 v[236:239], v[96:103], v[56:63], v[4:7], v146, v146 op_sel_hi:[0,0,0]
	v_mfma_scale_f32_16x16x128_f8f6f4 v[240:243], v[104:111], v[56:63], v[0:3], v146, v146 op_sel_hi:[0,0,0]
	s_setprio 0
	s_add_i32 s28, 0, 0x18000
	s_nop 1
	v_add_u32_e32 v12, s28, v150
	s_barrier
	s_nop 0
	ds_read_b128 v[0:3], v12
	ds_read_b128 v[4:7], v12 offset:1024
	ds_read_b128 v[8:11], v12 offset:2048
	ds_read_b128 v[12:15], v12 offset:3072
	s_add_u32 s24, s40, 0x40000
	v_mov_b32_e32 v40, v148
	ds_read_b128 v[16:19], v151 offset:32768
	ds_read_b128 v[20:23], v151 offset:33792
	ds_read_b128 v[24:27], v151 offset:34816
	ds_read_b128 v[28:31], v151 offset:35840
	ds_read_b128 v[32:35], v151 offset:36864
	ds_read_b128 v[36:39], v151 offset:37888
	ds_read_b128 v[64:67], v151 offset:38912
	ds_read_b128 v[68:71], v151 offset:39936
	s_addc_u32 s25, s41, 0
	s_nop 0
	v_mov_b32_e32 v40, v149
	s_nop 0
	s_waitcnt lgkmcnt(8)
	s_barrier
	s_waitcnt lgkmcnt(0)
	s_setprio 1
	s_waitcnt lgkmcnt(0)
	v_mfma_scale_f32_16x16x128_f8f6f4 v[124:127], v[0:7], v[16:23], v[124:127], v146, v146 op_sel_hi:[0,0,0]
	v_mfma_scale_f32_16x16x128_f8f6f4 v[120:123], v[8:15], v[16:23], v[120:123], v146, v146 op_sel_hi:[0,0,0]
	s_mov_b32 m0, s8
	v_mfma_scale_f32_16x16x128_f8f6f4 v[116:119], v[0:7], v[24:31], v[116:119], v146, v146 op_sel_hi:[0,0,0]
	global_load_lds_dwordx4 v148, s[24:25]
	v_mfma_scale_f32_16x16x128_f8f6f4 v[112:115], v[8:15], v[24:31], v[112:115], v146, v146 op_sel_hi:[0,0,0]
	v_mfma_scale_f32_16x16x128_f8f6f4 v[108:111], v[0:7], v[32:39], v[128:131], v146, v146 op_sel_hi:[0,0,0]
	s_mov_b32 m0, s9
	v_mfma_scale_f32_16x16x128_f8f6f4 v[104:107], v[8:15], v[32:39], v[192:195], v146, v146 op_sel_hi:[0,0,0]
	global_load_lds_dwordx4 v149, s[24:25]
	v_mfma_scale_f32_16x16x128_f8f6f4 v[100:103], v[0:7], v[64:71], v[196:199], v146, v146 op_sel_hi:[0,0,0]
	v_mfma_scale_f32_16x16x128_f8f6f4 v[96:99], v[8:15], v[64:71], v[200:203], v146, v146 op_sel_hi:[0,0,0]
	s_setprio 0
	s_barrier
	s_add_i32 s29, 0, 0x1c000
	v_add_u32_e32 v40, s29, v150
	v_mov_b32_e32 v132, v148
	ds_read_b128 v[136:139], v40
	ds_read_b128 v[140:143], v40 offset:1024
	ds_read_b128 v[152:155], v40 offset:2048
	ds_read_b128 v[156:159], v40 offset:3072
	s_add_i32 s24, s28, s21
	v_lshl_add_u64 v[40:41], s[38:39], 0, v[132:133]
	v_lshl_add_u64 v[40:41], v[40:41], 0, s[52:53]
	v_mov_b32_e32 v132, v149
	v_lshl_add_u64 v[40:41], s[38:39], 0, v[132:133]
	v_lshl_add_u64 v[40:41], v[40:41], 0, s[52:53]
	s_barrier
	s_waitcnt lgkmcnt(0)
	s_setprio 1
	s_waitcnt lgkmcnt(0)
	v_mfma_scale_f32_16x16x128_f8f6f4 v[60:63], v[136:143], v[16:23], v[204:207], v146, v146 op_sel_hi:[0,0,0]
	v_mfma_scale_f32_16x16x128_f8f6f4 v[56:59], v[152:159], v[16:23], v[160:163], v146, v146 op_sel_hi:[0,0,0]
	s_add_u32 s98, s38, s52
	s_addc_u32 s99, s39, s53
	s_mov_b32 m0, s24
	v_mfma_scale_f32_16x16x128_f8f6f4 v[52:55], v[136:143], v[24:31], v[164:167], v146, v146 op_sel_hi:[0,0,0]
	global_load_lds_dwordx4 v148, s[98:99]
	v_mfma_scale_f32_16x16x128_f8f6f4 v[48:51], v[152:159], v[24:31], v[168:171], v146, v146 op_sel_hi:[0,0,0]
	v_mfma_scale_f32_16x16x128_f8f6f4 v[44:47], v[136:143], v[32:39], v[172:175], v146, v146 op_sel_hi:[0,0,0]
	s_add_i32 m0, s24, 0x2000
	v_mfma_scale_f32_16x16x128_f8f6f4 v[40:43], v[152:159], v[32:39], v[176:179], v146, v146 op_sel_hi:[0,0,0]
	global_load_lds_dwordx4 v149, s[98:99]
	v_mfma_scale_f32_16x16x128_f8f6f4 v[36:39], v[136:143], v[64:71], v[180:183], v146, v146 op_sel_hi:[0,0,0]
	v_mfma_scale_f32_16x16x128_f8f6f4 v[32:35], v[152:159], v[64:71], v[184:187], v146, v146 op_sel_hi:[0,0,0]
	s_setprio 0
	v_mov_b32_e32 v132, v148
	s_barrier
	ds_read_b128 v[16:19], v151 offset:49152
	ds_read_b128 v[20:23], v151 offset:50176
	ds_read_b128 v[160:163], v151 offset:51200
	ds_read_b128 v[164:167], v151 offset:52224
	ds_read_b128 v[168:171], v151 offset:53248
	ds_read_b128 v[172:175], v151 offset:54272
	ds_read_b128 v[176:179], v151 offset:55296
	ds_read_b128 v[180:183], v151 offset:56320
	v_lshl_add_u64 v[24:25], s[40:41], 0, v[132:133]
	v_lshl_add_u64 v[24:25], v[24:25], 0, s[52:53]
	v_mov_b32_e32 v132, v149
	v_lshl_add_u64 v[24:25], s[40:41], 0, v[132:133]
	v_lshl_add_u64 v[24:25], v[24:25], 0, s[52:53]
	s_barrier
	s_waitcnt lgkmcnt(0)
	s_setprio 1
	s_waitcnt lgkmcnt(0)
	v_mfma_scale_f32_16x16x128_f8f6f4 v[92:95], v[0:7], v[16:23], v[92:95], v146, v146 op_sel_hi:[0,0,0]
	v_mfma_scale_f32_16x16x128_f8f6f4 v[88:91], v[8:15], v[16:23], v[88:91], v146, v146 op_sel_hi:[0,0,0]
	s_add_u32 s98, s40, s52
	s_addc_u32 s99, s41, s53
	s_mov_b32 m0, s10
	v_mfma_scale_f32_16x16x128_f8f6f4 v[84:87], v[0:7], v[160:167], v[84:87], v146, v146 op_sel_hi:[0,0,0]
	global_load_lds_dwordx4 v148, s[98:99]
	v_mfma_scale_f32_16x16x128_f8f6f4 v[80:83], v[8:15], v[160:167], v[80:83], v146, v146 op_sel_hi:[0,0,0]
	v_mfma_scale_f32_16x16x128_f8f6f4 v[76:79], v[0:7], v[168:175], v[76:79], v146, v146 op_sel_hi:[0,0,0]
	s_mov_b32 m0, s11
	v_mfma_scale_f32_16x16x128_f8f6f4 v[72:75], v[8:15], v[168:175], v[72:75], v146, v146 op_sel_hi:[0,0,0]
	global_load_lds_dwordx4 v149, s[98:99]
	v_mfma_scale_f32_16x16x128_f8f6f4 v[68:71], v[0:7], v[176:183], v[188:191], v146, v146 op_sel_hi:[0,0,0]
	v_mfma_scale_f32_16x16x128_f8f6f4 v[64:67], v[8:15], v[176:183], v[208:211], v146, v146 op_sel_hi:[0,0,0]
	s_setprio 0
	s_barrier
	s_add_u32 s24, s38, 0x40080
	s_addc_u32 s25, s39, 0
	v_mov_b32_e32 v0, v148
	s_add_i32 s28, s29, s21
	s_nop 0
	v_mov_b32_e32 v0, v149
	s_nop 0
	s_waitcnt vmcnt(4)
	s_barrier
	s_setprio 1
	v_mfma_scale_f32_16x16x128_f8f6f4 v[28:31], v[136:143], v[16:23], v[212:215], v146, v146 op_sel_hi:[0,0,0]
	v_mfma_scale_f32_16x16x128_f8f6f4 v[24:27], v[152:159], v[16:23], v[216:219], v146, v146 op_sel_hi:[0,0,0]
	s_mov_b32 m0, s28
	v_mfma_scale_f32_16x16x128_f8f6f4 v[20:23], v[136:143], v[160:167], v[220:223], v146, v146 op_sel_hi:[0,0,0]
	global_load_lds_dwordx4 v148, s[24:25]
	v_mfma_scale_f32_16x16x128_f8f6f4 v[16:19], v[152:159], v[160:167], v[224:227], v146, v146 op_sel_hi:[0,0,0]
	v_mfma_scale_f32_16x16x128_f8f6f4 v[12:15], v[136:143], v[168:175], v[228:231], v146, v146 op_sel_hi:[0,0,0]
	s_add_i32 m0, s28, 0x2000
	v_mfma_scale_f32_16x16x128_f8f6f4 v[8:11], v[152:159], v[168:175], v[232:235], v146, v146 op_sel_hi:[0,0,0]
	global_load_lds_dwordx4 v149, s[24:25]
	v_mfma_scale_f32_16x16x128_f8f6f4 v[4:7], v[136:143], v[176:183], v[236:239], v146, v146 op_sel_hi:[0,0,0]
	v_mfma_scale_f32_16x16x128_f8f6f4 v[0:3], v[152:159], v[176:183], v[240:243], v146, v146 op_sel_hi:[0,0,0]
	s_setprio 0
	s_add_i32 s22, s22, 2
	s_add_u32 s2, s2, 0x100
	s_addc_u32 s3, s3, 0
	s_add_u32 s7, s7, 0x100
	s_addc_u32 s20, s20, 0
	s_cmp_gt_u32 s22, 13
	s_barrier
	s_cbranch_scc0 .LBB0_1503
	s_ashr_i32 s2, s13, 4
	s_mul_hi_i32 s3, s2, 0xc000
	s_mul_i32 s2, s2, 0xc000
	s_add_u32 s7, s69, s2
	s_addc_u32 s20, s71, s3
	s_lshl_b32 s2, s15, 8
	s_ashr_i32 s3, s2, 31
	s_lshl_b64 s[24:25], s[2:3], 2
	s_add_u32 s7, s7, s24
	v_mbcnt_lo_u32_b32 v132, -1, 0
	v_mbcnt_hi_u32_b32 v132, -1, v132
	s_addc_u32 s15, s20, s25
	v_ashrrev_i32_e32 v136, 4, v132
	s_lshl_b32 s20, s23, 2
	s_add_u32 s24, s7, s20
	v_lshlrev_b32_e32 v128, 2, v136
	s_addc_u32 s25, s15, 0
	v_ashrrev_i32_e32 v129, 31, v128
	v_lshl_add_u64 v[130:131], v[128:129], 2, s[24:25]
	v_lshlrev_b32_e32 v128, 3, v136
	global_load_dwordx4 v[136:139], v[130:131], off
	global_load_dwordx4 v[152:155], v[130:131], off offset:64
	s_lshl_b32 s7, s13, 8
	s_add_i32 s24, s7, s16
	s_ashr_i32 s25, s24, 31
	s_lshl_b64 s[24:25], s[24:25], 11
	s_add_u32 s7, s61, s24
	s_addc_u32 s13, s65, s25
	s_add_u32 s2, s7, s2
	s_addc_u32 s3, s13, s3
	v_bfi_b32 v128, -16, v128, v132
	s_add_u32 s2, s2, s23
	v_ashrrev_i32_e32 v129, 31, v128
	s_addc_u32 s3, s3, 0
	v_lshlrev_b64 v[128:129], 11, v[128:129]
	v_lshl_add_u64 v[128:129], s[2:3], 0, v[128:129]
	v_and_b32_e32 v132, 16, v132
	v_lshl_add_u64 v[128:129], v[128:129], 0, v[132:133]
	s_mov_b32 s2, 0x10000
	s_mov_b32 s13, s36
	s_mov_b32 s15, s6
	s_mov_b64 s[34:35], s[58:59]
	s_waitcnt vmcnt(0)
	v_pk_mul_f32 v[140:141], v[138:139], s[54:55] op_sel_hi:[1,0]
	v_pk_mul_f32 v[138:139], v[136:137], s[54:55] op_sel_hi:[1,0]
	v_pk_mul_f32 v[136:137], v[152:153], s[54:55] op_sel_hi:[1,0]
	v_pk_mul_f32 v[152:153], v[124:125], v[138:139]
	v_mov_b32_e32 v124, v133
	v_cvt_pk_fp8_f32 v124, v152, v153
	v_pk_mul_f32 v[126:127], v[126:127], v[140:141]
	v_pk_mul_f32 v[112:113], v[112:113], v[136:137]
	v_pk_mul_f32 v[110:111], v[110:111], v[140:141]
	v_cvt_pk_fp8_f32 v124, v126, v127 op_sel:[0,0,1]
	v_mov_b32_e32 v127, v133
	v_cvt_pk_fp8_f32 v127, v112, v113
	v_pk_mul_f32 v[112:113], v[108:109], v[138:139]
	v_mov_b32_e32 v108, v133
	v_cvt_pk_fp8_f32 v108, v112, v113
	v_pk_mul_f32 v[96:97], v[96:97], v[136:137]
	v_pk_mul_f32 v[142:143], v[154:155], s[54:55] op_sel_hi:[1,0]
	v_pk_mul_f32 v[94:95], v[94:95], v[140:141]
	v_cvt_pk_fp8_f32 v108, v110, v111 op_sel:[0,0,1]
	v_mov_b32_e32 v111, v133
	v_cvt_pk_fp8_f32 v111, v96, v97
	v_pk_mul_f32 v[98:99], v[98:99], v[142:143]
	v_pk_mul_f32 v[80:81], v[80:81], v[136:137]
	v_pk_mul_f32 v[78:79], v[78:79], v[140:141]
	v_cvt_pk_fp8_f32 v111, v98, v99 op_sel:[0,0,1]
	v_pk_mul_f32 v[98:99], v[92:93], v[138:139]
	v_mov_b32_e32 v92, v133
	v_cvt_pk_fp8_f32 v92, v98, v99
	v_pk_mul_f32 v[120:121], v[120:121], v[136:137]
	v_mov_b32_e32 v125, v133
	v_pk_mul_f32 v[116:117], v[116:117], v[138:139]
	v_cvt_pk_fp8_f32 v92, v94, v95 op_sel:[0,0,1]
	v_mov_b32_e32 v95, v133
	v_cvt_pk_fp8_f32 v95, v80, v81
	v_pk_mul_f32 v[80:81], v[76:77], v[138:139]
	v_mov_b32_e32 v76, v133
	v_cvt_pk_fp8_f32 v76, v80, v81
	v_mov_b32_e32 v126, v133
	v_pk_mul_f32 v[104:105], v[104:105], v[136:137]
	v_mov_b32_e32 v109, v133
	v_pk_mul_f32 v[100:101], v[100:101], v[138:139]
	v_mov_b32_e32 v110, v133
	v_pk_mul_f32 v[88:89], v[88:89], v[136:137]
	v_mov_b32_e32 v93, v133
	v_pk_mul_f32 v[84:85], v[84:85], v[138:139]
	v_mov_b32_e32 v94, v133
	v_cvt_pk_fp8_f32 v76, v78, v79 op_sel:[0,0,1]
	v_pk_mul_f32 v[72:73], v[72:73], v[136:137]
	v_mov_b32_e32 v77, v133
	v_pk_mul_f32 v[68:69], v[68:69], v[138:139]
	v_mov_b32_e32 v78, v133
	v_pk_mul_f32 v[64:65], v[64:65], v[136:137]
	v_mov_b32_e32 v79, v133
	v_cvt_pk_fp8_f32 v125, v120, v121
	v_cvt_pk_fp8_f32 v126, v116, v117
	v_cvt_pk_fp8_f32 v109, v104, v105
	v_cvt_pk_fp8_f32 v110, v100, v101
	v_cvt_pk_fp8_f32 v93, v88, v89
	v_cvt_pk_fp8_f32 v94, v84, v85
	v_cvt_pk_fp8_f32 v77, v72, v73
	v_cvt_pk_fp8_f32 v78, v68, v69
	v_cvt_pk_fp8_f32 v79, v64, v65
	v_pk_mul_f32 v[122:123], v[122:123], v[142:143]
	v_pk_mul_f32 v[118:119], v[118:119], v[140:141]
	v_pk_mul_f32 v[114:115], v[114:115], v[142:143]
	v_pk_mul_f32 v[106:107], v[106:107], v[142:143]
	v_pk_mul_f32 v[102:103], v[102:103], v[140:141]
	v_pk_mul_f32 v[90:91], v[90:91], v[142:143]
	v_pk_mul_f32 v[86:87], v[86:87], v[140:141]
	v_pk_mul_f32 v[82:83], v[82:83], v[142:143]
	v_pk_mul_f32 v[74:75], v[74:75], v[142:143]
	v_pk_mul_f32 v[70:71], v[70:71], v[140:141]
	v_pk_mul_f32 v[66:67], v[66:67], v[142:143]
	v_cvt_pk_fp8_f32 v125, v122, v123 op_sel:[0,0,1]
	v_cvt_pk_fp8_f32 v126, v118, v119 op_sel:[0,0,1]
	v_cvt_pk_fp8_f32 v127, v114, v115 op_sel:[0,0,1]
	v_cvt_pk_fp8_f32 v109, v106, v107 op_sel:[0,0,1]
	v_cvt_pk_fp8_f32 v110, v102, v103 op_sel:[0,0,1]
	v_add_co_u32_e32 v96, vcc, s2, v128
	v_cvt_pk_fp8_f32 v93, v90, v91 op_sel:[0,0,1]
	v_cvt_pk_fp8_f32 v94, v86, v87 op_sel:[0,0,1]
	v_cvt_pk_fp8_f32 v95, v82, v83 op_sel:[0,0,1]
	v_cvt_pk_fp8_f32 v77, v74, v75 op_sel:[0,0,1]
	v_cvt_pk_fp8_f32 v78, v70, v71 op_sel:[0,0,1]
	v_cvt_pk_fp8_f32 v79, v66, v67 op_sel:[0,0,1]
	v_addc_co_u32_e32 v97, vcc, 0, v129, vcc
	s_mov_b32 s2, 0x40000
	v_add_co_u32_e32 v64, vcc, s2, v128
	s_mov_b32 s2, 0x50000
	s_nop 0
	v_addc_co_u32_e32 v65, vcc, 0, v129, vcc
	v_permlane32_swap_b32_e32 v124, v126
	v_permlane32_swap_b32_e32 v125, v127
	v_permlane32_swap_b32_e32 v108, v110
	v_permlane32_swap_b32_e32 v109, v111
	v_permlane32_swap_b32_e32 v92, v94
	v_permlane32_swap_b32_e32 v93, v95
	v_permlane32_swap_b32_e32 v76, v78
	v_permlane32_swap_b32_e32 v77, v79
	v_add_co_u32_e32 v66, vcc, s2, v128
	v_permlane16_swap_b32_e32 v124, v125
	v_permlane16_swap_b32_e32 v126, v127
	v_permlane16_swap_b32_e32 v108, v109
	v_permlane16_swap_b32_e32 v110, v111
	v_permlane16_swap_b32_e32 v92, v93
	v_permlane16_swap_b32_e32 v94, v95
	v_permlane16_swap_b32_e32 v76, v77
	v_permlane16_swap_b32_e32 v78, v79
	v_addc_co_u32_e32 v67, vcc, 0, v129, vcc
	global_store_dwordx4 v[128:129], v[124:127], off
	global_store_dwordx4 v[96:97], v[108:111], off
	global_store_dwordx4 v[64:65], v[92:95], off
	global_store_dwordx4 v[66:67], v[76:79], off
	global_load_dwordx4 v[68:71], v[130:131], off offset:512
	s_and_b64 vcc, exec, s[4:5]
	global_load_dwordx4 v[76:79], v[130:131], off offset:576
	s_mov_b64 s[2:3], s[48:49]
	s_waitcnt vmcnt(0)
	v_pk_mul_f32 v[72:73], v[70:71], s[54:55] op_sel_hi:[1,0]
	v_pk_mul_f32 v[70:71], v[68:69], s[54:55] op_sel_hi:[1,0]
	v_pk_mul_f32 v[68:69], v[76:77], s[54:55] op_sel_hi:[1,0]
	v_pk_mul_f32 v[76:77], v[60:61], v[70:71]
	v_mov_b32_e32 v60, v133
	v_cvt_pk_fp8_f32 v60, v76, v77
	v_pk_mul_f32 v[62:63], v[62:63], v[72:73]
	v_pk_mul_f32 v[48:49], v[48:49], v[68:69]
	v_pk_mul_f32 v[46:47], v[46:47], v[72:73]
	v_cvt_pk_fp8_f32 v60, v62, v63 op_sel:[0,0,1]
	v_mov_b32_e32 v63, v133
	v_cvt_pk_fp8_f32 v63, v48, v49
	v_pk_mul_f32 v[48:49], v[44:45], v[70:71]
	v_mov_b32_e32 v44, v133
	v_cvt_pk_fp8_f32 v44, v48, v49
	v_pk_mul_f32 v[32:33], v[32:33], v[68:69]
	v_pk_mul_f32 v[30:31], v[30:31], v[72:73]
	v_pk_mul_f32 v[16:17], v[16:17], v[68:69]
	v_cvt_pk_fp8_f32 v44, v46, v47 op_sel:[0,0,1]
	v_mov_b32_e32 v47, v133
	v_cvt_pk_fp8_f32 v47, v32, v33
	v_pk_mul_f32 v[32:33], v[28:29], v[70:71]
	v_mov_b32_e32 v28, v133
	v_cvt_pk_fp8_f32 v28, v32, v33
	v_pk_mul_f32 v[56:57], v[56:57], v[68:69]
	v_mov_b32_e32 v61, v133
	v_pk_mul_f32 v[52:53], v[52:53], v[70:71]
	v_cvt_pk_fp8_f32 v28, v30, v31 op_sel:[0,0,1]
	v_mov_b32_e32 v31, v133
	v_cvt_pk_fp8_f32 v31, v16, v17
	v_pk_mul_f32 v[16:17], v[12:13], v[70:71]
	v_mov_b32_e32 v12, v133
	v_cvt_pk_fp8_f32 v12, v16, v17
	v_mov_b32_e32 v62, v133
	v_pk_mul_f32 v[24:25], v[24:25], v[68:69]
	v_mov_b32_e32 v29, v133
	v_pk_mul_f32 v[20:21], v[20:21], v[70:71]
	v_mov_b32_e32 v30, v133
	v_pk_mul_f32 v[14:15], v[14:15], v[72:73]
	v_cvt_pk_fp8_f32 v61, v56, v57
	v_cvt_pk_fp8_f32 v62, v52, v53
	v_pk_mul_f32 v[40:41], v[40:41], v[68:69]
	v_mov_b32_e32 v45, v133
	v_pk_mul_f32 v[36:37], v[36:37], v[70:71]
	v_mov_b32_e32 v46, v133
	v_cvt_pk_fp8_f32 v29, v24, v25
	v_cvt_pk_fp8_f32 v30, v20, v21
	v_cvt_pk_fp8_f32 v12, v14, v15 op_sel:[0,0,1]
	v_pk_mul_f32 v[8:9], v[8:9], v[68:69]
	v_mov_b32_e32 v13, v133
	v_pk_mul_f32 v[4:5], v[4:5], v[70:71]
	v_mov_b32_e32 v14, v133
	v_pk_mul_f32 v[0:1], v[0:1], v[68:69]
	v_mov_b32_e32 v15, v133
	v_cvt_pk_fp8_f32 v45, v40, v41
	v_cvt_pk_fp8_f32 v46, v36, v37
	v_cvt_pk_fp8_f32 v13, v8, v9
	v_cvt_pk_fp8_f32 v14, v4, v5
	v_cvt_pk_fp8_f32 v15, v0, v1
	v_pk_mul_f32 v[74:75], v[78:79], s[54:55] op_sel_hi:[1,0]
	v_pk_mul_f32 v[54:55], v[54:55], v[72:73]
	v_pk_mul_f32 v[58:59], v[58:59], v[74:75]
	v_pk_mul_f32 v[50:51], v[50:51], v[74:75]
	v_pk_mul_f32 v[26:27], v[26:27], v[74:75]
	v_pk_mul_f32 v[22:23], v[22:23], v[72:73]
	v_pk_mul_f32 v[18:19], v[18:19], v[74:75]
	v_cvt_pk_fp8_f32 v61, v58, v59 op_sel:[0,0,1]
	v_cvt_pk_fp8_f32 v62, v54, v55 op_sel:[0,0,1]
	v_cvt_pk_fp8_f32 v63, v50, v51 op_sel:[0,0,1]
	v_pk_mul_f32 v[42:43], v[42:43], v[74:75]
	v_pk_mul_f32 v[38:39], v[38:39], v[72:73]
	v_pk_mul_f32 v[34:35], v[34:35], v[74:75]
	v_cvt_pk_fp8_f32 v29, v26, v27 op_sel:[0,0,1]
	v_cvt_pk_fp8_f32 v30, v22, v23 op_sel:[0,0,1]
	v_cvt_pk_fp8_f32 v31, v18, v19 op_sel:[0,0,1]
	v_pk_mul_f32 v[10:11], v[10:11], v[74:75]
	v_pk_mul_f32 v[6:7], v[6:7], v[72:73]
	v_pk_mul_f32 v[2:3], v[2:3], v[74:75]
	v_cvt_pk_fp8_f32 v45, v42, v43 op_sel:[0,0,1]
	v_cvt_pk_fp8_f32 v46, v38, v39 op_sel:[0,0,1]
	v_cvt_pk_fp8_f32 v47, v34, v35 op_sel:[0,0,1]
	v_cvt_pk_fp8_f32 v13, v10, v11 op_sel:[0,0,1]
	v_cvt_pk_fp8_f32 v14, v6, v7 op_sel:[0,0,1]
	v_cvt_pk_fp8_f32 v15, v2, v3 op_sel:[0,0,1]
	v_permlane32_swap_b32_e32 v60, v62
	v_permlane32_swap_b32_e32 v61, v63
	v_permlane32_swap_b32_e32 v28, v30
	v_permlane32_swap_b32_e32 v29, v31
	v_permlane16_swap_b32_e32 v60, v61
	v_permlane16_swap_b32_e32 v62, v63
	v_permlane32_swap_b32_e32 v44, v46
	v_permlane32_swap_b32_e32 v45, v47
	v_permlane16_swap_b32_e32 v28, v29
	v_permlane16_swap_b32_e32 v30, v31
	v_permlane32_swap_b32_e32 v12, v14
	v_permlane32_swap_b32_e32 v13, v15
	v_permlane16_swap_b32_e32 v44, v45
	v_permlane16_swap_b32_e32 v46, v47
	global_store_dwordx4 v[128:129], v[60:63], off offset:128
	global_store_dwordx4 v[96:97], v[44:47], off offset:128
	v_permlane16_swap_b32_e32 v12, v13
	v_permlane16_swap_b32_e32 v14, v15
	global_store_dwordx4 v[64:65], v[28:31], off offset:128
	global_store_dwordx4 v[66:67], v[12:15], off offset:128
	s_cbranch_vccz .LBB0_1496
	v_readlane_b32 s0, v252, 18
	s_waitcnt vmcnt(0)
	v_readlane_b32 s1, v252, 19
	s_andn2_b64 vcc, exec, s[0:1]
	s_cbranch_vccnz .LBB0_1227
	s_barrier
	s_branch .LBB0_1227

.LBB0_2382:
	ds_read_b128 v[140:143], v134
	ds_read_b128 v[144:147], v134 offset:1024
	ds_read_b128 v[148:151], v134 offset:2048
	ds_read_b128 v[152:155], v134 offset:3072
	s_add_u32 s18, s16, 0xfffd0080
	s_addc_u32 s19, s17, -1
	s_cmp_eq_u32 s54, 8
	s_cselect_b32 s21, s15, s19
	s_cselect_b32 s20, s14, s18
	s_cselect_b32 s19, s13, s53
	s_cselect_b32 s18, s12, s52
	v_mov_b32_e32 v128, v132
	ds_read_b128 v[156:159], v135
	ds_read_b128 v[160:163], v135 offset:1024
	ds_read_b128 v[164:167], v135 offset:2048
	ds_read_b128 v[168:171], v135 offset:3072
	ds_read_b128 v[172:175], v135 offset:4096
	ds_read_b128 v[176:179], v135 offset:5120
	ds_read_b128 v[180:183], v135 offset:6144
	ds_read_b128 v[184:187], v135 offset:7168
	s_nop 0
	v_mov_b32_e32 v128, v133
	s_nop 0
	s_waitcnt lgkmcnt(8)
	s_barrier
	s_waitcnt lgkmcnt(0)
	s_setprio 1
	s_waitcnt lgkmcnt(0)
	v_mfma_scale_f32_16x16x128_f8f6f4 v[124:127], v[140:147], v[156:163], v[124:127], v136, v136 op_sel_hi:[0,0,0]
	v_mfma_scale_f32_16x16x128_f8f6f4 v[120:123], v[148:155], v[156:163], v[120:123], v136, v136 op_sel_hi:[0,0,0]
	s_mov_b32 m0, s39
	v_mfma_scale_f32_16x16x128_f8f6f4 v[116:119], v[140:147], v[164:171], v[116:119], v136, v136 op_sel_hi:[0,0,0]
	global_load_lds_dwordx4 v132, s[16:17]
	v_mfma_scale_f32_16x16x128_f8f6f4 v[112:115], v[148:155], v[164:171], v[112:115], v136, v136 op_sel_hi:[0,0,0]
	v_mfma_scale_f32_16x16x128_f8f6f4 v[188:191], v[140:147], v[172:179], v[108:111], v136, v136 op_sel_hi:[0,0,0]
	s_mov_b32 m0, s40
	v_mfma_scale_f32_16x16x128_f8f6f4 v[192:195], v[148:155], v[172:179], v[104:107], v136, v136 op_sel_hi:[0,0,0]
	global_load_lds_dwordx4 v133, s[16:17]
	v_mfma_scale_f32_16x16x128_f8f6f4 v[196:199], v[140:147], v[180:187], v[100:103], v136, v136 op_sel_hi:[0,0,0]
	v_mfma_scale_f32_16x16x128_f8f6f4 v[200:203], v[148:155], v[180:187], v[96:99], v136, v136 op_sel_hi:[0,0,0]
	s_setprio 0
	s_barrier
	v_mov_b32_e32 v128, v132
	s_nop 2
	ds_read_b128 v[96:99], v137
	ds_read_b128 v[100:103], v137 offset:1024
	ds_read_b128 v[104:107], v137 offset:2048
	ds_read_b128 v[108:111], v137 offset:3072
	s_nop 0
	v_mov_b32_e32 v128, v133
	s_nop 0
	s_barrier
	s_waitcnt lgkmcnt(0)
	s_setprio 1
	s_waitcnt lgkmcnt(0)
	v_mfma_scale_f32_16x16x128_f8f6f4 v[204:207], v[96:103], v[156:163], v[92:95], v136, v136 op_sel_hi:[0,0,0]
	v_mfma_scale_f32_16x16x128_f8f6f4 v[156:159], v[104:111], v[156:163], v[88:91], v136, v136 op_sel_hi:[0,0,0]
	s_mov_b32 m0, s41
	v_mfma_scale_f32_16x16x128_f8f6f4 v[160:163], v[96:103], v[164:171], v[84:87], v136, v136 op_sel_hi:[0,0,0]
	global_load_lds_dwordx4 v132, s[18:19]
	v_mfma_scale_f32_16x16x128_f8f6f4 v[164:167], v[104:111], v[164:171], v[80:83], v136, v136 op_sel_hi:[0,0,0]
	v_mfma_scale_f32_16x16x128_f8f6f4 v[168:171], v[96:103], v[172:179], v[76:79], v136, v136 op_sel_hi:[0,0,0]
	s_mov_b32 m0, s42
	v_mfma_scale_f32_16x16x128_f8f6f4 v[172:175], v[104:111], v[172:179], v[72:75], v136, v136 op_sel_hi:[0,0,0]
	global_load_lds_dwordx4 v133, s[18:19]
	v_mfma_scale_f32_16x16x128_f8f6f4 v[176:179], v[96:103], v[180:187], v[68:71], v136, v136 op_sel_hi:[0,0,0]
	v_mfma_scale_f32_16x16x128_f8f6f4 v[180:183], v[104:111], v[180:187], v[64:67], v136, v136 op_sel_hi:[0,0,0]
	s_setprio 0
	v_mov_b32_e32 v128, v132
	s_barrier
	s_nop 2
	ds_read_b128 v[64:67], v135 offset:16384
	ds_read_b128 v[68:71], v135 offset:17408
	ds_read_b128 v[72:75], v135 offset:18432
	ds_read_b128 v[76:79], v135 offset:19456
	ds_read_b128 v[80:83], v135 offset:20480
	ds_read_b128 v[84:87], v135 offset:21504
	ds_read_b128 v[88:91], v135 offset:22528
	ds_read_b128 v[92:95], v135 offset:23552
	s_nop 0
	v_mov_b32_e32 v128, v133
	s_nop 0
	s_barrier
	s_waitcnt lgkmcnt(0)
	s_setprio 1
	s_waitcnt lgkmcnt(0)
	v_mfma_scale_f32_16x16x128_f8f6f4 v[60:63], v[140:147], v[64:71], v[60:63], v136, v136 op_sel_hi:[0,0,0]
	v_mfma_scale_f32_16x16x128_f8f6f4 v[56:59], v[148:155], v[64:71], v[56:59], v136, v136 op_sel_hi:[0,0,0]
	s_mov_b32 m0, s25
	v_mfma_scale_f32_16x16x128_f8f6f4 v[52:55], v[140:147], v[72:79], v[52:55], v136, v136 op_sel_hi:[0,0,0]
	global_load_lds_dwordx4 v132, s[20:21]
	v_mfma_scale_f32_16x16x128_f8f6f4 v[48:51], v[148:155], v[72:79], v[48:51], v136, v136 op_sel_hi:[0,0,0]
	v_mfma_scale_f32_16x16x128_f8f6f4 v[184:187], v[140:147], v[80:87], v[44:47], v136, v136 op_sel_hi:[0,0,0]
	s_mov_b32 m0, s26
	v_mfma_scale_f32_16x16x128_f8f6f4 v[208:211], v[148:155], v[80:87], v[40:43], v136, v136 op_sel_hi:[0,0,0]
	global_load_lds_dwordx4 v133, s[20:21]
	v_mfma_scale_f32_16x16x128_f8f6f4 v[212:215], v[140:147], v[88:95], v[36:39], v136, v136 op_sel_hi:[0,0,0]
	v_mfma_scale_f32_16x16x128_f8f6f4 v[216:219], v[148:155], v[88:95], v[32:35], v136, v136 op_sel_hi:[0,0,0]
	s_setprio 0
	s_barrier
	s_add_u32 s56, s18, 0x30000
	s_nop 3
	v_mov_b32_e32 v32, v132
	s_addc_u32 s57, s19, 0
	s_nop 0
	v_mov_b32_e32 v32, v133
	s_nop 0
	s_waitcnt vmcnt(4)
	s_barrier
	s_setprio 1
	v_mfma_scale_f32_16x16x128_f8f6f4 v[220:223], v[96:103], v[64:71], v[28:31], v136, v136 op_sel_hi:[0,0,0]
	v_mfma_scale_f32_16x16x128_f8f6f4 v[224:227], v[104:111], v[64:71], v[24:27], v136, v136 op_sel_hi:[0,0,0]
	s_mov_b32 m0, s43
	v_mfma_scale_f32_16x16x128_f8f6f4 v[228:231], v[96:103], v[72:79], v[20:23], v136, v136 op_sel_hi:[0,0,0]
	global_load_lds_dwordx4 v132, s[56:57]
	v_mfma_scale_f32_16x16x128_f8f6f4 v[232:235], v[104:111], v[72:79], v[16:19], v136, v136 op_sel_hi:[0,0,0]
	v_mfma_scale_f32_16x16x128_f8f6f4 v[236:239], v[96:103], v[80:87], v[12:15], v136, v136 op_sel_hi:[0,0,0]
	s_mov_b32 m0, s44
	v_mfma_scale_f32_16x16x128_f8f6f4 v[240:243], v[104:111], v[80:87], v[8:11], v136, v136 op_sel_hi:[0,0,0]
	global_load_lds_dwordx4 v133, s[56:57]
	v_mfma_scale_f32_16x16x128_f8f6f4 v[244:247], v[96:103], v[88:95], v[4:7], v136, v136 op_sel_hi:[0,0,0]
	v_mfma_scale_f32_16x16x128_f8f6f4 v[248:251], v[104:111], v[88:95], v[0:3], v136, v136 op_sel_hi:[0,0,0]
	s_setprio 0
	s_barrier
	s_nop 4
	ds_read_b128 v[0:3], v138
	ds_read_b128 v[4:7], v138 offset:1024
	ds_read_b128 v[8:11], v138 offset:2048
	ds_read_b128 v[12:15], v138 offset:3072
	s_add_u32 s56, s20, 0x30000
	v_mov_b32_e32 v64, v132
	ds_read_b128 v[16:19], v135 offset:32768
	ds_read_b128 v[20:23], v135 offset:33792
	ds_read_b128 v[24:27], v135 offset:34816
	ds_read_b128 v[28:31], v135 offset:35840
	ds_read_b128 v[32:35], v135 offset:36864
	ds_read_b128 v[36:39], v135 offset:37888
	ds_read_b128 v[40:43], v135 offset:38912
	ds_read_b128 v[44:47], v135 offset:39936
	s_addc_u32 s57, s21, 0
	s_nop 0
	v_mov_b32_e32 v64, v133
	s_nop 0
	s_waitcnt lgkmcnt(8)
	s_barrier
	s_waitcnt lgkmcnt(0)
	s_setprio 1
	s_waitcnt lgkmcnt(0)
	v_mfma_scale_f32_16x16x128_f8f6f4 v[124:127], v[0:7], v[16:23], v[124:127], v136, v136 op_sel_hi:[0,0,0]
	v_mfma_scale_f32_16x16x128_f8f6f4 v[120:123], v[8:15], v[16:23], v[120:123], v136, v136 op_sel_hi:[0,0,0]
	s_mov_b32 m0, s27
	v_mfma_scale_f32_16x16x128_f8f6f4 v[116:119], v[0:7], v[24:31], v[116:119], v136, v136 op_sel_hi:[0,0,0]
	global_load_lds_dwordx4 v132, s[56:57]
	v_mfma_scale_f32_16x16x128_f8f6f4 v[112:115], v[8:15], v[24:31], v[112:115], v136, v136 op_sel_hi:[0,0,0]
	v_mfma_scale_f32_16x16x128_f8f6f4 v[108:111], v[0:7], v[32:39], v[188:191], v136, v136 op_sel_hi:[0,0,0]
	s_mov_b32 m0, s28
	v_mfma_scale_f32_16x16x128_f8f6f4 v[104:107], v[8:15], v[32:39], v[192:195], v136, v136 op_sel_hi:[0,0,0]
	global_load_lds_dwordx4 v133, s[56:57]
	v_mfma_scale_f32_16x16x128_f8f6f4 v[100:103], v[0:7], v[40:47], v[196:199], v136, v136 op_sel_hi:[0,0,0]
	v_mfma_scale_f32_16x16x128_f8f6f4 v[96:99], v[8:15], v[40:47], v[200:203], v136, v136 op_sel_hi:[0,0,0]
	s_setprio 0
	s_barrier
	v_mov_b32_e32 v128, v132
	ds_read_b128 v[140:143], v139
	ds_read_b128 v[144:147], v139 offset:1024
	ds_read_b128 v[148:151], v139 offset:2048
	ds_read_b128 v[152:155], v139 offset:3072
	v_lshl_add_u64 v[64:65], s[18:19], 0, v[128:129]
	v_lshl_add_u64 v[64:65], v[64:65], 0, s[4:5]
	v_mov_b32_e32 v128, v133
	v_lshl_add_u64 v[64:65], s[18:19], 0, v[128:129]
	v_lshl_add_u64 v[64:65], v[64:65], 0, s[4:5]
	s_barrier
	s_waitcnt lgkmcnt(0)
	s_setprio 1
	s_waitcnt lgkmcnt(0)
	v_mfma_scale_f32_16x16x128_f8f6f4 v[92:95], v[140:147], v[16:23], v[204:207], v136, v136 op_sel_hi:[0,0,0]
	v_mfma_scale_f32_16x16x128_f8f6f4 v[88:91], v[148:155], v[16:23], v[156:159], v136, v136 op_sel_hi:[0,0,0]
	s_add_u32 s98, s18, s4
	s_addc_u32 s99, s19, s5
	s_mov_b32 m0, s46
	v_mfma_scale_f32_16x16x128_f8f6f4 v[84:87], v[140:147], v[24:31], v[160:163], v136, v136 op_sel_hi:[0,0,0]
	global_load_lds_dwordx4 v132, s[98:99]
	v_mfma_scale_f32_16x16x128_f8f6f4 v[80:83], v[148:155], v[24:31], v[164:167], v136, v136 op_sel_hi:[0,0,0]
	v_mfma_scale_f32_16x16x128_f8f6f4 v[76:79], v[140:147], v[32:39], v[168:171], v136, v136 op_sel_hi:[0,0,0]
	s_mov_b32 m0, s47
	v_mfma_scale_f32_16x16x128_f8f6f4 v[72:75], v[148:155], v[32:39], v[172:175], v136, v136 op_sel_hi:[0,0,0]
	global_load_lds_dwordx4 v133, s[98:99]
	v_mfma_scale_f32_16x16x128_f8f6f4 v[68:71], v[140:147], v[40:47], v[176:179], v136, v136 op_sel_hi:[0,0,0]
	v_mfma_scale_f32_16x16x128_f8f6f4 v[64:67], v[148:155], v[40:47], v[180:183], v136, v136 op_sel_hi:[0,0,0]
	s_setprio 0
	v_mov_b32_e32 v128, v132
	s_barrier
	ds_read_b128 v[16:19], v135 offset:49152
	ds_read_b128 v[20:23], v135 offset:50176
	ds_read_b128 v[156:159], v135 offset:51200
	ds_read_b128 v[160:163], v135 offset:52224
	ds_read_b128 v[164:167], v135 offset:53248
	ds_read_b128 v[168:171], v135 offset:54272
	ds_read_b128 v[172:175], v135 offset:55296
	ds_read_b128 v[176:179], v135 offset:56320
	v_lshl_add_u64 v[24:25], s[20:21], 0, v[128:129]
	v_lshl_add_u64 v[24:25], v[24:25], 0, s[4:5]
	v_mov_b32_e32 v128, v133
	v_lshl_add_u64 v[24:25], s[20:21], 0, v[128:129]
	v_lshl_add_u64 v[24:25], v[24:25], 0, s[4:5]
	s_barrier
	s_waitcnt lgkmcnt(0)
	s_setprio 1
	s_waitcnt lgkmcnt(0)
	v_mfma_scale_f32_16x16x128_f8f6f4 v[60:63], v[0:7], v[16:23], v[60:63], v136, v136 op_sel_hi:[0,0,0]
	v_mfma_scale_f32_16x16x128_f8f6f4 v[56:59], v[8:15], v[16:23], v[56:59], v136, v136 op_sel_hi:[0,0,0]
	s_add_u32 s98, s20, s4
	s_addc_u32 s99, s21, s5
	s_mov_b32 m0, s36
	v_mfma_scale_f32_16x16x128_f8f6f4 v[52:55], v[0:7], v[156:163], v[52:55], v136, v136 op_sel_hi:[0,0,0]
	global_load_lds_dwordx4 v132, s[98:99]
	v_mfma_scale_f32_16x16x128_f8f6f4 v[48:51], v[8:15], v[156:163], v[48:51], v136, v136 op_sel_hi:[0,0,0]
	v_mfma_scale_f32_16x16x128_f8f6f4 v[44:47], v[0:7], v[164:171], v[184:187], v136, v136 op_sel_hi:[0,0,0]
	s_mov_b32 m0, s37
	v_mfma_scale_f32_16x16x128_f8f6f4 v[40:43], v[8:15], v[164:171], v[208:211], v136, v136 op_sel_hi:[0,0,0]
	global_load_lds_dwordx4 v133, s[98:99]
	v_mfma_scale_f32_16x16x128_f8f6f4 v[36:39], v[0:7], v[172:179], v[212:215], v136, v136 op_sel_hi:[0,0,0]
	v_mfma_scale_f32_16x16x128_f8f6f4 v[32:35], v[8:15], v[172:179], v[216:219], v136, v136 op_sel_hi:[0,0,0]
	s_setprio 0
	s_barrier
	s_add_u32 s18, s18, 0x30080
	s_addc_u32 s19, s19, 0
	v_mov_b32_e32 v0, v132
	s_add_i32 s20, s45, s24
	s_nop 0
	v_mov_b32_e32 v0, v133
	s_nop 0
	s_waitcnt vmcnt(4)
	s_barrier
	s_setprio 1
	v_mfma_scale_f32_16x16x128_f8f6f4 v[28:31], v[140:147], v[16:23], v[220:223], v136, v136 op_sel_hi:[0,0,0]
	v_mfma_scale_f32_16x16x128_f8f6f4 v[24:27], v[148:155], v[16:23], v[224:227], v136, v136 op_sel_hi:[0,0,0]
	s_mov_b32 m0, s20
	v_mfma_scale_f32_16x16x128_f8f6f4 v[20:23], v[140:147], v[156:163], v[228:231], v136, v136 op_sel_hi:[0,0,0]
	global_load_lds_dwordx4 v132, s[18:19]
	v_mfma_scale_f32_16x16x128_f8f6f4 v[16:19], v[148:155], v[156:163], v[232:235], v136, v136 op_sel_hi:[0,0,0]
	v_mfma_scale_f32_16x16x128_f8f6f4 v[12:15], v[140:147], v[164:171], v[236:239], v136, v136 op_sel_hi:[0,0,0]
	s_add_i32 m0, s20, 0x2000
	v_mfma_scale_f32_16x16x128_f8f6f4 v[8:11], v[148:155], v[164:171], v[240:243], v136, v136 op_sel_hi:[0,0,0]
	global_load_lds_dwordx4 v133, s[18:19]
	v_mfma_scale_f32_16x16x128_f8f6f4 v[4:7], v[140:147], v[172:179], v[244:247], v136, v136 op_sel_hi:[0,0,0]
	v_mfma_scale_f32_16x16x128_f8f6f4 v[0:3], v[148:155], v[172:179], v[248:251], v136, v136 op_sel_hi:[0,0,0]
	s_setprio 0
	s_add_i32 s54, s54, 2
	s_add_u32 s16, s16, 0x100
	s_addc_u32 s17, s17, 0
	s_add_u32 s52, s52, 0x100
	s_addc_u32 s53, s53, 0
	s_cmp_gt_u32 s54, 9
	s_barrier
	s_cbranch_scc0 .LBB0_2382
	v_pk_mul_f32 v[140:141], v[124:125], s[8:9] op_sel_hi:[1,0]
	v_pk_mul_f32 v[120:121], v[120:121], s[8:9] op_sel_hi:[1,0]
	v_mov_b32_e32 v125, v129
	v_cvt_pk_fp8_f32 v125, v120, v121
	v_pk_mul_f32 v[120:121], v[126:127], s[8:9] op_sel_hi:[1,0]
	v_pk_mul_f32 v[116:117], v[116:117], s[8:9] op_sel_hi:[1,0]
	v_mov_b32_e32 v126, v129
	v_cvt_pk_fp8_f32 v126, v116, v117
	v_pk_mul_f32 v[112:113], v[112:113], s[8:9] op_sel_hi:[1,0]
	v_mov_b32_e32 v127, v129
	v_cvt_pk_fp8_f32 v127, v112, v113
	v_pk_mul_f32 v[112:113], v[118:119], s[8:9] op_sel_hi:[1,0]
	v_pk_mul_f32 v[104:105], v[104:105], s[8:9] op_sel_hi:[1,0]
	v_cvt_pk_fp8_f32 v126, v112, v113 op_sel:[0,0,1]
	v_pk_mul_f32 v[112:113], v[114:115], s[8:9] op_sel_hi:[1,0]
	v_pk_mul_f32 v[100:101], v[100:101], s[8:9] op_sel_hi:[1,0]
	v_cvt_pk_fp8_f32 v127, v112, v113 op_sel:[0,0,1]
	v_pk_mul_f32 v[112:113], v[108:109], s[8:9] op_sel_hi:[1,0]
	v_mov_b32_e32 v109, v129
	v_cvt_pk_fp8_f32 v109, v104, v105
	v_pk_mul_f32 v[104:105], v[110:111], s[8:9] op_sel_hi:[1,0]
	v_mov_b32_e32 v110, v129
	v_cvt_pk_fp8_f32 v110, v100, v101
	v_pk_mul_f32 v[100:101], v[92:93], s[8:9] op_sel_hi:[1,0]
	v_pk_mul_f32 v[88:89], v[88:89], s[8:9] op_sel_hi:[1,0]
	v_mov_b32_e32 v93, v129
	v_cvt_pk_fp8_f32 v93, v88, v89
	v_pk_mul_f32 v[88:89], v[94:95], s[8:9] op_sel_hi:[1,0]
	v_pk_mul_f32 v[84:85], v[84:85], s[8:9] op_sel_hi:[1,0]
	v_mov_b32_e32 v94, v129
	v_cvt_pk_fp8_f32 v94, v84, v85
	v_pk_mul_f32 v[80:81], v[80:81], s[8:9] op_sel_hi:[1,0]
	v_mov_b32_e32 v95, v129
	v_cvt_pk_fp8_f32 v95, v80, v81
	v_pk_mul_f32 v[80:81], v[86:87], s[8:9] op_sel_hi:[1,0]
	v_pk_mul_f32 v[72:73], v[72:73], s[8:9] op_sel_hi:[1,0]
	v_cvt_pk_fp8_f32 v94, v80, v81 op_sel:[0,0,1]
	v_pk_mul_f32 v[80:81], v[82:83], s[8:9] op_sel_hi:[1,0]
	v_pk_mul_f32 v[68:69], v[68:69], s[8:9] op_sel_hi:[1,0]
	v_cvt_pk_fp8_f32 v95, v80, v81 op_sel:[0,0,1]
	v_pk_mul_f32 v[80:81], v[76:77], s[8:9] op_sel_hi:[1,0]
	v_mov_b32_e32 v77, v129
	v_cvt_pk_fp8_f32 v77, v72, v73
	v_pk_mul_f32 v[72:73], v[78:79], s[8:9] op_sel_hi:[1,0]
	v_mov_b32_e32 v78, v129
	v_cvt_pk_fp8_f32 v78, v68, v69
	v_pk_mul_f32 v[64:65], v[64:65], s[8:9] op_sel_hi:[1,0]
	v_mov_b32_e32 v79, v129
	v_cvt_pk_fp8_f32 v79, v64, v65
	v_pk_mul_f32 v[64:65], v[70:71], s[8:9] op_sel_hi:[1,0]
	v_pk_mul_f32 v[56:57], v[56:57], s[8:9] op_sel_hi:[1,0]
	v_cvt_pk_fp8_f32 v78, v64, v65 op_sel:[0,0,1]
	v_pk_mul_f32 v[64:65], v[66:67], s[8:9] op_sel_hi:[1,0]
	v_pk_mul_f32 v[52:53], v[52:53], s[8:9] op_sel_hi:[1,0]
	v_cvt_pk_fp8_f32 v79, v64, v65 op_sel:[0,0,1]
	v_pk_mul_f32 v[64:65], v[60:61], s[8:9] op_sel_hi:[1,0]
	v_mov_b32_e32 v61, v129
	v_cvt_pk_fp8_f32 v61, v56, v57
	v_pk_mul_f32 v[56:57], v[62:63], s[8:9] op_sel_hi:[1,0]
	v_mov_b32_e32 v62, v129
	v_cvt_pk_fp8_f32 v62, v52, v53
	v_pk_mul_f32 v[48:49], v[48:49], s[8:9] op_sel_hi:[1,0]
	v_mov_b32_e32 v63, v129
	v_cvt_pk_fp8_f32 v63, v48, v49
	s_lshl_b32 s16, s50, 8
	v_pk_mul_f32 v[48:49], v[54:55], s[8:9] op_sel_hi:[1,0]
	s_add_i32 s16, s16, s34
	v_cvt_pk_fp8_f32 v62, v48, v49 op_sel:[0,0,1]
	v_pk_mul_f32 v[48:49], v[50:51], s[8:9] op_sel_hi:[1,0]
	s_lshl_b32 s18, s51, 8
	s_ashr_i32 s17, s16, 31
	v_cvt_pk_fp8_f32 v63, v48, v49 op_sel:[0,0,1]
	v_pk_mul_f32 v[48:49], v[44:45], s[8:9] op_sel_hi:[1,0]
	v_pk_mul_f32 v[40:41], v[40:41], s[8:9] op_sel_hi:[1,0]
	v_mov_b32_e32 v45, v129
	s_ashr_i32 s19, s18, 31
	s_lshl_b64 s[20:21], s[16:17], 11
	v_cvt_pk_fp8_f32 v45, v40, v41
	v_pk_mul_f32 v[40:41], v[46:47], s[8:9] op_sel_hi:[1,0]
	v_pk_mul_f32 v[36:37], v[36:37], s[8:9] op_sel_hi:[1,0]
	v_mov_b32_e32 v46, v129
	s_add_u32 s17, s31, s20
	v_cvt_pk_fp8_f32 v46, v36, v37
	v_pk_mul_f32 v[36:37], v[28:29], s[8:9] op_sel_hi:[1,0]
	v_pk_mul_f32 v[24:25], v[24:25], s[8:9] op_sel_hi:[1,0]
	v_mov_b32_e32 v29, v129
	s_addc_u32 s20, s33, s21
	v_cvt_pk_fp8_f32 v29, v24, v25
	v_pk_mul_f32 v[24:25], v[30:31], s[8:9] op_sel_hi:[1,0]
	v_pk_mul_f32 v[20:21], v[20:21], s[8:9] op_sel_hi:[1,0]
	v_mov_b32_e32 v30, v129
	s_add_u32 s17, s17, s18
	v_cvt_pk_fp8_f32 v30, v20, v21
	v_pk_mul_f32 v[16:17], v[16:17], s[8:9] op_sel_hi:[1,0]
	v_mov_b32_e32 v31, v129
	s_addc_u32 s21, s20, s19
	v_cvt_pk_fp8_f32 v31, v16, v17
	s_add_u32 s20, s17, s35
	s_addc_u32 s21, s21, 0
	s_addk_i32 s16, 0x80
	v_pk_mul_f32 v[16:17], v[22:23], s[8:9] op_sel_hi:[1,0]
	s_ashr_i32 s17, s16, 31
	v_cvt_pk_fp8_f32 v30, v16, v17 op_sel:[0,0,1]
	v_pk_mul_f32 v[16:17], v[18:19], s[8:9] op_sel_hi:[1,0]
	v_mov_b32_e32 v124, v129
	v_mov_b32_e32 v108, v129
	v_pk_mul_f32 v[96:97], v[96:97], s[8:9] op_sel_hi:[1,0]
	v_mov_b32_e32 v111, v129
	v_mov_b32_e32 v92, v129
	s_lshl_b64 s[16:17], s[16:17], 11
	v_mov_b32_e32 v60, v129
	v_mov_b32_e32 v44, v129
	v_mov_b32_e32 v28, v129
	v_cvt_pk_fp8_f32 v31, v16, v17 op_sel:[0,0,1]
	v_pk_mul_f32 v[16:17], v[12:13], s[8:9] op_sel_hi:[1,0]
	v_pk_mul_f32 v[8:9], v[8:9], s[8:9] op_sel_hi:[1,0]
	v_mov_b32_e32 v13, v129
	v_mbcnt_lo_u32_b32 v128, -1, 0
	v_mbcnt_hi_u32_b32 v128, -1, v128
	v_cvt_pk_fp8_f32 v124, v140, v141
	v_ashrrev_i32_e32 v130, 1, v128
	v_cvt_pk_fp8_f32 v108, v112, v113
	v_cvt_pk_fp8_f32 v111, v96, v97
	v_cvt_pk_fp8_f32 v92, v100, v101
	v_mov_b32_e32 v76, v129
	v_cvt_pk_fp8_f32 v60, v64, v65
	v_cvt_pk_fp8_f32 v44, v48, v49
	v_pk_mul_f32 v[32:33], v[32:33], s[8:9] op_sel_hi:[1,0]
	v_mov_b32_e32 v47, v129
	s_add_u32 s16, s31, s16
	v_cvt_pk_fp8_f32 v28, v36, v37
	v_mov_b32_e32 v12, v129
	v_cvt_pk_fp8_f32 v13, v8, v9
	v_pk_mul_f32 v[8:9], v[14:15], s[8:9] op_sel_hi:[1,0]
	v_pk_mul_f32 v[4:5], v[4:5], s[8:9] op_sel_hi:[1,0]
	v_mov_b32_e32 v14, v129
	v_bfi_b32 v130, -16, v130, v128
	v_cvt_pk_fp8_f32 v76, v80, v81
	v_cvt_pk_fp8_f32 v47, v32, v33
	s_addc_u32 s17, s33, s17
	v_cvt_pk_fp8_f32 v12, v16, v17
	v_cvt_pk_fp8_f32 v14, v4, v5
	v_pk_mul_f32 v[0:1], v[0:1], s[8:9] op_sel_hi:[1,0]
	v_mov_b32_e32 v15, v129
	v_ashrrev_i32_e32 v131, 31, v130
	v_pk_mul_f32 v[96:97], v[102:103], s[8:9] op_sel_hi:[1,0]
	s_add_u32 s16, s16, s18
	v_cvt_pk_fp8_f32 v15, v0, v1
	v_lshlrev_b64 v[130:131], 11, v[130:131]
	v_cvt_pk_fp8_f32 v110, v96, v97 op_sel:[0,0,1]
	v_pk_mul_f32 v[96:97], v[98:99], s[8:9] op_sel_hi:[1,0]
	v_pk_mul_f32 v[32:33], v[38:39], s[8:9] op_sel_hi:[1,0]
	s_addc_u32 s17, s17, s19
	v_and_b32_e32 v128, 16, v128
	v_cvt_pk_fp8_f32 v124, v120, v121 op_sel:[0,0,1]
	v_pk_mul_f32 v[120:121], v[122:123], s[8:9] op_sel_hi:[1,0]
	v_cvt_pk_fp8_f32 v108, v104, v105 op_sel:[0,0,1]
	v_pk_mul_f32 v[104:105], v[106:107], s[8:9] op_sel_hi:[1,0]
	v_cvt_pk_fp8_f32 v111, v96, v97 op_sel:[0,0,1]
	v_lshl_add_u64 v[96:97], s[20:21], 0, v[130:131]
	v_cvt_pk_fp8_f32 v92, v88, v89 op_sel:[0,0,1]
	v_pk_mul_f32 v[88:89], v[90:91], s[8:9] op_sel_hi:[1,0]
	v_cvt_pk_fp8_f32 v60, v56, v57 op_sel:[0,0,1]
	v_pk_mul_f32 v[56:57], v[58:59], s[8:9] op_sel_hi:[1,0]
	v_cvt_pk_fp8_f32 v44, v40, v41 op_sel:[0,0,1]
	v_pk_mul_f32 v[40:41], v[42:43], s[8:9] op_sel_hi:[1,0]
	v_cvt_pk_fp8_f32 v46, v32, v33 op_sel:[0,0,1]
	v_pk_mul_f32 v[32:33], v[34:35], s[8:9] op_sel_hi:[1,0]
	s_add_u32 s16, s16, s35
	v_cvt_pk_fp8_f32 v28, v24, v25 op_sel:[0,0,1]
	v_pk_mul_f32 v[24:25], v[26:27], s[8:9] op_sel_hi:[1,0]
	v_pk_mul_f32 v[0:1], v[6:7], s[8:9] op_sel_hi:[1,0]
	v_cvt_pk_fp8_f32 v125, v120, v121 op_sel:[0,0,1]
	v_cvt_pk_fp8_f32 v109, v104, v105 op_sel:[0,0,1]
	v_lshl_add_u64 v[96:97], v[96:97], 0, v[128:129]
	v_cvt_pk_fp8_f32 v93, v88, v89 op_sel:[0,0,1]
	v_cvt_pk_fp8_f32 v76, v72, v73 op_sel:[0,0,1]
	v_pk_mul_f32 v[72:73], v[74:75], s[8:9] op_sel_hi:[1,0]
	v_cvt_pk_fp8_f32 v61, v56, v57 op_sel:[0,0,1]
	v_cvt_pk_fp8_f32 v45, v40, v41 op_sel:[0,0,1]
	v_cvt_pk_fp8_f32 v47, v32, v33 op_sel:[0,0,1]
	s_addc_u32 s17, s17, 0
	v_cvt_pk_fp8_f32 v29, v24, v25 op_sel:[0,0,1]
	v_cvt_pk_fp8_f32 v12, v8, v9 op_sel:[0,0,1]
	v_pk_mul_f32 v[8:9], v[10:11], s[8:9] op_sel_hi:[1,0]
	v_cvt_pk_fp8_f32 v14, v0, v1 op_sel:[0,0,1]
	v_pk_mul_f32 v[0:1], v[2:3], s[8:9] op_sel_hi:[1,0]
	v_add_co_u32_e32 v98, vcc, s30, v96
	v_cvt_pk_fp8_f32 v77, v72, v73 op_sel:[0,0,1]
	v_lshl_add_u64 v[32:33], s[16:17], 0, v[130:131]
	v_cvt_pk_fp8_f32 v13, v8, v9 op_sel:[0,0,1]
	v_cvt_pk_fp8_f32 v15, v0, v1 op_sel:[0,0,1]
	v_addc_co_u32_e32 v99, vcc, 0, v97, vcc
	v_lshl_add_u64 v[32:33], v[32:33], 0, v[128:129]
	v_add_co_u32_e32 v34, vcc, s30, v32
	v_permlane32_swap_b32_e32 v124, v126
	v_permlane32_swap_b32_e32 v125, v127
	v_permlane32_swap_b32_e32 v108, v110
	v_permlane32_swap_b32_e32 v109, v111
	v_permlane32_swap_b32_e32 v92, v94
	v_permlane32_swap_b32_e32 v93, v95
	v_permlane32_swap_b32_e32 v60, v62
	v_permlane32_swap_b32_e32 v61, v63
	v_permlane32_swap_b32_e32 v44, v46
	v_permlane32_swap_b32_e32 v45, v47
	v_addc_co_u32_e32 v35, vcc, 0, v33, vcc
	v_permlane32_swap_b32_e32 v28, v30
	v_permlane32_swap_b32_e32 v29, v31
	v_permlane16_swap_b32_e32 v124, v125
	v_permlane16_swap_b32_e32 v126, v127
	v_permlane16_swap_b32_e32 v108, v109
	v_permlane16_swap_b32_e32 v110, v111
	v_permlane16_swap_b32_e32 v92, v93
	v_permlane16_swap_b32_e32 v94, v95
	v_permlane32_swap_b32_e32 v76, v78
	v_permlane32_swap_b32_e32 v77, v79
	v_permlane16_swap_b32_e32 v60, v61
	v_permlane16_swap_b32_e32 v62, v63
	v_permlane16_swap_b32_e32 v44, v45
	v_permlane16_swap_b32_e32 v46, v47
	v_permlane16_swap_b32_e32 v28, v29
	v_permlane16_swap_b32_e32 v30, v31
	v_permlane32_swap_b32_e32 v12, v14
	v_permlane32_swap_b32_e32 v13, v15
	s_and_b64 vcc, exec, s[10:11]
	s_mov_b32 s51, s49
	s_mov_b32 s50, s48
	s_mov_b64 s[18:19], s[12:13]
	s_mov_b64 s[16:17], s[14:15]
	global_store_dwordx4 v[96:97], v[124:127], off
	global_store_dwordx4 v[98:99], v[108:111], off
	v_permlane16_swap_b32_e32 v76, v77
	v_permlane16_swap_b32_e32 v78, v79
	global_store_dwordx4 v[96:97], v[92:95], off offset:128
	global_store_dwordx4 v[98:99], v[76:79], off offset:128
	global_store_dwordx4 v[32:33], v[60:63], off
	global_store_dwordx4 v[34:35], v[44:47], off
	v_permlane16_swap_b32_e32 v12, v13
	v_permlane16_swap_b32_e32 v14, v15
	global_store_dwordx4 v[32:33], v[28:31], off offset:128
	global_store_dwordx4 v[34:35], v[12:15], off offset:128
	s_cbranch_vccz .LBB0_2377
	s_waitcnt vmcnt(0)
	v_readlane_b32 s0, v252, 2
	s_cmpk_gt_u32 s0, 0xff
	s_cbranch_scc1 .LBB0_2386
	s_barrier

.LBB0_3995:
	s_add_i32 s34, s6, 2
	s_add_u32 s8, s4, 0xfffe0080
	s_addc_u32 s7, s5, -1
	s_add_i32 s30, 0, 0x10000
	v_add_u32_e32 v140, s30, v200
	ds_read_b128 v[128:131], v140
	ds_read_b128 v[132:135], v140 offset:1024
	ds_read_b128 v[136:139], v140 offset:2048
	ds_read_b128 v[140:143], v140 offset:3072
	s_cmp_eq_u32 s12, s6
	s_cselect_b32 s6, s52, s8
	s_cselect_b32 s7, s53, s7
	s_cselect_b32 s9, s55, s27
	s_cselect_b32 s8, s54, s25
	v_mov_b32_e32 v168, v169
	ds_read_b128 v[144:147], v182
	ds_read_b128 v[148:151], v182 offset:1024
	ds_read_b128 v[152:155], v182 offset:2048
	ds_read_b128 v[156:159], v182 offset:3072
	ds_read_b128 v[160:163], v182 offset:4096
	ds_read_b128 v[164:167], v182 offset:5120
	ds_read_b128 v[184:187], v182 offset:6144
	ds_read_b128 v[188:191], v182 offset:7168
	s_nop 0
	v_mov_b32_e32 v168, v181
	s_nop 0
	s_waitcnt lgkmcnt(8)
	s_barrier
	s_waitcnt lgkmcnt(0)
	s_setprio 1
	s_waitcnt lgkmcnt(0)
	v_mfma_scale_f32_16x16x128_f8f6f4 v[120:123], v[128:135], v[144:151], v[120:123], v183, v183 op_sel_hi:[0,0,0]
	v_mov_b32_e32 v170, v200
	v_mfma_scale_f32_16x16x128_f8f6f4 v[124:127], v[136:143], v[144:151], v[124:127], v183, v183 op_sel_hi:[0,0,0]
	s_add_i32 m0, s3, 0xc000
	v_mfma_scale_f32_16x16x128_f8f6f4 v[200:203], v[136:143], v[160:167], v[88:91], v183, v183 op_sel_hi:[0,0,0]
	global_load_lds_dwordx4 v169, s[4:5]
	v_mfma_scale_f32_16x16x128_f8f6f4 v[176:179], v[128:135], v[152:159], v[108:111], v183, v183 op_sel_hi:[0,0,0]
	v_mfma_scale_f32_16x16x128_f8f6f4 v[192:195], v[136:143], v[152:159], v[104:107], v183, v183 op_sel_hi:[0,0,0]
	s_add_i32 m0, s3, 0xe000
	v_mfma_scale_f32_16x16x128_f8f6f4 v[196:199], v[128:135], v[160:167], v[92:95], v183, v183 op_sel_hi:[0,0,0]
	global_load_lds_dwordx4 v181, s[4:5]
	v_mfma_scale_f32_16x16x128_f8f6f4 v[204:207], v[128:135], v[184:191], v[76:79], v183, v183 op_sel_hi:[0,0,0]
	v_mfma_scale_f32_16x16x128_f8f6f4 v[208:211], v[136:143], v[184:191], v[72:75], v183, v183 op_sel_hi:[0,0,0]
	s_setprio 0
	s_barrier
	s_add_i32 s35, 0, 0x14000
	s_nop 1
	v_add_u32_e32 v92, s35, v170
	v_mov_b32_e32 v104, v180
	s_add_i32 s30, s30, s33
	ds_read_b128 v[72:75], v92
	ds_read_b128 v[76:79], v92 offset:1024
	ds_read_b128 v[88:91], v92 offset:2048
	ds_read_b128 v[92:95], v92 offset:3072
	s_mov_b32 m0, s30
	s_nop 0
	global_load_lds_dwordx4 v104, s[8:9]
	v_mov_b32_e32 v104, v212
	s_add_i32 m0, s30, 0x2000
	s_nop 0
	global_load_lds_dwordx4 v104, s[8:9]
	s_barrier
	s_waitcnt lgkmcnt(0)
	s_setprio 1
	s_waitcnt lgkmcnt(0)
	v_mfma_scale_f32_16x16x128_f8f6f4 v[116:119], v[144:151], v[72:79], v[116:119], v183, v183 op_sel_hi:[0,0,0]
	v_mov_b32_e32 v168, v212
	v_mfma_scale_f32_16x16x128_f8f6f4 v[112:115], v[144:151], v[88:95], v[112:115], v183, v183 op_sel_hi:[0,0,0]
	v_mfma_scale_f32_16x16x128_f8f6f4 v[212:215], v[152:159], v[72:79], v[100:103], v183, v183 op_sel_hi:[0,0,0]
	v_mfma_scale_f32_16x16x128_f8f6f4 v[216:219], v[152:159], v[88:95], v[96:99], v183, v183 op_sel_hi:[0,0,0]
	v_mfma_scale_f32_16x16x128_f8f6f4 v[220:223], v[160:167], v[72:79], v[84:87], v183, v183 op_sel_hi:[0,0,0]
	v_mfma_scale_f32_16x16x128_f8f6f4 v[160:163], v[160:167], v[88:95], v[80:83], v183, v183 op_sel_hi:[0,0,0]
	v_mfma_scale_f32_16x16x128_f8f6f4 v[164:167], v[184:191], v[72:79], v[68:71], v183, v183 op_sel_hi:[0,0,0]
	v_mfma_scale_f32_16x16x128_f8f6f4 v[184:187], v[184:191], v[88:95], v[64:67], v183, v183 op_sel_hi:[0,0,0]
	s_setprio 0
	v_mov_b32_e32 v144, v169
	s_barrier
	s_nop 2
	ds_read_b128 v[64:67], v182 offset:16384
	ds_read_b128 v[68:71], v182 offset:17408
	ds_read_b128 v[80:83], v182 offset:18432
	ds_read_b128 v[84:87], v182 offset:19456
	ds_read_b128 v[96:99], v182 offset:20480
	ds_read_b128 v[100:103], v182 offset:21504
	ds_read_b128 v[104:107], v182 offset:22528
	ds_read_b128 v[108:111], v182 offset:23552
	s_nop 0
	v_mov_b32_e32 v144, v181
	s_nop 0
	s_barrier
	s_waitcnt lgkmcnt(0)
	s_setprio 1
	s_waitcnt lgkmcnt(0)
	v_mfma_scale_f32_16x16x128_f8f6f4 v[224:227], v[128:135], v[64:71], v[60:63], v183, v183 op_sel_hi:[0,0,0]
	v_mfma_scale_f32_16x16x128_f8f6f4 v[228:231], v[136:143], v[64:71], v[56:59], v183, v183 op_sel_hi:[0,0,0]
	s_mov_b32 m0, s3
	v_mfma_scale_f32_16x16x128_f8f6f4 v[232:235], v[128:135], v[80:87], v[44:47], v183, v183 op_sel_hi:[0,0,0]
	global_load_lds_dwordx4 v169, s[6:7]
	v_mfma_scale_f32_16x16x128_f8f6f4 v[236:239], v[136:143], v[80:87], v[40:43], v183, v183 op_sel_hi:[0,0,0]
	v_mfma_scale_f32_16x16x128_f8f6f4 v[240:243], v[128:135], v[96:103], v[28:31], v183, v183 op_sel_hi:[0,0,0]
	s_mov_b32 m0, s11
	v_mfma_scale_f32_16x16x128_f8f6f4 v[244:247], v[136:143], v[96:103], v[24:27], v183, v183 op_sel_hi:[0,0,0]
	global_load_lds_dwordx4 v181, s[6:7]
	v_mfma_scale_f32_16x16x128_f8f6f4 v[248:251], v[128:135], v[104:111], v[12:15], v183, v183 op_sel_hi:[0,0,0]
	v_mfma_scale_f32_16x16x128_f8f6f4 v[172:175], v[136:143], v[104:111], v[8:11], v183, v183 op_sel_hi:[0,0,0]
	s_setprio 0
	s_barrier
	s_add_u32 s30, s8, s20
	s_addc_u32 s31, s9, s21
	s_nop 2
	v_mov_b32_e32 v8, v180
	s_add_i32 s35, s35, s33
	s_mov_b32 s100, s35
	s_nop 0
	v_mov_b32_e32 v8, v168
	s_add_i32 s101, s35, 0x2000
	s_nop 0
	s_waitcnt vmcnt(4)
	s_barrier
	s_setprio 1
	v_mfma_scale_f32_16x16x128_f8f6f4 v[52:55], v[64:71], v[72:79], v[52:55], v183, v183 op_sel_hi:[0,0,0]
	v_mfma_scale_f32_16x16x128_f8f6f4 v[48:51], v[64:71], v[88:95], v[48:51], v183, v183 op_sel_hi:[0,0,0]
	s_mov_b32 m0, s100
	v_mfma_scale_f32_16x16x128_f8f6f4 v[36:39], v[80:87], v[72:79], v[36:39], v183, v183 op_sel_hi:[0,0,0]
	global_load_lds_dwordx4 v180, s[30:31]
	v_mfma_scale_f32_16x16x128_f8f6f4 v[32:35], v[80:87], v[88:95], v[32:35], v183, v183 op_sel_hi:[0,0,0]
	v_mfma_scale_f32_16x16x128_f8f6f4 v[20:23], v[96:103], v[72:79], v[20:23], v183, v183 op_sel_hi:[0,0,0]
	s_mov_b32 m0, s101
	v_mfma_scale_f32_16x16x128_f8f6f4 v[16:19], v[96:103], v[88:95], v[16:19], v183, v183 op_sel_hi:[0,0,0]
	global_load_lds_dwordx4 v168, s[30:31]
	v_mfma_scale_f32_16x16x128_f8f6f4 v[4:7], v[104:111], v[72:79], v[4:7], v183, v183 op_sel_hi:[0,0,0]
	v_mfma_scale_f32_16x16x128_f8f6f4 v[0:3], v[104:111], v[88:95], v[0:3], v183, v183 op_sel_hi:[0,0,0]
	s_setprio 0
	s_add_i32 s35, 0, 0x18000
	v_add_u32_e32 v24, s35, v170
	s_barrier
	ds_read_b128 v[8:11], v24
	ds_read_b128 v[12:15], v24 offset:1024
	ds_read_b128 v[128:131], v24 offset:2048
	ds_read_b128 v[132:135], v24 offset:3072
	s_add_u32 s36, s6, 0x20000
	v_mov_b32_e32 v64, v169
	ds_read_b128 v[24:27], v182 offset:32768
	ds_read_b128 v[28:31], v182 offset:33792
	ds_read_b128 v[40:43], v182 offset:34816
	ds_read_b128 v[44:47], v182 offset:35840
	ds_read_b128 v[56:59], v182 offset:36864
	ds_read_b128 v[60:63], v182 offset:37888
	ds_read_b128 v[136:139], v182 offset:38912
	ds_read_b128 v[140:143], v182 offset:39936
	s_addc_u32 s37, s7, 0
	s_nop 0
	v_mov_b32_e32 v64, v181
	s_nop 0
	s_waitcnt lgkmcnt(8)
	s_barrier
	s_waitcnt lgkmcnt(0)
	s_setprio 1
	s_waitcnt lgkmcnt(0)
	v_mfma_scale_f32_16x16x128_f8f6f4 v[120:123], v[8:15], v[24:31], v[120:123], v183, v183 op_sel_hi:[0,0,0]
	v_mfma_scale_f32_16x16x128_f8f6f4 v[124:127], v[128:135], v[24:31], v[124:127], v183, v183 op_sel_hi:[0,0,0]
	s_mov_b32 m0, s14
	v_mfma_scale_f32_16x16x128_f8f6f4 v[108:111], v[8:15], v[40:47], v[176:179], v183, v183 op_sel_hi:[0,0,0]
	global_load_lds_dwordx4 v169, s[36:37]
	v_mfma_scale_f32_16x16x128_f8f6f4 v[104:107], v[128:135], v[40:47], v[192:195], v183, v183 op_sel_hi:[0,0,0]
	v_mfma_scale_f32_16x16x128_f8f6f4 v[92:95], v[8:15], v[56:63], v[196:199], v183, v183 op_sel_hi:[0,0,0]
	s_mov_b32 m0, s15
	v_mfma_scale_f32_16x16x128_f8f6f4 v[88:91], v[128:135], v[56:63], v[200:203], v183, v183 op_sel_hi:[0,0,0]
	global_load_lds_dwordx4 v181, s[36:37]
	v_mfma_scale_f32_16x16x128_f8f6f4 v[76:79], v[8:15], v[136:143], v[204:207], v183, v183 op_sel_hi:[0,0,0]
	s_nop 5
	v_mov_b32_e32 v200, v170
	v_mfma_scale_f32_16x16x128_f8f6f4 v[72:75], v[128:135], v[136:143], v[208:211], v183, v183 op_sel_hi:[0,0,0]
	s_setprio 0
	s_barrier
	s_add_i32 s36, 0, 0x1c000
	v_add_u32_e32 v64, s36, v200
	v_mov_b32_e32 v170, v180
	ds_read_b128 v[144:147], v64
	ds_read_b128 v[148:151], v64 offset:1024
	ds_read_b128 v[152:155], v64 offset:2048
	ds_read_b128 v[156:159], v64 offset:3072
	s_add_i32 s35, s35, s33
	v_lshl_add_u64 v[64:65], s[8:9], 0, v[170:171]
	v_lshl_add_u64 v[64:65], v[64:65], 0, s[62:63]
	v_mov_b32_e32 v170, v168
	v_lshl_add_u64 v[64:65], s[8:9], 0, v[170:171]
	v_lshl_add_u64 v[64:65], v[64:65], 0, s[62:63]
	s_barrier
	s_waitcnt lgkmcnt(0)
	s_setprio 1
	s_waitcnt lgkmcnt(0)
	v_mfma_scale_f32_16x16x128_f8f6f4 v[116:119], v[24:31], v[144:151], v[116:119], v183, v183 op_sel_hi:[0,0,0]
	v_mfma_scale_f32_16x16x128_f8f6f4 v[112:115], v[24:31], v[152:159], v[112:115], v183, v183 op_sel_hi:[0,0,0]
	s_add_u32 s98, s8, s62
	s_addc_u32 s99, s9, s63
	s_mov_b32 m0, s35
	v_mfma_scale_f32_16x16x128_f8f6f4 v[100:103], v[40:47], v[144:151], v[212:215], v183, v183 op_sel_hi:[0,0,0]
	global_load_lds_dwordx4 v180, s[98:99]
	v_mfma_scale_f32_16x16x128_f8f6f4 v[96:99], v[40:47], v[152:159], v[216:219], v183, v183 op_sel_hi:[0,0,0]
	s_nop 5
	v_mov_b32_e32 v212, v168
	v_mfma_scale_f32_16x16x128_f8f6f4 v[84:87], v[56:63], v[144:151], v[220:223], v183, v183 op_sel_hi:[0,0,0]
	s_add_i32 m0, s35, 0x2000
	v_mfma_scale_f32_16x16x128_f8f6f4 v[80:83], v[56:63], v[152:159], v[160:163], v183, v183 op_sel_hi:[0,0,0]
	global_load_lds_dwordx4 v168, s[98:99]
	v_mfma_scale_f32_16x16x128_f8f6f4 v[68:71], v[136:143], v[144:151], v[164:167], v183, v183 op_sel_hi:[0,0,0]
	v_mfma_scale_f32_16x16x128_f8f6f4 v[64:67], v[136:143], v[152:159], v[184:187], v183, v183 op_sel_hi:[0,0,0]
	s_setprio 0
	v_mov_b32_e32 v170, v169
	s_barrier
	ds_read_b128 v[136:139], v182 offset:49152
	ds_read_b128 v[140:143], v182 offset:50176
	ds_read_b128 v[160:163], v182 offset:51200
	ds_read_b128 v[164:167], v182 offset:52224
	ds_read_b128 v[184:187], v182 offset:53248
	ds_read_b128 v[188:191], v182 offset:54272
	ds_read_b128 v[192:195], v182 offset:55296
	ds_read_b128 v[196:199], v182 offset:56320
	v_lshl_add_u64 v[24:25], s[6:7], 0, v[170:171]
	v_lshl_add_u64 v[24:25], v[24:25], 0, s[62:63]
	v_mov_b32_e32 v170, v181
	v_lshl_add_u64 v[24:25], s[6:7], 0, v[170:171]
	v_lshl_add_u64 v[24:25], v[24:25], 0, s[62:63]
	s_barrier
	s_waitcnt lgkmcnt(0)
	s_setprio 1
	s_waitcnt lgkmcnt(0)
	v_mfma_scale_f32_16x16x128_f8f6f4 v[60:63], v[8:15], v[136:143], v[224:227], v183, v183 op_sel_hi:[0,0,0]
	v_mfma_scale_f32_16x16x128_f8f6f4 v[56:59], v[128:135], v[136:143], v[228:231], v183, v183 op_sel_hi:[0,0,0]
	s_add_u32 s98, s6, s62
	s_addc_u32 s99, s7, s63
	s_mov_b32 m0, s16
	v_mfma_scale_f32_16x16x128_f8f6f4 v[44:47], v[8:15], v[160:167], v[232:235], v183, v183 op_sel_hi:[0,0,0]
	global_load_lds_dwordx4 v169, s[98:99]
	v_mfma_scale_f32_16x16x128_f8f6f4 v[40:43], v[128:135], v[160:167], v[236:239], v183, v183 op_sel_hi:[0,0,0]
	v_mfma_scale_f32_16x16x128_f8f6f4 v[28:31], v[8:15], v[184:191], v[240:243], v183, v183 op_sel_hi:[0,0,0]
	s_mov_b32 m0, s17
	v_mfma_scale_f32_16x16x128_f8f6f4 v[24:27], v[128:135], v[184:191], v[244:247], v183, v183 op_sel_hi:[0,0,0]
	global_load_lds_dwordx4 v181, s[98:99]
	v_mfma_scale_f32_16x16x128_f8f6f4 v[12:15], v[8:15], v[192:199], v[248:251], v183, v183 op_sel_hi:[0,0,0]
	v_mfma_scale_f32_16x16x128_f8f6f4 v[8:11], v[128:135], v[192:199], v[172:175], v183, v183 op_sel_hi:[0,0,0]
	s_setprio 0
	s_barrier
	v_mov_b32_e32 v170, v180
	s_add_i32 s6, s36, s33
	v_lshl_add_u64 v[128:129], s[30:31], 0, v[170:171]
	v_lshl_add_u64 v[128:129], v[128:129], 0, s[62:63]
	s_mov_b32 s100, s6
	v_mov_b32_e32 v170, v168
	s_add_i32 s101, s6, 0x2000
	v_lshl_add_u64 v[128:129], s[30:31], 0, v[170:171]
	v_lshl_add_u64 v[128:129], v[128:129], 0, s[62:63]
	s_waitcnt vmcnt(4)
	s_barrier
	s_setprio 1
	v_mfma_scale_f32_16x16x128_f8f6f4 v[52:55], v[136:143], v[144:151], v[52:55], v183, v183 op_sel_hi:[0,0,0]
	v_mfma_scale_f32_16x16x128_f8f6f4 v[48:51], v[136:143], v[152:159], v[48:51], v183, v183 op_sel_hi:[0,0,0]
	s_add_u32 s98, s30, s62
	s_addc_u32 s99, s31, s63
	s_mov_b32 m0, s100
	v_mfma_scale_f32_16x16x128_f8f6f4 v[36:39], v[160:167], v[144:151], v[36:39], v183, v183 op_sel_hi:[0,0,0]
	global_load_lds_dwordx4 v180, s[98:99]
	v_mfma_scale_f32_16x16x128_f8f6f4 v[32:35], v[160:167], v[152:159], v[32:35], v183, v183 op_sel_hi:[0,0,0]
	v_mfma_scale_f32_16x16x128_f8f6f4 v[20:23], v[184:191], v[144:151], v[20:23], v183, v183 op_sel_hi:[0,0,0]
	s_mov_b32 m0, s101
	v_mfma_scale_f32_16x16x128_f8f6f4 v[16:19], v[184:191], v[152:159], v[16:19], v183, v183 op_sel_hi:[0,0,0]
	global_load_lds_dwordx4 v168, s[98:99]
	v_mfma_scale_f32_16x16x128_f8f6f4 v[4:7], v[192:199], v[144:151], v[4:7], v183, v183 op_sel_hi:[0,0,0]
	v_mfma_scale_f32_16x16x128_f8f6f4 v[0:3], v[192:199], v[152:159], v[0:3], v183, v183 op_sel_hi:[0,0,0]
	s_setprio 0
	s_add_u32 s4, s4, 0x100
	s_addc_u32 s5, s5, 0
	s_add_u32 s25, s25, 0x100
	s_addc_u32 s27, s27, 0
	s_cmp_ge_i32 s34, s13
	s_mov_b32 s6, s34
	s_barrier
	s_cbranch_scc0 .LBB0_3995

.LBB0_4066:
	s_add_i32 s34, s6, 2
	s_add_u32 s8, s4, 0xfffe0080
	s_addc_u32 s7, s5, -1
	s_add_i32 s30, 0, 0x10000
	v_add_u32_e32 v140, s30, v181
	ds_read_b128 v[128:131], v140
	ds_read_b128 v[132:135], v140 offset:1024
	ds_read_b128 v[136:139], v140 offset:2048
	ds_read_b128 v[140:143], v140 offset:3072
	s_cmp_eq_u32 s12, s6
	s_cselect_b32 s6, s52, s8
	s_cselect_b32 s7, s53, s7
	s_cselect_b32 s9, s55, s27
	s_cselect_b32 s8, s54, s25
	v_mov_b32_e32 v168, v169
	ds_read_b128 v[144:147], v182
	ds_read_b128 v[148:151], v182 offset:1024
	ds_read_b128 v[152:155], v182 offset:2048
	ds_read_b128 v[156:159], v182 offset:3072
	ds_read_b128 v[160:163], v182 offset:4096
	ds_read_b128 v[164:167], v182 offset:5120
	ds_read_b128 v[184:187], v182 offset:6144
	ds_read_b128 v[188:191], v182 offset:7168
	s_add_i32 m0, s3, 0xc000
	s_nop 0
	global_load_lds_dwordx4 v168, s[4:5]
	v_mov_b32_e32 v168, v200
	s_add_i32 m0, s3, 0xe000
	s_nop 0
	global_load_lds_dwordx4 v168, s[4:5]
	s_waitcnt lgkmcnt(8)
	s_barrier
	s_waitcnt lgkmcnt(0)
	s_setprio 1
	s_waitcnt lgkmcnt(0)
	v_mfma_scale_f32_16x16x128_f8f6f4 v[120:123], v[128:135], v[144:151], v[120:123], v183, v183 op_sel_hi:[0,0,0]
	v_mov_b32_e32 v170, v200
	v_mfma_scale_f32_16x16x128_f8f6f4 v[124:127], v[136:143], v[144:151], v[124:127], v183, v183 op_sel_hi:[0,0,0]
	v_mfma_scale_f32_16x16x128_f8f6f4 v[200:203], v[128:135], v[160:167], v[92:95], v183, v183 op_sel_hi:[0,0,0]
	v_mfma_scale_f32_16x16x128_f8f6f4 v[192:195], v[128:135], v[152:159], v[108:111], v183, v183 op_sel_hi:[0,0,0]
	v_mfma_scale_f32_16x16x128_f8f6f4 v[196:199], v[136:143], v[152:159], v[104:107], v183, v183 op_sel_hi:[0,0,0]
	v_mfma_scale_f32_16x16x128_f8f6f4 v[204:207], v[136:143], v[160:167], v[88:91], v183, v183 op_sel_hi:[0,0,0]
	v_mfma_scale_f32_16x16x128_f8f6f4 v[208:211], v[128:135], v[184:191], v[76:79], v183, v183 op_sel_hi:[0,0,0]
	v_mfma_scale_f32_16x16x128_f8f6f4 v[212:215], v[136:143], v[184:191], v[72:75], v183, v183 op_sel_hi:[0,0,0]
	s_setprio 0
	s_barrier
	s_add_i32 s35, 0, 0x14000
	v_add_u32_e32 v92, s35, v181
	v_mov_b32_e32 v104, v216
	s_add_i32 s30, s30, s33
	s_nop 0
	ds_read_b128 v[72:75], v92
	ds_read_b128 v[76:79], v92 offset:1024
	ds_read_b128 v[88:91], v92 offset:2048
	ds_read_b128 v[92:95], v92 offset:3072
	s_mov_b32 m0, s30
	s_nop 0
	global_load_lds_dwordx4 v104, s[8:9]
	v_mov_b32_e32 v104, v180
	s_add_i32 m0, s30, 0x2000
	s_nop 0
	global_load_lds_dwordx4 v104, s[8:9]
	s_barrier
	s_waitcnt lgkmcnt(0)
	s_setprio 1
	s_waitcnt lgkmcnt(0)
	v_mfma_scale_f32_16x16x128_f8f6f4 v[116:119], v[72:79], v[144:151], v[116:119], v183, v183 op_sel_hi:[0,0,0]
	v_mov_b32_e32 v168, v216
	v_mfma_scale_f32_16x16x128_f8f6f4 v[112:115], v[88:95], v[144:151], v[112:115], v183, v183 op_sel_hi:[0,0,0]
	v_mfma_scale_f32_16x16x128_f8f6f4 v[216:219], v[72:79], v[152:159], v[100:103], v183, v183 op_sel_hi:[0,0,0]
	v_mfma_scale_f32_16x16x128_f8f6f4 v[220:223], v[88:95], v[152:159], v[96:99], v183, v183 op_sel_hi:[0,0,0]
	v_mfma_scale_f32_16x16x128_f8f6f4 v[224:227], v[72:79], v[160:167], v[84:87], v183, v183 op_sel_hi:[0,0,0]
	v_mfma_scale_f32_16x16x128_f8f6f4 v[160:163], v[88:95], v[160:167], v[80:83], v183, v183 op_sel_hi:[0,0,0]
	v_mfma_scale_f32_16x16x128_f8f6f4 v[164:167], v[72:79], v[184:191], v[68:71], v183, v183 op_sel_hi:[0,0,0]
	v_mfma_scale_f32_16x16x128_f8f6f4 v[184:187], v[88:95], v[184:191], v[64:67], v183, v183 op_sel_hi:[0,0,0]
	s_setprio 0
	v_mov_b32_e32 v144, v169
	s_barrier
	s_nop 2
	ds_read_b128 v[64:67], v182 offset:16384
	ds_read_b128 v[68:71], v182 offset:17408
	ds_read_b128 v[80:83], v182 offset:18432
	ds_read_b128 v[84:87], v182 offset:19456
	ds_read_b128 v[96:99], v182 offset:20480
	ds_read_b128 v[100:103], v182 offset:21504
	ds_read_b128 v[104:107], v182 offset:22528
	ds_read_b128 v[108:111], v182 offset:23552
	s_nop 0
	v_mov_b32_e32 v144, v170
	s_nop 0
	s_barrier
	s_waitcnt lgkmcnt(0)
	s_setprio 1
	s_waitcnt lgkmcnt(0)
	v_mfma_scale_f32_16x16x128_f8f6f4 v[228:231], v[128:135], v[64:71], v[60:63], v183, v183 op_sel_hi:[0,0,0]
	v_mfma_scale_f32_16x16x128_f8f6f4 v[232:235], v[136:143], v[64:71], v[56:59], v183, v183 op_sel_hi:[0,0,0]
	s_mov_b32 m0, s3
	v_mfma_scale_f32_16x16x128_f8f6f4 v[236:239], v[128:135], v[80:87], v[44:47], v183, v183 op_sel_hi:[0,0,0]
	global_load_lds_dwordx4 v169, s[6:7]
	v_mfma_scale_f32_16x16x128_f8f6f4 v[240:243], v[136:143], v[80:87], v[40:43], v183, v183 op_sel_hi:[0,0,0]
	v_mfma_scale_f32_16x16x128_f8f6f4 v[244:247], v[128:135], v[96:103], v[28:31], v183, v183 op_sel_hi:[0,0,0]
	s_mov_b32 m0, s11
	v_mfma_scale_f32_16x16x128_f8f6f4 v[248:251], v[136:143], v[96:103], v[24:27], v183, v183 op_sel_hi:[0,0,0]
	global_load_lds_dwordx4 v170, s[6:7]
	v_mfma_scale_f32_16x16x128_f8f6f4 v[172:175], v[128:135], v[104:111], v[12:15], v183, v183 op_sel_hi:[0,0,0]
	v_mfma_scale_f32_16x16x128_f8f6f4 v[176:179], v[136:143], v[104:111], v[8:11], v183, v183 op_sel_hi:[0,0,0]
	s_setprio 0
	s_barrier
	s_add_u32 s30, s8, s20
	s_addc_u32 s31, s9, s21
	s_nop 2
	v_mov_b32_e32 v8, v168
	s_add_i32 s35, s35, s33
	s_mov_b32 s100, s35
	s_nop 0
	v_mov_b32_e32 v8, v180
	s_add_i32 s101, s35, 0x2000
	s_nop 0
	s_waitcnt vmcnt(4)
	s_barrier
	s_setprio 1
	v_mfma_scale_f32_16x16x128_f8f6f4 v[52:55], v[72:79], v[64:71], v[52:55], v183, v183 op_sel_hi:[0,0,0]
	v_mfma_scale_f32_16x16x128_f8f6f4 v[48:51], v[88:95], v[64:71], v[48:51], v183, v183 op_sel_hi:[0,0,0]
	s_mov_b32 m0, s100
	v_mfma_scale_f32_16x16x128_f8f6f4 v[36:39], v[72:79], v[80:87], v[36:39], v183, v183 op_sel_hi:[0,0,0]
	global_load_lds_dwordx4 v168, s[30:31]
	v_mfma_scale_f32_16x16x128_f8f6f4 v[32:35], v[88:95], v[80:87], v[32:35], v183, v183 op_sel_hi:[0,0,0]
	v_mfma_scale_f32_16x16x128_f8f6f4 v[20:23], v[72:79], v[96:103], v[20:23], v183, v183 op_sel_hi:[0,0,0]
	s_mov_b32 m0, s101
	v_mfma_scale_f32_16x16x128_f8f6f4 v[16:19], v[88:95], v[96:103], v[16:19], v183, v183 op_sel_hi:[0,0,0]
	global_load_lds_dwordx4 v180, s[30:31]
	v_mfma_scale_f32_16x16x128_f8f6f4 v[4:7], v[72:79], v[104:111], v[4:7], v183, v183 op_sel_hi:[0,0,0]
	v_mfma_scale_f32_16x16x128_f8f6f4 v[0:3], v[88:95], v[104:111], v[0:3], v183, v183 op_sel_hi:[0,0,0]
	s_setprio 0
	s_add_i32 s35, 0, 0x18000
	v_add_u32_e32 v24, s35, v181
	s_barrier
	ds_read_b128 v[8:11], v24
	ds_read_b128 v[12:15], v24 offset:1024
	ds_read_b128 v[128:131], v24 offset:2048
	ds_read_b128 v[132:135], v24 offset:3072
	s_add_u32 s36, s6, 0x20000
	v_mov_b32_e32 v64, v169
	ds_read_b128 v[24:27], v182 offset:32768
	ds_read_b128 v[28:31], v182 offset:33792
	ds_read_b128 v[40:43], v182 offset:34816
	ds_read_b128 v[44:47], v182 offset:35840
	ds_read_b128 v[56:59], v182 offset:36864
	ds_read_b128 v[60:63], v182 offset:37888
	ds_read_b128 v[136:139], v182 offset:38912
	ds_read_b128 v[140:143], v182 offset:39936
	s_addc_u32 s37, s7, 0
	s_nop 0
	v_mov_b32_e32 v64, v170
	s_nop 0
	s_waitcnt lgkmcnt(8)
	s_barrier
	s_waitcnt lgkmcnt(0)
	s_setprio 1
	s_waitcnt lgkmcnt(0)
	v_mfma_scale_f32_16x16x128_f8f6f4 v[120:123], v[8:15], v[24:31], v[120:123], v183, v183 op_sel_hi:[0,0,0]
	v_mfma_scale_f32_16x16x128_f8f6f4 v[124:127], v[128:135], v[24:31], v[124:127], v183, v183 op_sel_hi:[0,0,0]
	s_mov_b32 m0, s14
	v_mfma_scale_f32_16x16x128_f8f6f4 v[108:111], v[8:15], v[40:47], v[192:195], v183, v183 op_sel_hi:[0,0,0]
	global_load_lds_dwordx4 v169, s[36:37]
	v_mfma_scale_f32_16x16x128_f8f6f4 v[104:107], v[128:135], v[40:47], v[196:199], v183, v183 op_sel_hi:[0,0,0]
	v_mfma_scale_f32_16x16x128_f8f6f4 v[92:95], v[8:15], v[56:63], v[200:203], v183, v183 op_sel_hi:[0,0,0]
	s_mov_b32 m0, s15
	v_mfma_scale_f32_16x16x128_f8f6f4 v[88:91], v[128:135], v[56:63], v[204:207], v183, v183 op_sel_hi:[0,0,0]
	global_load_lds_dwordx4 v170, s[36:37]
	s_nop 5
	v_mov_b32_e32 v200, v170
	v_mfma_scale_f32_16x16x128_f8f6f4 v[76:79], v[8:15], v[136:143], v[208:211], v183, v183 op_sel_hi:[0,0,0]
	v_mfma_scale_f32_16x16x128_f8f6f4 v[72:75], v[128:135], v[136:143], v[212:215], v183, v183 op_sel_hi:[0,0,0]
	s_setprio 0
	s_barrier
	s_add_i32 s36, 0, 0x1c000
	v_add_u32_e32 v64, s36, v181
	v_mov_b32_e32 v170, v168
	ds_read_b128 v[144:147], v64
	ds_read_b128 v[148:151], v64 offset:1024
	ds_read_b128 v[152:155], v64 offset:2048
	ds_read_b128 v[156:159], v64 offset:3072
	s_add_i32 s35, s35, s33
	v_lshl_add_u64 v[64:65], s[8:9], 0, v[170:171]
	v_lshl_add_u64 v[64:65], v[64:65], 0, s[62:63]
	v_mov_b32_e32 v170, v180
	v_lshl_add_u64 v[64:65], s[8:9], 0, v[170:171]
	v_lshl_add_u64 v[64:65], v[64:65], 0, s[62:63]
	s_barrier
	s_waitcnt lgkmcnt(0)
	s_setprio 1
	s_waitcnt lgkmcnt(0)
	v_mfma_scale_f32_16x16x128_f8f6f4 v[116:119], v[144:151], v[24:31], v[116:119], v183, v183 op_sel_hi:[0,0,0]
	v_mfma_scale_f32_16x16x128_f8f6f4 v[112:115], v[152:159], v[24:31], v[112:115], v183, v183 op_sel_hi:[0,0,0]
	s_add_u32 s98, s8, s62
	s_addc_u32 s99, s9, s63
	s_mov_b32 m0, s35
	v_mfma_scale_f32_16x16x128_f8f6f4 v[100:103], v[144:151], v[40:47], v[216:219], v183, v183 op_sel_hi:[0,0,0]
	global_load_lds_dwordx4 v168, s[98:99]
	v_mfma_scale_f32_16x16x128_f8f6f4 v[96:99], v[152:159], v[40:47], v[220:223], v183, v183 op_sel_hi:[0,0,0]
	s_nop 5
	v_mov_b32_e32 v216, v168
	v_mfma_scale_f32_16x16x128_f8f6f4 v[84:87], v[144:151], v[56:63], v[224:227], v183, v183 op_sel_hi:[0,0,0]
	s_add_i32 m0, s35, 0x2000
	v_mfma_scale_f32_16x16x128_f8f6f4 v[80:83], v[152:159], v[56:63], v[160:163], v183, v183 op_sel_hi:[0,0,0]
	global_load_lds_dwordx4 v180, s[98:99]
	v_mfma_scale_f32_16x16x128_f8f6f4 v[68:71], v[144:151], v[136:143], v[164:167], v183, v183 op_sel_hi:[0,0,0]
	v_mfma_scale_f32_16x16x128_f8f6f4 v[64:67], v[152:159], v[136:143], v[184:187], v183, v183 op_sel_hi:[0,0,0]
	s_setprio 0
	v_mov_b32_e32 v170, v169
	s_barrier
	ds_read_b128 v[136:139], v182 offset:49152
	ds_read_b128 v[140:143], v182 offset:50176
	ds_read_b128 v[160:163], v182 offset:51200
	ds_read_b128 v[164:167], v182 offset:52224
	ds_read_b128 v[184:187], v182 offset:53248
	ds_read_b128 v[188:191], v182 offset:54272
	ds_read_b128 v[192:195], v182 offset:55296
	ds_read_b128 v[196:199], v182 offset:56320
	v_lshl_add_u64 v[24:25], s[6:7], 0, v[170:171]
	v_lshl_add_u64 v[24:25], v[24:25], 0, s[62:63]
	v_mov_b32_e32 v170, v200
	v_lshl_add_u64 v[24:25], s[6:7], 0, v[170:171]
	v_lshl_add_u64 v[24:25], v[24:25], 0, s[62:63]
	s_barrier
	s_waitcnt lgkmcnt(0)
	s_setprio 1
	s_waitcnt lgkmcnt(0)
	v_mfma_scale_f32_16x16x128_f8f6f4 v[60:63], v[8:15], v[136:143], v[228:231], v183, v183 op_sel_hi:[0,0,0]
	v_mfma_scale_f32_16x16x128_f8f6f4 v[56:59], v[128:135], v[136:143], v[232:235], v183, v183 op_sel_hi:[0,0,0]
	s_add_u32 s98, s6, s62
	s_addc_u32 s99, s7, s63
	s_mov_b32 m0, s16
	v_mfma_scale_f32_16x16x128_f8f6f4 v[44:47], v[8:15], v[160:167], v[236:239], v183, v183 op_sel_hi:[0,0,0]
	global_load_lds_dwordx4 v169, s[98:99]
	v_mfma_scale_f32_16x16x128_f8f6f4 v[40:43], v[128:135], v[160:167], v[240:243], v183, v183 op_sel_hi:[0,0,0]
	v_mfma_scale_f32_16x16x128_f8f6f4 v[28:31], v[8:15], v[184:191], v[244:247], v183, v183 op_sel_hi:[0,0,0]
	s_mov_b32 m0, s17
	v_mfma_scale_f32_16x16x128_f8f6f4 v[24:27], v[128:135], v[184:191], v[248:251], v183, v183 op_sel_hi:[0,0,0]
	global_load_lds_dwordx4 v200, s[98:99]
	v_mfma_scale_f32_16x16x128_f8f6f4 v[12:15], v[8:15], v[192:199], v[172:175], v183, v183 op_sel_hi:[0,0,0]
	v_mfma_scale_f32_16x16x128_f8f6f4 v[8:11], v[128:135], v[192:199], v[176:179], v183, v183 op_sel_hi:[0,0,0]
	s_setprio 0
	s_barrier
	v_mov_b32_e32 v170, v168
	s_add_i32 s6, s36, s33
	v_lshl_add_u64 v[128:129], s[30:31], 0, v[170:171]
	v_lshl_add_u64 v[128:129], v[128:129], 0, s[62:63]
	s_mov_b32 s100, s6
	v_mov_b32_e32 v170, v180
	s_add_i32 s101, s6, 0x2000
	v_lshl_add_u64 v[128:129], s[30:31], 0, v[170:171]
	v_lshl_add_u64 v[128:129], v[128:129], 0, s[62:63]
	s_waitcnt vmcnt(4)
	s_barrier
	s_setprio 1
	v_mfma_scale_f32_16x16x128_f8f6f4 v[52:55], v[144:151], v[136:143], v[52:55], v183, v183 op_sel_hi:[0,0,0]
	v_mfma_scale_f32_16x16x128_f8f6f4 v[48:51], v[152:159], v[136:143], v[48:51], v183, v183 op_sel_hi:[0,0,0]
	s_add_u32 s98, s30, s62
	s_addc_u32 s99, s31, s63
	s_mov_b32 m0, s100
	v_mfma_scale_f32_16x16x128_f8f6f4 v[36:39], v[144:151], v[160:167], v[36:39], v183, v183 op_sel_hi:[0,0,0]
	global_load_lds_dwordx4 v168, s[98:99]
	v_mfma_scale_f32_16x16x128_f8f6f4 v[32:35], v[152:159], v[160:167], v[32:35], v183, v183 op_sel_hi:[0,0,0]
	v_mfma_scale_f32_16x16x128_f8f6f4 v[20:23], v[144:151], v[184:191], v[20:23], v183, v183 op_sel_hi:[0,0,0]
	s_mov_b32 m0, s101
	v_mfma_scale_f32_16x16x128_f8f6f4 v[16:19], v[152:159], v[184:191], v[16:19], v183, v183 op_sel_hi:[0,0,0]
	global_load_lds_dwordx4 v180, s[98:99]
	v_mfma_scale_f32_16x16x128_f8f6f4 v[4:7], v[144:151], v[192:199], v[4:7], v183, v183 op_sel_hi:[0,0,0]
	v_mfma_scale_f32_16x16x128_f8f6f4 v[0:3], v[152:159], v[192:199], v[0:3], v183, v183 op_sel_hi:[0,0,0]
	s_setprio 0
	s_add_u32 s4, s4, 0x100
	s_addc_u32 s5, s5, 0
	s_add_u32 s25, s25, 0x100
	s_addc_u32 s27, s27, 0
	s_cmp_ge_i32 s34, s13
	s_mov_b32 s6, s34
	s_barrier
	s_cbranch_scc0 .LBB0_4066

.LBB0_4932:
	ds_read_b128 v[146:149], v141
	ds_read_b128 v[150:153], v141 offset:1024
	ds_read_b128 v[154:157], v141 offset:2048
	ds_read_b128 v[158:161], v141 offset:3072
	s_add_u32 s22, s20, 0xfffc0080
	s_addc_u32 s23, s21, -1
	s_cmp_eq_u32 s50, 12
	s_cselect_b32 s25, s15, s23
	s_cselect_b32 s24, s14, s22
	s_cselect_b32 s23, s17, s13
	s_cselect_b32 s22, s16, s11
	v_mov_b32_e32 v128, v138
	ds_read_b128 v[162:165], v142
	ds_read_b128 v[166:169], v142 offset:1024
	ds_read_b128 v[170:173], v142 offset:2048
	ds_read_b128 v[174:177], v142 offset:3072
	ds_read_b128 v[178:181], v142 offset:4096
	ds_read_b128 v[182:185], v142 offset:5120
	ds_read_b128 v[186:189], v142 offset:6144
	ds_read_b128 v[190:193], v142 offset:7168
	s_nop 0
	v_mov_b32_e32 v128, v139
	s_nop 0
	s_waitcnt lgkmcnt(8)
	s_barrier
	s_waitcnt lgkmcnt(0)
	s_setprio 1
	s_waitcnt lgkmcnt(0)
	v_mfma_scale_f32_16x16x128_f8f6f4 v[124:127], v[146:153], v[162:169], v[124:127], v143, v143 op_sel_hi:[0,0,0]
	v_mfma_scale_f32_16x16x128_f8f6f4 v[120:123], v[154:161], v[162:169], v[120:123], v143, v143 op_sel_hi:[0,0,0]
	s_add_i32 m0, s19, 0xc000
	v_mfma_scale_f32_16x16x128_f8f6f4 v[116:119], v[146:153], v[170:177], v[116:119], v143, v143 op_sel_hi:[0,0,0]
	global_load_lds_dwordx4 v138, s[20:21]
	v_mfma_scale_f32_16x16x128_f8f6f4 v[112:115], v[154:161], v[170:177], v[112:115], v143, v143 op_sel_hi:[0,0,0]
	v_mfma_scale_f32_16x16x128_f8f6f4 v[132:135], v[146:153], v[178:185], v[108:111], v143, v143 op_sel_hi:[0,0,0]
	s_add_i32 m0, s19, 0xe000
	v_mfma_scale_f32_16x16x128_f8f6f4 v[194:197], v[154:161], v[178:185], v[104:107], v143, v143 op_sel_hi:[0,0,0]
	global_load_lds_dwordx4 v139, s[20:21]
	v_mfma_scale_f32_16x16x128_f8f6f4 v[198:201], v[146:153], v[186:193], v[100:103], v143, v143 op_sel_hi:[0,0,0]
	v_mfma_scale_f32_16x16x128_f8f6f4 v[202:205], v[154:161], v[186:193], v[96:99], v143, v143 op_sel_hi:[0,0,0]
	s_setprio 0
	s_barrier
	v_mov_b32_e32 v128, v138
	s_add_i32 s51, s44, s28
	s_nop 2
	ds_read_b128 v[96:99], v144
	ds_read_b128 v[100:103], v144 offset:1024
	ds_read_b128 v[104:107], v144 offset:2048
	ds_read_b128 v[108:111], v144 offset:3072
	s_nop 0
	v_mov_b32_e32 v128, v139
	s_nop 0
	s_barrier
	s_waitcnt lgkmcnt(0)
	s_setprio 1
	s_waitcnt lgkmcnt(0)
	v_mfma_scale_f32_16x16x128_f8f6f4 v[206:209], v[96:103], v[162:169], v[60:63], v143, v143 op_sel_hi:[0,0,0]
	v_mfma_scale_f32_16x16x128_f8f6f4 v[162:165], v[104:111], v[162:169], v[56:59], v143, v143 op_sel_hi:[0,0,0]
	s_mov_b32 m0, s51
	v_mfma_scale_f32_16x16x128_f8f6f4 v[166:169], v[96:103], v[170:177], v[52:55], v143, v143 op_sel_hi:[0,0,0]
	global_load_lds_dwordx4 v138, s[22:23]
	v_mfma_scale_f32_16x16x128_f8f6f4 v[170:173], v[104:111], v[170:177], v[48:51], v143, v143 op_sel_hi:[0,0,0]
	v_mfma_scale_f32_16x16x128_f8f6f4 v[174:177], v[96:103], v[178:185], v[44:47], v143, v143 op_sel_hi:[0,0,0]
	s_add_i32 m0, s51, 0x2000
	v_mfma_scale_f32_16x16x128_f8f6f4 v[178:181], v[104:111], v[178:185], v[40:43], v143, v143 op_sel_hi:[0,0,0]
	global_load_lds_dwordx4 v139, s[22:23]
	v_mfma_scale_f32_16x16x128_f8f6f4 v[182:185], v[96:103], v[186:193], v[36:39], v143, v143 op_sel_hi:[0,0,0]
	v_mfma_scale_f32_16x16x128_f8f6f4 v[186:189], v[104:111], v[186:193], v[32:35], v143, v143 op_sel_hi:[0,0,0]
	s_setprio 0
	v_mov_b32_e32 v128, v138
	s_barrier
	s_nop 2
	ds_read_b128 v[32:35], v142 offset:16384
	ds_read_b128 v[36:39], v142 offset:17408
	ds_read_b128 v[40:43], v142 offset:18432
	ds_read_b128 v[44:47], v142 offset:19456
	ds_read_b128 v[48:51], v142 offset:20480
	ds_read_b128 v[52:55], v142 offset:21504
	ds_read_b128 v[56:59], v142 offset:22528
	ds_read_b128 v[60:63], v142 offset:23552
	s_nop 0
	v_mov_b32_e32 v128, v139
	s_nop 0
	s_barrier
	s_waitcnt lgkmcnt(0)
	s_setprio 1
	s_waitcnt lgkmcnt(0)
	v_mfma_scale_f32_16x16x128_f8f6f4 v[92:95], v[146:153], v[32:39], v[92:95], v143, v143 op_sel_hi:[0,0,0]
	v_mfma_scale_f32_16x16x128_f8f6f4 v[88:91], v[154:161], v[32:39], v[88:91], v143, v143 op_sel_hi:[0,0,0]
	s_mov_b32 m0, s19
	v_mfma_scale_f32_16x16x128_f8f6f4 v[84:87], v[146:153], v[40:47], v[84:87], v143, v143 op_sel_hi:[0,0,0]
	global_load_lds_dwordx4 v138, s[24:25]
	v_mfma_scale_f32_16x16x128_f8f6f4 v[80:83], v[154:161], v[40:47], v[80:83], v143, v143 op_sel_hi:[0,0,0]
	v_mfma_scale_f32_16x16x128_f8f6f4 v[76:79], v[146:153], v[48:55], v[76:79], v143, v143 op_sel_hi:[0,0,0]
	s_mov_b32 m0, s29
	v_mfma_scale_f32_16x16x128_f8f6f4 v[72:75], v[154:161], v[48:55], v[72:75], v143, v143 op_sel_hi:[0,0,0]
	global_load_lds_dwordx4 v139, s[24:25]
	v_mfma_scale_f32_16x16x128_f8f6f4 v[190:193], v[146:153], v[56:63], v[68:71], v143, v143 op_sel_hi:[0,0,0]
	v_mfma_scale_f32_16x16x128_f8f6f4 v[210:213], v[154:161], v[56:63], v[64:67], v143, v143 op_sel_hi:[0,0,0]
	s_setprio 0
	s_barrier
	s_add_u32 s52, s22, 0x40000
	s_addc_u32 s53, s23, 0
	s_nop 2
	v_mov_b32_e32 v64, v138
	s_add_i32 s51, s45, s28
	s_mov_b32 s100, s51
	s_nop 0
	v_mov_b32_e32 v64, v139
	s_add_i32 s101, s51, 0x2000
	s_nop 0
	s_waitcnt vmcnt(4)
	s_barrier
	s_setprio 1
	v_mfma_scale_f32_16x16x128_f8f6f4 v[214:217], v[96:103], v[32:39], v[28:31], v143, v143 op_sel_hi:[0,0,0]
	v_mfma_scale_f32_16x16x128_f8f6f4 v[218:221], v[104:111], v[32:39], v[24:27], v143, v143 op_sel_hi:[0,0,0]
	s_mov_b32 m0, s100
	v_mfma_scale_f32_16x16x128_f8f6f4 v[222:225], v[96:103], v[40:47], v[20:23], v143, v143 op_sel_hi:[0,0,0]
	global_load_lds_dwordx4 v138, s[52:53]
	v_mfma_scale_f32_16x16x128_f8f6f4 v[226:229], v[104:111], v[40:47], v[16:19], v143, v143 op_sel_hi:[0,0,0]
	v_mfma_scale_f32_16x16x128_f8f6f4 v[230:233], v[96:103], v[48:55], v[12:15], v143, v143 op_sel_hi:[0,0,0]
	s_mov_b32 m0, s101
	v_mfma_scale_f32_16x16x128_f8f6f4 v[234:237], v[104:111], v[48:55], v[8:11], v143, v143 op_sel_hi:[0,0,0]
	global_load_lds_dwordx4 v139, s[52:53]
	v_mfma_scale_f32_16x16x128_f8f6f4 v[238:241], v[96:103], v[56:63], v[4:7], v143, v143 op_sel_hi:[0,0,0]
	v_mfma_scale_f32_16x16x128_f8f6f4 v[242:245], v[104:111], v[56:63], v[0:3], v143, v143 op_sel_hi:[0,0,0]
	s_setprio 0
	s_add_i32 s51, 0, 0x18000
	s_nop 1
	v_add_u32_e32 v12, s51, v140
	s_barrier
	s_nop 0
	ds_read_b128 v[0:3], v12
	ds_read_b128 v[4:7], v12 offset:1024
	ds_read_b128 v[8:11], v12 offset:2048
	ds_read_b128 v[12:15], v12 offset:3072
	s_add_u32 s52, s24, 0x40000
	v_mov_b32_e32 v40, v138
	ds_read_b128 v[16:19], v142 offset:32768
	ds_read_b128 v[20:23], v142 offset:33792
	ds_read_b128 v[24:27], v142 offset:34816
	ds_read_b128 v[28:31], v142 offset:35840
	ds_read_b128 v[32:35], v142 offset:36864
	ds_read_b128 v[36:39], v142 offset:37888
	ds_read_b128 v[64:67], v142 offset:38912
	ds_read_b128 v[68:71], v142 offset:39936
	s_addc_u32 s53, s25, 0
	s_nop 0
	v_mov_b32_e32 v40, v139
	s_nop 0
	s_waitcnt lgkmcnt(8)
	s_barrier
	s_waitcnt lgkmcnt(0)
	s_setprio 1
	s_waitcnt lgkmcnt(0)
	v_mfma_scale_f32_16x16x128_f8f6f4 v[124:127], v[0:7], v[16:23], v[124:127], v143, v143 op_sel_hi:[0,0,0]
	v_mfma_scale_f32_16x16x128_f8f6f4 v[120:123], v[8:15], v[16:23], v[120:123], v143, v143 op_sel_hi:[0,0,0]
	s_mov_b32 m0, s30
	v_mfma_scale_f32_16x16x128_f8f6f4 v[116:119], v[0:7], v[24:31], v[116:119], v143, v143 op_sel_hi:[0,0,0]
	global_load_lds_dwordx4 v138, s[52:53]
	v_mfma_scale_f32_16x16x128_f8f6f4 v[112:115], v[8:15], v[24:31], v[112:115], v143, v143 op_sel_hi:[0,0,0]
	v_mfma_scale_f32_16x16x128_f8f6f4 v[108:111], v[0:7], v[32:39], v[132:135], v143, v143 op_sel_hi:[0,0,0]
	s_mov_b32 m0, s31
	v_mfma_scale_f32_16x16x128_f8f6f4 v[104:107], v[8:15], v[32:39], v[194:197], v143, v143 op_sel_hi:[0,0,0]
	global_load_lds_dwordx4 v139, s[52:53]
	v_mfma_scale_f32_16x16x128_f8f6f4 v[100:103], v[0:7], v[64:71], v[198:201], v143, v143 op_sel_hi:[0,0,0]
	v_mfma_scale_f32_16x16x128_f8f6f4 v[96:99], v[8:15], v[64:71], v[202:205], v143, v143 op_sel_hi:[0,0,0]
	s_setprio 0
	s_barrier
	s_add_i32 s52, 0, 0x1c000
	v_add_u32_e32 v40, s52, v140
	v_mov_b32_e32 v128, v138
	ds_read_b128 v[146:149], v40
	ds_read_b128 v[150:153], v40 offset:1024
	ds_read_b128 v[154:157], v40 offset:2048
	ds_read_b128 v[158:161], v40 offset:3072
	s_add_i32 s51, s51, s28
	v_lshl_add_u64 v[40:41], s[22:23], 0, v[128:129]
	v_lshl_add_u64 v[40:41], v[40:41], 0, s[6:7]
	v_mov_b32_e32 v128, v139
	v_lshl_add_u64 v[40:41], s[22:23], 0, v[128:129]
	v_lshl_add_u64 v[40:41], v[40:41], 0, s[6:7]
	s_barrier
	s_waitcnt lgkmcnt(0)
	s_setprio 1
	s_waitcnt lgkmcnt(0)
	v_mfma_scale_f32_16x16x128_f8f6f4 v[60:63], v[146:153], v[16:23], v[206:209], v143, v143 op_sel_hi:[0,0,0]
	v_mfma_scale_f32_16x16x128_f8f6f4 v[56:59], v[154:161], v[16:23], v[162:165], v143, v143 op_sel_hi:[0,0,0]
	s_add_u32 s98, s22, s6
	s_addc_u32 s99, s23, s7
	s_mov_b32 m0, s51
	v_mfma_scale_f32_16x16x128_f8f6f4 v[52:55], v[146:153], v[24:31], v[166:169], v143, v143 op_sel_hi:[0,0,0]
	global_load_lds_dwordx4 v138, s[98:99]
	v_mfma_scale_f32_16x16x128_f8f6f4 v[48:51], v[154:161], v[24:31], v[170:173], v143, v143 op_sel_hi:[0,0,0]
	v_mfma_scale_f32_16x16x128_f8f6f4 v[44:47], v[146:153], v[32:39], v[174:177], v143, v143 op_sel_hi:[0,0,0]
	s_add_i32 m0, s51, 0x2000
	v_mfma_scale_f32_16x16x128_f8f6f4 v[40:43], v[154:161], v[32:39], v[178:181], v143, v143 op_sel_hi:[0,0,0]
	global_load_lds_dwordx4 v139, s[98:99]
	v_mfma_scale_f32_16x16x128_f8f6f4 v[36:39], v[146:153], v[64:71], v[182:185], v143, v143 op_sel_hi:[0,0,0]
	v_mfma_scale_f32_16x16x128_f8f6f4 v[32:35], v[154:161], v[64:71], v[186:189], v143, v143 op_sel_hi:[0,0,0]
	s_setprio 0
	v_mov_b32_e32 v128, v138
	s_barrier
	ds_read_b128 v[16:19], v142 offset:49152
	ds_read_b128 v[20:23], v142 offset:50176
	ds_read_b128 v[162:165], v142 offset:51200
	ds_read_b128 v[166:169], v142 offset:52224
	ds_read_b128 v[170:173], v142 offset:53248
	ds_read_b128 v[174:177], v142 offset:54272
	ds_read_b128 v[178:181], v142 offset:55296
	ds_read_b128 v[182:185], v142 offset:56320
	v_lshl_add_u64 v[24:25], s[24:25], 0, v[128:129]
	v_lshl_add_u64 v[24:25], v[24:25], 0, s[6:7]
	v_mov_b32_e32 v128, v139
	v_lshl_add_u64 v[24:25], s[24:25], 0, v[128:129]
	v_lshl_add_u64 v[24:25], v[24:25], 0, s[6:7]
	s_barrier
	s_waitcnt lgkmcnt(0)
	s_setprio 1
	s_waitcnt lgkmcnt(0)
	v_mfma_scale_f32_16x16x128_f8f6f4 v[92:95], v[0:7], v[16:23], v[92:95], v143, v143 op_sel_hi:[0,0,0]
	v_mfma_scale_f32_16x16x128_f8f6f4 v[88:91], v[8:15], v[16:23], v[88:91], v143, v143 op_sel_hi:[0,0,0]
	s_add_u32 s98, s24, s6
	s_addc_u32 s99, s25, s7
	s_mov_b32 m0, s41
	v_mfma_scale_f32_16x16x128_f8f6f4 v[84:87], v[0:7], v[162:169], v[84:87], v143, v143 op_sel_hi:[0,0,0]
	global_load_lds_dwordx4 v138, s[98:99]
	v_mfma_scale_f32_16x16x128_f8f6f4 v[80:83], v[8:15], v[162:169], v[80:83], v143, v143 op_sel_hi:[0,0,0]
	v_mfma_scale_f32_16x16x128_f8f6f4 v[76:79], v[0:7], v[170:177], v[76:79], v143, v143 op_sel_hi:[0,0,0]
	s_mov_b32 m0, s42
	v_mfma_scale_f32_16x16x128_f8f6f4 v[72:75], v[8:15], v[170:177], v[72:75], v143, v143 op_sel_hi:[0,0,0]
	global_load_lds_dwordx4 v139, s[98:99]
	v_mfma_scale_f32_16x16x128_f8f6f4 v[68:71], v[0:7], v[178:185], v[190:193], v143, v143 op_sel_hi:[0,0,0]
	v_mfma_scale_f32_16x16x128_f8f6f4 v[64:67], v[8:15], v[178:185], v[210:213], v143, v143 op_sel_hi:[0,0,0]
	s_setprio 0
	s_barrier
	s_add_u32 s22, s22, 0x40080
	s_addc_u32 s23, s23, 0
	v_mov_b32_e32 v0, v138
	s_add_i32 s24, s52, s28
	s_nop 0
	v_mov_b32_e32 v0, v139
	s_nop 0
	s_waitcnt vmcnt(4)
	s_barrier
	s_setprio 1
	v_mfma_scale_f32_16x16x128_f8f6f4 v[28:31], v[146:153], v[16:23], v[214:217], v143, v143 op_sel_hi:[0,0,0]
	v_mfma_scale_f32_16x16x128_f8f6f4 v[24:27], v[154:161], v[16:23], v[218:221], v143, v143 op_sel_hi:[0,0,0]
	s_mov_b32 m0, s24
	v_mfma_scale_f32_16x16x128_f8f6f4 v[20:23], v[146:153], v[162:169], v[222:225], v143, v143 op_sel_hi:[0,0,0]
	global_load_lds_dwordx4 v138, s[22:23]
	v_mfma_scale_f32_16x16x128_f8f6f4 v[16:19], v[154:161], v[162:169], v[226:229], v143, v143 op_sel_hi:[0,0,0]
	v_mfma_scale_f32_16x16x128_f8f6f4 v[12:15], v[146:153], v[170:177], v[230:233], v143, v143 op_sel_hi:[0,0,0]
	s_add_i32 m0, s24, 0x2000
	v_mfma_scale_f32_16x16x128_f8f6f4 v[8:11], v[154:161], v[170:177], v[234:237], v143, v143 op_sel_hi:[0,0,0]
	global_load_lds_dwordx4 v139, s[22:23]
	v_mfma_scale_f32_16x16x128_f8f6f4 v[4:7], v[146:153], v[178:185], v[238:241], v143, v143 op_sel_hi:[0,0,0]
	v_mfma_scale_f32_16x16x128_f8f6f4 v[0:3], v[154:161], v[178:185], v[242:245], v143, v143 op_sel_hi:[0,0,0]
	s_setprio 0
	s_add_i32 s50, s50, 2
	s_add_u32 s20, s20, 0x100
	s_addc_u32 s21, s21, 0
	s_add_u32 s11, s11, 0x100
	s_addc_u32 s13, s13, 0
	s_cmp_gt_u32 s50, 13
	s_barrier
	s_cbranch_scc0 .LBB0_4932
	s_ashr_i32 s11, s18, 4
	s_mul_hi_i32 s13, s11, 0xc000
	s_mul_i32 s11, s11, 0xc000
	s_add_u32 s11, s37, s11
	s_addc_u32 s13, s38, s13
	s_lshl_b32 s20, s49, 8
	s_ashr_i32 s21, s20, 31
	s_lshl_b64 s[22:23], s[20:21], 2
	s_add_u32 s11, s11, s22
	v_mbcnt_lo_u32_b32 v134, -1, 0
	v_mbcnt_hi_u32_b32 v134, -1, v134
	s_addc_u32 s13, s13, s23
	v_ashrrev_i32_e32 v135, 4, v134
	s_add_u32 s22, s11, s46
	v_lshlrev_b32_e32 v132, 2, v135
	s_addc_u32 s23, s13, 0
	v_ashrrev_i32_e32 v133, 31, v132
	v_lshl_add_u64 v[132:133], v[132:133], 2, s[22:23]
	global_load_dwordx4 v[146:149], v[132:133], off
	global_load_dwordx4 v[150:153], v[132:133], off offset:64
	v_mov_b32_e32 v164, v129
	s_lshl_b32 s11, s18, 8
	v_mov_b32_e32 v165, v129
	s_add_i32 s22, s11, s39
	s_ashr_i32 s23, s22, 31
	s_lshl_b64 s[22:23], s[22:23], 11
	s_add_u32 s11, s35, s22
	s_addc_u32 s13, s36, s23
	v_mov_b32_e32 v162, v129
	v_lshlrev_b32_e32 v135, 3, v135
	s_add_u32 s11, s11, s20
	v_mov_b32_e32 v154, v129
	v_mov_b32_e32 v155, v129
	v_mov_b32_e32 v156, v129
	v_mov_b32_e32 v157, v129
	v_and_b32_e32 v128, 16, v134
	v_bfi_b32 v134, -16, v135, v134
	s_addc_u32 s13, s13, s21
	v_mov_b32_e32 v163, v129
	v_mov_b32_e32 v158, v129
	v_mov_b32_e32 v159, v129
	v_mov_b32_e32 v160, v129
	v_mov_b32_e32 v161, v129
	v_ashrrev_i32_e32 v135, 31, v134
	s_add_u32 s20, s11, s40
	v_lshlrev_b64 v[134:135], 11, v[134:135]
	s_addc_u32 s21, s13, 0
	v_lshl_add_u64 v[134:135], s[20:21], 0, v[134:135]
	v_lshl_add_u64 v[134:135], v[134:135], 0, v[128:129]
	v_add_co_u32_e32 v136, vcc, s34, v134
	s_mov_b32 s18, s12
	s_nop 0
	v_addc_co_u32_e32 v137, vcc, 0, v135, vcc
	s_mov_b32 s49, s10
	s_mov_b64 s[22:23], s[16:17]
	s_mov_b64 s[20:21], s[14:15]
	s_waitcnt vmcnt(0)
	v_pk_mul_f32 v[146:147], v[146:147], s[8:9] op_sel_hi:[1,0]
	v_pk_mul_f32 v[150:151], v[150:151], s[8:9] op_sel_hi:[1,0]
	v_pk_mul_f32 v[84:85], v[84:85], v[146:147]
	v_pk_mul_f32 v[80:81], v[80:81], v[150:151]
	v_cvt_pk_fp8_f32 v164, v84, v85
	v_cvt_pk_fp8_f32 v165, v80, v81
	v_pk_mul_f32 v[148:149], v[148:149], s[8:9] op_sel_hi:[1,0]
	v_pk_mul_f32 v[152:153], v[152:153], s[8:9] op_sel_hi:[1,0]
	v_pk_mul_f32 v[80:81], v[86:87], v[148:149]
	v_pk_mul_f32 v[72:73], v[72:73], v[150:151]
	v_cvt_pk_fp8_f32 v164, v80, v81 op_sel:[0,0,1]
	v_pk_mul_f32 v[80:81], v[82:83], v[152:153]
	v_pk_mul_f32 v[92:93], v[92:93], v[146:147]
	v_cvt_pk_fp8_f32 v165, v80, v81 op_sel:[0,0,1]
	v_pk_mul_f32 v[80:81], v[76:77], v[146:147]
	v_mov_b32_e32 v77, v129
	v_mov_b32_e32 v76, v129
	v_cvt_pk_fp8_f32 v77, v72, v73
	v_pk_mul_f32 v[72:73], v[78:79], v[148:149]
	v_pk_mul_f32 v[68:69], v[68:69], v[146:147]
	v_mov_b32_e32 v78, v129
	v_pk_mul_f32 v[124:125], v[124:125], v[146:147]
	v_pk_mul_f32 v[120:121], v[120:121], v[150:151]
	v_pk_mul_f32 v[116:117], v[116:117], v[146:147]
	v_pk_mul_f32 v[112:113], v[112:113], v[150:151]
	v_cvt_pk_fp8_f32 v162, v92, v93
	v_pk_mul_f32 v[88:89], v[88:89], v[150:151]
	v_cvt_pk_fp8_f32 v76, v80, v81
	v_cvt_pk_fp8_f32 v78, v68, v69
	v_pk_mul_f32 v[64:65], v[64:65], v[150:151]
	v_mov_b32_e32 v79, v129
	v_pk_mul_f32 v[108:109], v[108:109], v[146:147]
	v_pk_mul_f32 v[104:105], v[104:105], v[150:151]
	v_pk_mul_f32 v[100:101], v[100:101], v[146:147]
	v_pk_mul_f32 v[96:97], v[96:97], v[150:151]
	v_cvt_pk_fp8_f32 v154, v124, v125
	v_cvt_pk_fp8_f32 v155, v120, v121
	v_cvt_pk_fp8_f32 v156, v116, v117
	v_cvt_pk_fp8_f32 v157, v112, v113
	v_cvt_pk_fp8_f32 v163, v88, v89
	v_cvt_pk_fp8_f32 v79, v64, v65
	v_cvt_pk_fp8_f32 v158, v108, v109
	v_cvt_pk_fp8_f32 v159, v104, v105
	v_cvt_pk_fp8_f32 v160, v100, v101
	v_cvt_pk_fp8_f32 v161, v96, v97
	v_pk_mul_f32 v[88:89], v[94:95], v[148:149]
	v_pk_mul_f32 v[64:65], v[70:71], v[148:149]
	v_pk_mul_f32 v[126:127], v[126:127], v[148:149]
	v_pk_mul_f32 v[122:123], v[122:123], v[152:153]
	v_pk_mul_f32 v[118:119], v[118:119], v[148:149]
	v_pk_mul_f32 v[114:115], v[114:115], v[152:153]
	v_cvt_pk_fp8_f32 v162, v88, v89 op_sel:[0,0,1]
	v_pk_mul_f32 v[88:89], v[90:91], v[152:153]
	v_cvt_pk_fp8_f32 v76, v72, v73 op_sel:[0,0,1]
	v_pk_mul_f32 v[72:73], v[74:75], v[152:153]
	v_cvt_pk_fp8_f32 v78, v64, v65 op_sel:[0,0,1]
	v_pk_mul_f32 v[64:65], v[66:67], v[152:153]
	v_pk_mul_f32 v[110:111], v[110:111], v[148:149]
	v_pk_mul_f32 v[106:107], v[106:107], v[152:153]
	v_pk_mul_f32 v[102:103], v[102:103], v[148:149]
	v_pk_mul_f32 v[98:99], v[98:99], v[152:153]
	v_cvt_pk_fp8_f32 v154, v126, v127 op_sel:[0,0,1]
	v_cvt_pk_fp8_f32 v155, v122, v123 op_sel:[0,0,1]
	v_cvt_pk_fp8_f32 v156, v118, v119 op_sel:[0,0,1]
	v_cvt_pk_fp8_f32 v157, v114, v115 op_sel:[0,0,1]
	v_cvt_pk_fp8_f32 v163, v88, v89 op_sel:[0,0,1]
	v_cvt_pk_fp8_f32 v77, v72, v73 op_sel:[0,0,1]
	v_cvt_pk_fp8_f32 v79, v64, v65 op_sel:[0,0,1]
	v_cvt_pk_fp8_f32 v158, v110, v111 op_sel:[0,0,1]
	v_cvt_pk_fp8_f32 v159, v106, v107 op_sel:[0,0,1]
	v_cvt_pk_fp8_f32 v160, v102, v103 op_sel:[0,0,1]
	v_cvt_pk_fp8_f32 v161, v98, v99 op_sel:[0,0,1]
	v_add_co_u32_e32 v80, vcc, s47, v134
	v_permlane32_swap_b32_e32 v154, v156
	s_nop 0
	v_addc_co_u32_e32 v81, vcc, 0, v135, vcc
	v_permlane32_swap_b32_e32 v155, v157
	v_permlane32_swap_b32_e32 v162, v164
	v_permlane32_swap_b32_e32 v163, v165
	v_permlane32_swap_b32_e32 v76, v78
	v_permlane32_swap_b32_e32 v77, v79
	v_add_co_u32_e32 v82, vcc, s48, v134
	v_permlane32_swap_b32_e32 v158, v160
	v_permlane32_swap_b32_e32 v159, v161
	v_permlane16_swap_b32_e32 v154, v155
	v_permlane16_swap_b32_e32 v156, v157
	v_permlane16_swap_b32_e32 v162, v163
	v_permlane16_swap_b32_e32 v164, v165
	v_permlane16_swap_b32_e32 v76, v77
	v_permlane16_swap_b32_e32 v78, v79
	v_addc_co_u32_e32 v83, vcc, 0, v135, vcc
	v_permlane16_swap_b32_e32 v158, v159
	v_permlane16_swap_b32_e32 v160, v161
	global_store_dwordx4 v[134:135], v[154:157], off
	global_store_dwordx4 v[136:137], v[158:161], off
	global_store_dwordx4 v[80:81], v[162:165], off
	global_store_dwordx4 v[82:83], v[76:79], off
	global_load_dwordx4 v[64:67], v[132:133], off offset:512
	global_load_dwordx4 v[68:71], v[132:133], off offset:576
	v_mov_b32_e32 v75, v129
	v_mov_b32_e32 v72, v129
	v_mov_b32_e32 v73, v129
	v_mov_b32_e32 v74, v129
	s_and_b64 vcc, exec, s[4:5]
	s_waitcnt vmcnt(0)
	v_pk_mul_f32 v[64:65], v[64:65], s[8:9] op_sel_hi:[1,0]
	v_pk_mul_f32 v[68:69], v[68:69], s[8:9] op_sel_hi:[1,0]
	v_pk_mul_f32 v[70:71], v[70:71], s[8:9] op_sel_hi:[1,0]
	v_pk_mul_f32 v[48:49], v[48:49], v[68:69]
	v_pk_mul_f32 v[66:67], v[66:67], s[8:9] op_sel_hi:[1,0]
	v_cvt_pk_fp8_f32 v75, v48, v49
	v_pk_mul_f32 v[48:49], v[50:51], v[70:71]
	v_pk_mul_f32 v[40:41], v[40:41], v[68:69]
	v_pk_mul_f32 v[36:37], v[36:37], v[64:65]
	v_cvt_pk_fp8_f32 v75, v48, v49 op_sel:[0,0,1]
	v_pk_mul_f32 v[48:49], v[44:45], v[64:65]
	v_mov_b32_e32 v45, v129
	v_cvt_pk_fp8_f32 v45, v40, v41
	v_pk_mul_f32 v[40:41], v[46:47], v[66:67]
	v_mov_b32_e32 v46, v129
	v_cvt_pk_fp8_f32 v46, v36, v37
	v_pk_mul_f32 v[32:33], v[32:33], v[68:69]
	v_mov_b32_e32 v47, v129
	v_cvt_pk_fp8_f32 v47, v32, v33
	v_pk_mul_f32 v[32:33], v[38:39], v[66:67]
	v_pk_mul_f32 v[24:25], v[24:25], v[68:69]
	v_cvt_pk_fp8_f32 v46, v32, v33 op_sel:[0,0,1]
	v_pk_mul_f32 v[32:33], v[34:35], v[70:71]
	v_pk_mul_f32 v[20:21], v[20:21], v[64:65]
	v_cvt_pk_fp8_f32 v47, v32, v33 op_sel:[0,0,1]
	v_pk_mul_f32 v[32:33], v[28:29], v[64:65]
	v_mov_b32_e32 v29, v129
	v_cvt_pk_fp8_f32 v29, v24, v25
	v_pk_mul_f32 v[24:25], v[30:31], v[66:67]
	v_mov_b32_e32 v30, v129
	v_cvt_pk_fp8_f32 v30, v20, v21
	v_pk_mul_f32 v[16:17], v[16:17], v[68:69]
	v_mov_b32_e32 v31, v129
	v_cvt_pk_fp8_f32 v31, v16, v17
	v_pk_mul_f32 v[16:17], v[22:23], v[66:67]
	v_mov_b32_e32 v28, v129
	v_cvt_pk_fp8_f32 v30, v16, v17 op_sel:[0,0,1]
	v_pk_mul_f32 v[16:17], v[18:19], v[70:71]
	v_pk_mul_f32 v[8:9], v[8:9], v[68:69]
	v_cvt_pk_fp8_f32 v31, v16, v17 op_sel:[0,0,1]
	v_pk_mul_f32 v[16:17], v[12:13], v[64:65]
	v_mov_b32_e32 v13, v129
	v_pk_mul_f32 v[60:61], v[60:61], v[64:65]
	v_pk_mul_f32 v[56:57], v[56:57], v[68:69]
	v_pk_mul_f32 v[52:53], v[52:53], v[64:65]
	v_mov_b32_e32 v44, v129
	v_cvt_pk_fp8_f32 v28, v32, v33
	v_mov_b32_e32 v12, v129
	v_cvt_pk_fp8_f32 v13, v8, v9
	v_pk_mul_f32 v[8:9], v[14:15], v[66:67]
	v_pk_mul_f32 v[4:5], v[4:5], v[64:65]
	v_mov_b32_e32 v14, v129
	v_cvt_pk_fp8_f32 v72, v60, v61
	v_cvt_pk_fp8_f32 v73, v56, v57
	v_cvt_pk_fp8_f32 v74, v52, v53
	v_cvt_pk_fp8_f32 v44, v48, v49
	v_cvt_pk_fp8_f32 v12, v16, v17
	v_cvt_pk_fp8_f32 v14, v4, v5
	v_pk_mul_f32 v[0:1], v[0:1], v[68:69]
	v_mov_b32_e32 v15, v129
	v_cvt_pk_fp8_f32 v15, v0, v1
	v_pk_mul_f32 v[62:63], v[62:63], v[66:67]
	v_pk_mul_f32 v[58:59], v[58:59], v[70:71]
	v_pk_mul_f32 v[54:55], v[54:55], v[66:67]
	v_cvt_pk_fp8_f32 v28, v24, v25 op_sel:[0,0,1]
	v_pk_mul_f32 v[24:25], v[26:27], v[70:71]
	v_pk_mul_f32 v[0:1], v[6:7], v[66:67]
	v_cvt_pk_fp8_f32 v72, v62, v63 op_sel:[0,0,1]
	v_cvt_pk_fp8_f32 v73, v58, v59 op_sel:[0,0,1]
	v_cvt_pk_fp8_f32 v74, v54, v55 op_sel:[0,0,1]
	v_cvt_pk_fp8_f32 v44, v40, v41 op_sel:[0,0,1]
	v_pk_mul_f32 v[40:41], v[42:43], v[70:71]
	v_cvt_pk_fp8_f32 v29, v24, v25 op_sel:[0,0,1]
	v_cvt_pk_fp8_f32 v12, v8, v9 op_sel:[0,0,1]
	v_pk_mul_f32 v[8:9], v[10:11], v[70:71]
	v_cvt_pk_fp8_f32 v14, v0, v1 op_sel:[0,0,1]
	v_pk_mul_f32 v[0:1], v[2:3], v[70:71]
	v_cvt_pk_fp8_f32 v45, v40, v41 op_sel:[0,0,1]
	v_cvt_pk_fp8_f32 v13, v8, v9 op_sel:[0,0,1]
	v_cvt_pk_fp8_f32 v15, v0, v1 op_sel:[0,0,1]
	v_permlane32_swap_b32_e32 v72, v74
	v_permlane32_swap_b32_e32 v73, v75
	v_permlane32_swap_b32_e32 v28, v30
	v_permlane32_swap_b32_e32 v29, v31
	v_permlane16_swap_b32_e32 v72, v73
	v_permlane16_swap_b32_e32 v74, v75
	v_permlane32_swap_b32_e32 v44, v46
	v_permlane32_swap_b32_e32 v45, v47
	v_permlane16_swap_b32_e32 v28, v29
	v_permlane16_swap_b32_e32 v30, v31
	v_permlane32_swap_b32_e32 v12, v14
	v_permlane32_swap_b32_e32 v13, v15
	v_permlane16_swap_b32_e32 v44, v45
	v_permlane16_swap_b32_e32 v46, v47
	global_store_dwordx4 v[134:135], v[72:75], off offset:128
	global_store_dwordx4 v[136:137], v[44:47], off offset:128
	v_permlane16_swap_b32_e32 v12, v13
	v_permlane16_swap_b32_e32 v14, v15
	global_store_dwordx4 v[80:81], v[28:31], off offset:128
	global_store_dwordx4 v[82:83], v[12:15], off offset:128
	s_cbranch_vccz .LBB0_4925
	s_waitcnt vmcnt(0)
	v_readlane_b32 s0, v252, 2
	s_cmpk_gt_u32 s0, 0xff
	s_cbranch_scc1 .LBB0_4936
	s_barrier

.LBB0_5813:
	ds_read_b128 v[140:143], v134
	ds_read_b128 v[144:147], v134 offset:1024
	ds_read_b128 v[148:151], v134 offset:2048
	ds_read_b128 v[152:155], v134 offset:3072
	s_add_u32 s16, s14, 0xfffd0080
	s_addc_u32 s17, s15, -1
	s_cmp_eq_u32 s53, 8
	s_cselect_b32 s19, s13, s17
	s_cselect_b32 s18, s12, s16
	s_cselect_b32 s17, s11, s52
	s_cselect_b32 s16, s10, s51
	v_mov_b32_e32 v128, v132
	ds_read_b128 v[156:159], v135
	ds_read_b128 v[160:163], v135 offset:1024
	ds_read_b128 v[164:167], v135 offset:2048
	ds_read_b128 v[168:171], v135 offset:3072
	ds_read_b128 v[172:175], v135 offset:4096
	ds_read_b128 v[176:179], v135 offset:5120
	ds_read_b128 v[180:183], v135 offset:6144
	ds_read_b128 v[184:187], v135 offset:7168
	s_nop 0
	v_mov_b32_e32 v128, v133
	s_nop 0
	s_waitcnt lgkmcnt(8)
	s_barrier
	s_waitcnt lgkmcnt(0)
	s_setprio 1
	s_waitcnt lgkmcnt(0)
	v_mfma_scale_f32_16x16x128_f8f6f4 v[124:127], v[140:147], v[156:163], v[124:127], v136, v136 op_sel_hi:[0,0,0]
	v_mfma_scale_f32_16x16x128_f8f6f4 v[120:123], v[148:155], v[156:163], v[120:123], v136, v136 op_sel_hi:[0,0,0]
	s_mov_b32 m0, s38
	v_mfma_scale_f32_16x16x128_f8f6f4 v[116:119], v[140:147], v[164:171], v[116:119], v136, v136 op_sel_hi:[0,0,0]
	global_load_lds_dwordx4 v132, s[14:15]
	v_mfma_scale_f32_16x16x128_f8f6f4 v[112:115], v[148:155], v[164:171], v[112:115], v136, v136 op_sel_hi:[0,0,0]
	v_mfma_scale_f32_16x16x128_f8f6f4 v[188:191], v[140:147], v[172:179], v[108:111], v136, v136 op_sel_hi:[0,0,0]
	s_mov_b32 m0, s39
	v_mfma_scale_f32_16x16x128_f8f6f4 v[192:195], v[148:155], v[172:179], v[104:107], v136, v136 op_sel_hi:[0,0,0]
	global_load_lds_dwordx4 v133, s[14:15]
	v_mfma_scale_f32_16x16x128_f8f6f4 v[196:199], v[140:147], v[180:187], v[100:103], v136, v136 op_sel_hi:[0,0,0]
	v_mfma_scale_f32_16x16x128_f8f6f4 v[200:203], v[148:155], v[180:187], v[96:99], v136, v136 op_sel_hi:[0,0,0]
	s_setprio 0
	s_barrier
	v_mov_b32_e32 v128, v132
	s_nop 2
	ds_read_b128 v[96:99], v137
	ds_read_b128 v[100:103], v137 offset:1024
	ds_read_b128 v[104:107], v137 offset:2048
	ds_read_b128 v[108:111], v137 offset:3072
	s_nop 0
	v_mov_b32_e32 v128, v133
	s_nop 0
	s_barrier
	s_waitcnt lgkmcnt(0)
	s_setprio 1
	s_waitcnt lgkmcnt(0)
	v_mfma_scale_f32_16x16x128_f8f6f4 v[204:207], v[96:103], v[156:163], v[92:95], v136, v136 op_sel_hi:[0,0,0]
	v_mfma_scale_f32_16x16x128_f8f6f4 v[156:159], v[104:111], v[156:163], v[88:91], v136, v136 op_sel_hi:[0,0,0]
	s_mov_b32 m0, s40
	v_mfma_scale_f32_16x16x128_f8f6f4 v[160:163], v[96:103], v[164:171], v[84:87], v136, v136 op_sel_hi:[0,0,0]
	global_load_lds_dwordx4 v132, s[16:17]
	v_mfma_scale_f32_16x16x128_f8f6f4 v[164:167], v[104:111], v[164:171], v[80:83], v136, v136 op_sel_hi:[0,0,0]
	v_mfma_scale_f32_16x16x128_f8f6f4 v[168:171], v[96:103], v[172:179], v[76:79], v136, v136 op_sel_hi:[0,0,0]
	s_mov_b32 m0, s41
	v_mfma_scale_f32_16x16x128_f8f6f4 v[172:175], v[104:111], v[172:179], v[72:75], v136, v136 op_sel_hi:[0,0,0]
	global_load_lds_dwordx4 v133, s[16:17]
	v_mfma_scale_f32_16x16x128_f8f6f4 v[176:179], v[96:103], v[180:187], v[68:71], v136, v136 op_sel_hi:[0,0,0]
	v_mfma_scale_f32_16x16x128_f8f6f4 v[180:183], v[104:111], v[180:187], v[64:67], v136, v136 op_sel_hi:[0,0,0]
	s_setprio 0
	v_mov_b32_e32 v128, v132
	s_barrier
	s_nop 2
	ds_read_b128 v[64:67], v135 offset:16384
	ds_read_b128 v[68:71], v135 offset:17408
	ds_read_b128 v[72:75], v135 offset:18432
	ds_read_b128 v[76:79], v135 offset:19456
	ds_read_b128 v[80:83], v135 offset:20480
	ds_read_b128 v[84:87], v135 offset:21504
	ds_read_b128 v[88:91], v135 offset:22528
	ds_read_b128 v[92:95], v135 offset:23552
	s_nop 0
	v_mov_b32_e32 v128, v133
	s_nop 0
	s_barrier
	s_waitcnt lgkmcnt(0)
	s_setprio 1
	s_waitcnt lgkmcnt(0)
	v_mfma_scale_f32_16x16x128_f8f6f4 v[60:63], v[140:147], v[64:71], v[60:63], v136, v136 op_sel_hi:[0,0,0]
	v_mfma_scale_f32_16x16x128_f8f6f4 v[56:59], v[148:155], v[64:71], v[56:59], v136, v136 op_sel_hi:[0,0,0]
	s_mov_b32 m0, s24
	v_mfma_scale_f32_16x16x128_f8f6f4 v[52:55], v[140:147], v[72:79], v[52:55], v136, v136 op_sel_hi:[0,0,0]
	global_load_lds_dwordx4 v132, s[18:19]
	v_mfma_scale_f32_16x16x128_f8f6f4 v[48:51], v[148:155], v[72:79], v[48:51], v136, v136 op_sel_hi:[0,0,0]
	v_mfma_scale_f32_16x16x128_f8f6f4 v[184:187], v[140:147], v[80:87], v[44:47], v136, v136 op_sel_hi:[0,0,0]
	s_mov_b32 m0, s25
	v_mfma_scale_f32_16x16x128_f8f6f4 v[208:211], v[148:155], v[80:87], v[40:43], v136, v136 op_sel_hi:[0,0,0]
	global_load_lds_dwordx4 v133, s[18:19]
	v_mfma_scale_f32_16x16x128_f8f6f4 v[212:215], v[140:147], v[88:95], v[36:39], v136, v136 op_sel_hi:[0,0,0]
	v_mfma_scale_f32_16x16x128_f8f6f4 v[216:219], v[148:155], v[88:95], v[32:35], v136, v136 op_sel_hi:[0,0,0]
	s_setprio 0
	s_barrier
	s_add_u32 s54, s16, 0x30000
	s_nop 3
	v_mov_b32_e32 v32, v132
	s_addc_u32 s55, s17, 0
	s_nop 0
	v_mov_b32_e32 v32, v133
	s_nop 0
	s_waitcnt vmcnt(4)
	s_barrier
	s_setprio 1
	v_mfma_scale_f32_16x16x128_f8f6f4 v[220:223], v[96:103], v[64:71], v[28:31], v136, v136 op_sel_hi:[0,0,0]
	v_mfma_scale_f32_16x16x128_f8f6f4 v[224:227], v[104:111], v[64:71], v[24:27], v136, v136 op_sel_hi:[0,0,0]
	s_mov_b32 m0, s42
	v_mfma_scale_f32_16x16x128_f8f6f4 v[228:231], v[96:103], v[72:79], v[20:23], v136, v136 op_sel_hi:[0,0,0]
	global_load_lds_dwordx4 v132, s[54:55]
	v_mfma_scale_f32_16x16x128_f8f6f4 v[232:235], v[104:111], v[72:79], v[16:19], v136, v136 op_sel_hi:[0,0,0]
	v_mfma_scale_f32_16x16x128_f8f6f4 v[236:239], v[96:103], v[80:87], v[12:15], v136, v136 op_sel_hi:[0,0,0]
	s_mov_b32 m0, s43
	v_mfma_scale_f32_16x16x128_f8f6f4 v[240:243], v[104:111], v[80:87], v[8:11], v136, v136 op_sel_hi:[0,0,0]
	global_load_lds_dwordx4 v133, s[54:55]
	v_mfma_scale_f32_16x16x128_f8f6f4 v[244:247], v[96:103], v[88:95], v[4:7], v136, v136 op_sel_hi:[0,0,0]
	v_mfma_scale_f32_16x16x128_f8f6f4 v[248:251], v[104:111], v[88:95], v[0:3], v136, v136 op_sel_hi:[0,0,0]
	s_setprio 0
	s_barrier
	s_nop 4
	ds_read_b128 v[0:3], v138
	ds_read_b128 v[4:7], v138 offset:1024
	ds_read_b128 v[8:11], v138 offset:2048
	ds_read_b128 v[12:15], v138 offset:3072
	s_add_u32 s54, s18, 0x30000
	v_mov_b32_e32 v64, v132
	ds_read_b128 v[16:19], v135 offset:32768
	ds_read_b128 v[20:23], v135 offset:33792
	ds_read_b128 v[24:27], v135 offset:34816
	ds_read_b128 v[28:31], v135 offset:35840
	ds_read_b128 v[32:35], v135 offset:36864
	ds_read_b128 v[36:39], v135 offset:37888
	ds_read_b128 v[40:43], v135 offset:38912
	ds_read_b128 v[44:47], v135 offset:39936
	s_addc_u32 s55, s19, 0
	s_nop 0
	v_mov_b32_e32 v64, v133
	s_nop 0
	s_waitcnt lgkmcnt(8)
	s_barrier
	s_waitcnt lgkmcnt(0)
	s_setprio 1
	s_waitcnt lgkmcnt(0)
	v_mfma_scale_f32_16x16x128_f8f6f4 v[124:127], v[0:7], v[16:23], v[124:127], v136, v136 op_sel_hi:[0,0,0]
	v_mfma_scale_f32_16x16x128_f8f6f4 v[120:123], v[8:15], v[16:23], v[120:123], v136, v136 op_sel_hi:[0,0,0]
	s_mov_b32 m0, s26
	v_mfma_scale_f32_16x16x128_f8f6f4 v[116:119], v[0:7], v[24:31], v[116:119], v136, v136 op_sel_hi:[0,0,0]
	global_load_lds_dwordx4 v132, s[54:55]
	v_mfma_scale_f32_16x16x128_f8f6f4 v[112:115], v[8:15], v[24:31], v[112:115], v136, v136 op_sel_hi:[0,0,0]
	v_mfma_scale_f32_16x16x128_f8f6f4 v[108:111], v[0:7], v[32:39], v[188:191], v136, v136 op_sel_hi:[0,0,0]
	s_mov_b32 m0, s27
	v_mfma_scale_f32_16x16x128_f8f6f4 v[104:107], v[8:15], v[32:39], v[192:195], v136, v136 op_sel_hi:[0,0,0]
	global_load_lds_dwordx4 v133, s[54:55]
	v_mfma_scale_f32_16x16x128_f8f6f4 v[100:103], v[0:7], v[40:47], v[196:199], v136, v136 op_sel_hi:[0,0,0]
	v_mfma_scale_f32_16x16x128_f8f6f4 v[96:99], v[8:15], v[40:47], v[200:203], v136, v136 op_sel_hi:[0,0,0]
	s_setprio 0
	s_barrier
	v_mov_b32_e32 v128, v132
	ds_read_b128 v[140:143], v139
	ds_read_b128 v[144:147], v139 offset:1024
	ds_read_b128 v[148:151], v139 offset:2048
	ds_read_b128 v[152:155], v139 offset:3072
	v_lshl_add_u64 v[64:65], s[16:17], 0, v[128:129]
	v_lshl_add_u64 v[64:65], v[64:65], 0, s[4:5]
	v_mov_b32_e32 v128, v133
	v_lshl_add_u64 v[64:65], s[16:17], 0, v[128:129]
	v_lshl_add_u64 v[64:65], v[64:65], 0, s[4:5]
	s_barrier
	s_waitcnt lgkmcnt(0)
	s_setprio 1
	s_waitcnt lgkmcnt(0)
	v_mfma_scale_f32_16x16x128_f8f6f4 v[92:95], v[140:147], v[16:23], v[204:207], v136, v136 op_sel_hi:[0,0,0]
	v_mfma_scale_f32_16x16x128_f8f6f4 v[88:91], v[148:155], v[16:23], v[156:159], v136, v136 op_sel_hi:[0,0,0]
	s_add_u32 s98, s16, s4
	s_addc_u32 s99, s17, s5
	s_mov_b32 m0, s45
	v_mfma_scale_f32_16x16x128_f8f6f4 v[84:87], v[140:147], v[24:31], v[160:163], v136, v136 op_sel_hi:[0,0,0]
	global_load_lds_dwordx4 v132, s[98:99]
	v_mfma_scale_f32_16x16x128_f8f6f4 v[80:83], v[148:155], v[24:31], v[164:167], v136, v136 op_sel_hi:[0,0,0]
	v_mfma_scale_f32_16x16x128_f8f6f4 v[76:79], v[140:147], v[32:39], v[168:171], v136, v136 op_sel_hi:[0,0,0]
	s_mov_b32 m0, s46
	v_mfma_scale_f32_16x16x128_f8f6f4 v[72:75], v[148:155], v[32:39], v[172:175], v136, v136 op_sel_hi:[0,0,0]
	global_load_lds_dwordx4 v133, s[98:99]
	v_mfma_scale_f32_16x16x128_f8f6f4 v[68:71], v[140:147], v[40:47], v[176:179], v136, v136 op_sel_hi:[0,0,0]
	v_mfma_scale_f32_16x16x128_f8f6f4 v[64:67], v[148:155], v[40:47], v[180:183], v136, v136 op_sel_hi:[0,0,0]
	s_setprio 0
	v_mov_b32_e32 v128, v132
	s_barrier
	ds_read_b128 v[16:19], v135 offset:49152
	ds_read_b128 v[20:23], v135 offset:50176
	ds_read_b128 v[156:159], v135 offset:51200
	ds_read_b128 v[160:163], v135 offset:52224
	ds_read_b128 v[164:167], v135 offset:53248
	ds_read_b128 v[168:171], v135 offset:54272
	ds_read_b128 v[172:175], v135 offset:55296
	ds_read_b128 v[176:179], v135 offset:56320
	v_lshl_add_u64 v[24:25], s[18:19], 0, v[128:129]
	v_lshl_add_u64 v[24:25], v[24:25], 0, s[4:5]
	v_mov_b32_e32 v128, v133
	v_lshl_add_u64 v[24:25], s[18:19], 0, v[128:129]
	v_lshl_add_u64 v[24:25], v[24:25], 0, s[4:5]
	s_barrier
	s_waitcnt lgkmcnt(0)
	s_setprio 1
	s_waitcnt lgkmcnt(0)
	v_mfma_scale_f32_16x16x128_f8f6f4 v[60:63], v[0:7], v[16:23], v[60:63], v136, v136 op_sel_hi:[0,0,0]
	v_mfma_scale_f32_16x16x128_f8f6f4 v[56:59], v[8:15], v[16:23], v[56:59], v136, v136 op_sel_hi:[0,0,0]
	s_add_u32 s98, s18, s4
	s_addc_u32 s99, s19, s5
	s_mov_b32 m0, s35
	v_mfma_scale_f32_16x16x128_f8f6f4 v[52:55], v[0:7], v[156:163], v[52:55], v136, v136 op_sel_hi:[0,0,0]
	global_load_lds_dwordx4 v132, s[98:99]
	v_mfma_scale_f32_16x16x128_f8f6f4 v[48:51], v[8:15], v[156:163], v[48:51], v136, v136 op_sel_hi:[0,0,0]
	v_mfma_scale_f32_16x16x128_f8f6f4 v[44:47], v[0:7], v[164:171], v[184:187], v136, v136 op_sel_hi:[0,0,0]
	s_mov_b32 m0, s36
	v_mfma_scale_f32_16x16x128_f8f6f4 v[40:43], v[8:15], v[164:171], v[208:211], v136, v136 op_sel_hi:[0,0,0]
	global_load_lds_dwordx4 v133, s[98:99]
	v_mfma_scale_f32_16x16x128_f8f6f4 v[36:39], v[0:7], v[172:179], v[212:215], v136, v136 op_sel_hi:[0,0,0]
	v_mfma_scale_f32_16x16x128_f8f6f4 v[32:35], v[8:15], v[172:179], v[216:219], v136, v136 op_sel_hi:[0,0,0]
	s_setprio 0
	s_barrier
	s_add_u32 s16, s16, 0x30080
	s_addc_u32 s17, s17, 0
	v_mov_b32_e32 v0, v132
	s_add_i32 s18, s44, s23
	s_nop 0
	v_mov_b32_e32 v0, v133
	s_nop 0
	s_waitcnt vmcnt(4)
	s_barrier
	s_setprio 1
	v_mfma_scale_f32_16x16x128_f8f6f4 v[28:31], v[140:147], v[16:23], v[220:223], v136, v136 op_sel_hi:[0,0,0]
	v_mfma_scale_f32_16x16x128_f8f6f4 v[24:27], v[148:155], v[16:23], v[224:227], v136, v136 op_sel_hi:[0,0,0]
	s_mov_b32 m0, s18
	v_mfma_scale_f32_16x16x128_f8f6f4 v[20:23], v[140:147], v[156:163], v[228:231], v136, v136 op_sel_hi:[0,0,0]
	global_load_lds_dwordx4 v132, s[16:17]
	v_mfma_scale_f32_16x16x128_f8f6f4 v[16:19], v[148:155], v[156:163], v[232:235], v136, v136 op_sel_hi:[0,0,0]
	v_mfma_scale_f32_16x16x128_f8f6f4 v[12:15], v[140:147], v[164:171], v[236:239], v136, v136 op_sel_hi:[0,0,0]
	s_add_i32 m0, s18, 0x2000
	v_mfma_scale_f32_16x16x128_f8f6f4 v[8:11], v[148:155], v[164:171], v[240:243], v136, v136 op_sel_hi:[0,0,0]
	global_load_lds_dwordx4 v133, s[16:17]
	v_mfma_scale_f32_16x16x128_f8f6f4 v[4:7], v[140:147], v[172:179], v[244:247], v136, v136 op_sel_hi:[0,0,0]
	v_mfma_scale_f32_16x16x128_f8f6f4 v[0:3], v[148:155], v[172:179], v[248:251], v136, v136 op_sel_hi:[0,0,0]
	s_setprio 0
	s_add_i32 s53, s53, 2
	s_add_u32 s14, s14, 0x100
	s_addc_u32 s15, s15, 0
	s_add_u32 s51, s51, 0x100
	s_addc_u32 s52, s52, 0
	s_cmp_gt_u32 s53, 9
	s_barrier
	s_cbranch_scc0 .LBB0_5813
	v_pk_mul_f32 v[140:141], v[124:125], s[6:7] op_sel_hi:[1,0]
	v_pk_mul_f32 v[120:121], v[120:121], s[6:7] op_sel_hi:[1,0]
	v_mov_b32_e32 v125, v129
	v_cvt_pk_fp8_f32 v125, v120, v121
	v_pk_mul_f32 v[120:121], v[126:127], s[6:7] op_sel_hi:[1,0]
	v_pk_mul_f32 v[116:117], v[116:117], s[6:7] op_sel_hi:[1,0]
	v_mov_b32_e32 v126, v129
	v_cvt_pk_fp8_f32 v126, v116, v117
	v_pk_mul_f32 v[112:113], v[112:113], s[6:7] op_sel_hi:[1,0]
	v_mov_b32_e32 v127, v129
	v_cvt_pk_fp8_f32 v127, v112, v113
	v_pk_mul_f32 v[112:113], v[118:119], s[6:7] op_sel_hi:[1,0]
	v_pk_mul_f32 v[104:105], v[104:105], s[6:7] op_sel_hi:[1,0]
	v_cvt_pk_fp8_f32 v126, v112, v113 op_sel:[0,0,1]
	v_pk_mul_f32 v[112:113], v[114:115], s[6:7] op_sel_hi:[1,0]
	v_pk_mul_f32 v[100:101], v[100:101], s[6:7] op_sel_hi:[1,0]
	v_cvt_pk_fp8_f32 v127, v112, v113 op_sel:[0,0,1]
	v_pk_mul_f32 v[112:113], v[108:109], s[6:7] op_sel_hi:[1,0]
	v_mov_b32_e32 v109, v129
	v_cvt_pk_fp8_f32 v109, v104, v105
	v_pk_mul_f32 v[104:105], v[110:111], s[6:7] op_sel_hi:[1,0]
	v_mov_b32_e32 v110, v129
	v_cvt_pk_fp8_f32 v110, v100, v101
	v_pk_mul_f32 v[100:101], v[92:93], s[6:7] op_sel_hi:[1,0]
	v_pk_mul_f32 v[88:89], v[88:89], s[6:7] op_sel_hi:[1,0]
	v_mov_b32_e32 v93, v129
	v_cvt_pk_fp8_f32 v93, v88, v89
	v_pk_mul_f32 v[88:89], v[94:95], s[6:7] op_sel_hi:[1,0]
	v_pk_mul_f32 v[84:85], v[84:85], s[6:7] op_sel_hi:[1,0]
	v_mov_b32_e32 v94, v129
	v_cvt_pk_fp8_f32 v94, v84, v85
	v_pk_mul_f32 v[80:81], v[80:81], s[6:7] op_sel_hi:[1,0]
	v_mov_b32_e32 v95, v129
	v_cvt_pk_fp8_f32 v95, v80, v81
	v_pk_mul_f32 v[80:81], v[86:87], s[6:7] op_sel_hi:[1,0]
	v_pk_mul_f32 v[72:73], v[72:73], s[6:7] op_sel_hi:[1,0]
	v_cvt_pk_fp8_f32 v94, v80, v81 op_sel:[0,0,1]
	v_pk_mul_f32 v[80:81], v[82:83], s[6:7] op_sel_hi:[1,0]
	v_pk_mul_f32 v[68:69], v[68:69], s[6:7] op_sel_hi:[1,0]
	v_cvt_pk_fp8_f32 v95, v80, v81 op_sel:[0,0,1]
	v_pk_mul_f32 v[80:81], v[76:77], s[6:7] op_sel_hi:[1,0]
	v_mov_b32_e32 v77, v129
	v_cvt_pk_fp8_f32 v77, v72, v73
	v_pk_mul_f32 v[72:73], v[78:79], s[6:7] op_sel_hi:[1,0]
	v_mov_b32_e32 v78, v129
	v_cvt_pk_fp8_f32 v78, v68, v69
	v_pk_mul_f32 v[64:65], v[64:65], s[6:7] op_sel_hi:[1,0]
	v_mov_b32_e32 v79, v129
	v_cvt_pk_fp8_f32 v79, v64, v65
	v_pk_mul_f32 v[64:65], v[70:71], s[6:7] op_sel_hi:[1,0]
	v_pk_mul_f32 v[56:57], v[56:57], s[6:7] op_sel_hi:[1,0]
	v_cvt_pk_fp8_f32 v78, v64, v65 op_sel:[0,0,1]
	v_pk_mul_f32 v[64:65], v[66:67], s[6:7] op_sel_hi:[1,0]
	v_pk_mul_f32 v[52:53], v[52:53], s[6:7] op_sel_hi:[1,0]
	v_cvt_pk_fp8_f32 v79, v64, v65 op_sel:[0,0,1]
	v_pk_mul_f32 v[64:65], v[60:61], s[6:7] op_sel_hi:[1,0]
	v_mov_b32_e32 v61, v129
	v_cvt_pk_fp8_f32 v61, v56, v57
	v_pk_mul_f32 v[56:57], v[62:63], s[6:7] op_sel_hi:[1,0]
	v_mov_b32_e32 v62, v129
	v_cvt_pk_fp8_f32 v62, v52, v53
	v_pk_mul_f32 v[48:49], v[48:49], s[6:7] op_sel_hi:[1,0]
	v_mov_b32_e32 v63, v129
	v_cvt_pk_fp8_f32 v63, v48, v49
	s_lshl_b32 s14, s49, 8
	v_pk_mul_f32 v[48:49], v[54:55], s[6:7] op_sel_hi:[1,0]
	s_add_i32 s14, s14, s33
	v_cvt_pk_fp8_f32 v62, v48, v49 op_sel:[0,0,1]
	v_pk_mul_f32 v[48:49], v[50:51], s[6:7] op_sel_hi:[1,0]
	s_lshl_b32 s16, s50, 8
	s_ashr_i32 s15, s14, 31
	v_cvt_pk_fp8_f32 v63, v48, v49 op_sel:[0,0,1]
	v_pk_mul_f32 v[48:49], v[44:45], s[6:7] op_sel_hi:[1,0]
	v_pk_mul_f32 v[40:41], v[40:41], s[6:7] op_sel_hi:[1,0]
	v_mov_b32_e32 v45, v129
	s_ashr_i32 s17, s16, 31
	s_lshl_b64 s[18:19], s[14:15], 11
	v_cvt_pk_fp8_f32 v45, v40, v41
	v_pk_mul_f32 v[40:41], v[46:47], s[6:7] op_sel_hi:[1,0]
	v_pk_mul_f32 v[36:37], v[36:37], s[6:7] op_sel_hi:[1,0]
	v_mov_b32_e32 v46, v129
	s_add_u32 s15, s30, s18
	v_cvt_pk_fp8_f32 v46, v36, v37
	v_pk_mul_f32 v[36:37], v[28:29], s[6:7] op_sel_hi:[1,0]
	v_pk_mul_f32 v[24:25], v[24:25], s[6:7] op_sel_hi:[1,0]
	v_mov_b32_e32 v29, v129
	s_addc_u32 s18, s31, s19
	v_cvt_pk_fp8_f32 v29, v24, v25
	v_pk_mul_f32 v[24:25], v[30:31], s[6:7] op_sel_hi:[1,0]
	v_pk_mul_f32 v[20:21], v[20:21], s[6:7] op_sel_hi:[1,0]
	v_mov_b32_e32 v30, v129
	s_add_u32 s15, s15, s16
	v_cvt_pk_fp8_f32 v30, v20, v21
	v_pk_mul_f32 v[16:17], v[16:17], s[6:7] op_sel_hi:[1,0]
	v_mov_b32_e32 v31, v129
	s_addc_u32 s19, s18, s17
	v_cvt_pk_fp8_f32 v31, v16, v17
	s_add_u32 s18, s15, s34
	s_addc_u32 s19, s19, 0
	s_addk_i32 s14, 0x80
	v_pk_mul_f32 v[16:17], v[22:23], s[6:7] op_sel_hi:[1,0]
	s_ashr_i32 s15, s14, 31
	v_cvt_pk_fp8_f32 v30, v16, v17 op_sel:[0,0,1]
	v_pk_mul_f32 v[16:17], v[18:19], s[6:7] op_sel_hi:[1,0]
	v_mov_b32_e32 v124, v129
	v_mov_b32_e32 v108, v129
	v_pk_mul_f32 v[96:97], v[96:97], s[6:7] op_sel_hi:[1,0]
	v_mov_b32_e32 v111, v129
	v_mov_b32_e32 v92, v129
	s_lshl_b64 s[14:15], s[14:15], 11
	v_mov_b32_e32 v60, v129
	v_mov_b32_e32 v44, v129
	v_mov_b32_e32 v28, v129
	v_cvt_pk_fp8_f32 v31, v16, v17 op_sel:[0,0,1]
	v_pk_mul_f32 v[16:17], v[12:13], s[6:7] op_sel_hi:[1,0]
	v_pk_mul_f32 v[8:9], v[8:9], s[6:7] op_sel_hi:[1,0]
	v_mov_b32_e32 v13, v129
	v_mbcnt_lo_u32_b32 v128, -1, 0
	v_mbcnt_hi_u32_b32 v128, -1, v128
	v_cvt_pk_fp8_f32 v124, v140, v141
	v_ashrrev_i32_e32 v130, 1, v128
	v_cvt_pk_fp8_f32 v108, v112, v113
	v_cvt_pk_fp8_f32 v111, v96, v97
	v_cvt_pk_fp8_f32 v92, v100, v101
	v_mov_b32_e32 v76, v129
	v_cvt_pk_fp8_f32 v60, v64, v65
	v_cvt_pk_fp8_f32 v44, v48, v49
	v_pk_mul_f32 v[32:33], v[32:33], s[6:7] op_sel_hi:[1,0]
	v_mov_b32_e32 v47, v129
	s_add_u32 s14, s30, s14
	v_cvt_pk_fp8_f32 v28, v36, v37
	v_mov_b32_e32 v12, v129
	v_cvt_pk_fp8_f32 v13, v8, v9
	v_pk_mul_f32 v[8:9], v[14:15], s[6:7] op_sel_hi:[1,0]
	v_pk_mul_f32 v[4:5], v[4:5], s[6:7] op_sel_hi:[1,0]
	v_mov_b32_e32 v14, v129
	v_bfi_b32 v130, -16, v130, v128
	v_cvt_pk_fp8_f32 v76, v80, v81
	v_cvt_pk_fp8_f32 v47, v32, v33
	s_addc_u32 s15, s31, s15
	v_cvt_pk_fp8_f32 v12, v16, v17
	v_cvt_pk_fp8_f32 v14, v4, v5
	v_pk_mul_f32 v[0:1], v[0:1], s[6:7] op_sel_hi:[1,0]
	v_mov_b32_e32 v15, v129
	v_ashrrev_i32_e32 v131, 31, v130
	v_pk_mul_f32 v[96:97], v[102:103], s[6:7] op_sel_hi:[1,0]
	s_add_u32 s14, s14, s16
	v_cvt_pk_fp8_f32 v15, v0, v1
	v_lshlrev_b64 v[130:131], 11, v[130:131]
	v_cvt_pk_fp8_f32 v110, v96, v97 op_sel:[0,0,1]
	v_pk_mul_f32 v[96:97], v[98:99], s[6:7] op_sel_hi:[1,0]
	v_pk_mul_f32 v[32:33], v[38:39], s[6:7] op_sel_hi:[1,0]
	s_addc_u32 s15, s15, s17
	v_and_b32_e32 v128, 16, v128
	v_cvt_pk_fp8_f32 v124, v120, v121 op_sel:[0,0,1]
	v_pk_mul_f32 v[120:121], v[122:123], s[6:7] op_sel_hi:[1,0]
	v_cvt_pk_fp8_f32 v108, v104, v105 op_sel:[0,0,1]
	v_pk_mul_f32 v[104:105], v[106:107], s[6:7] op_sel_hi:[1,0]
	v_cvt_pk_fp8_f32 v111, v96, v97 op_sel:[0,0,1]
	v_lshl_add_u64 v[96:97], s[18:19], 0, v[130:131]
	v_cvt_pk_fp8_f32 v92, v88, v89 op_sel:[0,0,1]
	v_pk_mul_f32 v[88:89], v[90:91], s[6:7] op_sel_hi:[1,0]
	v_cvt_pk_fp8_f32 v60, v56, v57 op_sel:[0,0,1]
	v_pk_mul_f32 v[56:57], v[58:59], s[6:7] op_sel_hi:[1,0]
	v_cvt_pk_fp8_f32 v44, v40, v41 op_sel:[0,0,1]
	v_pk_mul_f32 v[40:41], v[42:43], s[6:7] op_sel_hi:[1,0]
	v_cvt_pk_fp8_f32 v46, v32, v33 op_sel:[0,0,1]
	v_pk_mul_f32 v[32:33], v[34:35], s[6:7] op_sel_hi:[1,0]
	s_add_u32 s14, s14, s34
	v_cvt_pk_fp8_f32 v28, v24, v25 op_sel:[0,0,1]
	v_pk_mul_f32 v[24:25], v[26:27], s[6:7] op_sel_hi:[1,0]
	v_pk_mul_f32 v[0:1], v[6:7], s[6:7] op_sel_hi:[1,0]
	v_cvt_pk_fp8_f32 v125, v120, v121 op_sel:[0,0,1]
	v_cvt_pk_fp8_f32 v109, v104, v105 op_sel:[0,0,1]
	v_lshl_add_u64 v[96:97], v[96:97], 0, v[128:129]
	v_cvt_pk_fp8_f32 v93, v88, v89 op_sel:[0,0,1]
	v_cvt_pk_fp8_f32 v76, v72, v73 op_sel:[0,0,1]
	v_pk_mul_f32 v[72:73], v[74:75], s[6:7] op_sel_hi:[1,0]
	v_cvt_pk_fp8_f32 v61, v56, v57 op_sel:[0,0,1]
	v_cvt_pk_fp8_f32 v45, v40, v41 op_sel:[0,0,1]
	v_cvt_pk_fp8_f32 v47, v32, v33 op_sel:[0,0,1]
	s_addc_u32 s15, s15, 0
	v_cvt_pk_fp8_f32 v29, v24, v25 op_sel:[0,0,1]
	v_cvt_pk_fp8_f32 v12, v8, v9 op_sel:[0,0,1]
	v_pk_mul_f32 v[8:9], v[10:11], s[6:7] op_sel_hi:[1,0]
	v_cvt_pk_fp8_f32 v14, v0, v1 op_sel:[0,0,1]
	v_pk_mul_f32 v[0:1], v[2:3], s[6:7] op_sel_hi:[1,0]
	v_add_co_u32_e32 v98, vcc, s29, v96
	v_cvt_pk_fp8_f32 v77, v72, v73 op_sel:[0,0,1]
	v_lshl_add_u64 v[32:33], s[14:15], 0, v[130:131]
	v_cvt_pk_fp8_f32 v13, v8, v9 op_sel:[0,0,1]
	v_cvt_pk_fp8_f32 v15, v0, v1 op_sel:[0,0,1]
	v_addc_co_u32_e32 v99, vcc, 0, v97, vcc
	v_lshl_add_u64 v[32:33], v[32:33], 0, v[128:129]
	v_add_co_u32_e32 v34, vcc, s29, v32
	v_permlane32_swap_b32_e32 v124, v126
	v_permlane32_swap_b32_e32 v125, v127
	v_permlane32_swap_b32_e32 v108, v110
	v_permlane32_swap_b32_e32 v109, v111
	v_permlane32_swap_b32_e32 v92, v94
	v_permlane32_swap_b32_e32 v93, v95
	v_permlane32_swap_b32_e32 v60, v62
	v_permlane32_swap_b32_e32 v61, v63
	v_permlane32_swap_b32_e32 v44, v46
	v_permlane32_swap_b32_e32 v45, v47
	v_addc_co_u32_e32 v35, vcc, 0, v33, vcc
	v_permlane32_swap_b32_e32 v28, v30
	v_permlane32_swap_b32_e32 v29, v31
	v_permlane16_swap_b32_e32 v124, v125
	v_permlane16_swap_b32_e32 v126, v127
	v_permlane16_swap_b32_e32 v108, v109
	v_permlane16_swap_b32_e32 v110, v111
	v_permlane16_swap_b32_e32 v92, v93
	v_permlane16_swap_b32_e32 v94, v95
	v_permlane32_swap_b32_e32 v76, v78
	v_permlane32_swap_b32_e32 v77, v79
	v_permlane16_swap_b32_e32 v60, v61
	v_permlane16_swap_b32_e32 v62, v63
	v_permlane16_swap_b32_e32 v44, v45
	v_permlane16_swap_b32_e32 v46, v47
	v_permlane16_swap_b32_e32 v28, v29
	v_permlane16_swap_b32_e32 v30, v31
	v_permlane32_swap_b32_e32 v12, v14
	v_permlane32_swap_b32_e32 v13, v15
	s_and_b64 vcc, exec, s[8:9]
	s_mov_b32 s50, s48
	s_mov_b32 s49, s47
	s_mov_b64 s[16:17], s[10:11]
	s_mov_b64 s[14:15], s[12:13]
	global_store_dwordx4 v[96:97], v[124:127], off
	global_store_dwordx4 v[98:99], v[108:111], off
	v_permlane16_swap_b32_e32 v76, v77
	v_permlane16_swap_b32_e32 v78, v79
	global_store_dwordx4 v[96:97], v[92:95], off offset:128
	global_store_dwordx4 v[98:99], v[76:79], off offset:128
	global_store_dwordx4 v[32:33], v[60:63], off
	global_store_dwordx4 v[34:35], v[44:47], off
	v_permlane16_swap_b32_e32 v12, v13
	v_permlane16_swap_b32_e32 v14, v15
	global_store_dwordx4 v[32:33], v[28:31], off offset:128
	global_store_dwordx4 v[34:35], v[12:15], off offset:128
	s_cbranch_vccz .LBB0_5808
	s_waitcnt vmcnt(0)
	v_readlane_b32 s0, v252, 2
	s_cmpk_gt_u32 s0, 0xff
	s_cbranch_scc1 .LBB0_5817
	s_barrier

	.amdhsa_kernel _Z10fwd_kernel6Params
		.amdhsa_group_segment_fixed_size 0
		.amdhsa_private_segment_fixed_size 0
		.amdhsa_kernarg_size 648
		.amdhsa_user_sgpr_count 2
		.amdhsa_user_sgpr_dispatch_ptr 0
		.amdhsa_user_sgpr_queue_ptr 0
		.amdhsa_user_sgpr_kernarg_segment_ptr 1
		.amdhsa_user_sgpr_dispatch_id 0
		.amdhsa_user_sgpr_kernarg_preload_length 0
		.amdhsa_user_sgpr_kernarg_preload_offset 0
		.amdhsa_user_sgpr_private_segment_size 0
		.amdhsa_uses_dynamic_stack 0
		.amdhsa_enable_private_segment 0
		.amdhsa_system_sgpr_workgroup_id_x 1
		.amdhsa_system_sgpr_workgroup_id_y 0
		.amdhsa_system_sgpr_workgroup_id_z 0
		.amdhsa_system_sgpr_workgroup_info 0
		.amdhsa_system_vgpr_workitem_id 0
		.amdhsa_next_free_vgpr 256
		.amdhsa_next_free_sgpr 102
		.amdhsa_accum_offset 256
		.amdhsa_reserve_vcc 1
		.amdhsa_float_round_mode_32 0
		.amdhsa_float_round_mode_16_64 0
		.amdhsa_float_denorm_mode_32 3
		.amdhsa_float_denorm_mode_16_64 3
		.amdhsa_dx10_clamp 1
		.amdhsa_ieee_mode 1
		.amdhsa_fp16_overflow 0
		.amdhsa_tg_split 0
		.amdhsa_exception_fp_ieee_invalid_op 0
		.amdhsa_exception_fp_denorm_src 0
		.amdhsa_exception_fp_ieee_div_zero 0
		.amdhsa_exception_fp_ieee_overflow 0
		.amdhsa_exception_fp_ieee_underflow 0
		.amdhsa_exception_fp_ieee_inexact 0
		.amdhsa_exception_int_div_zero 0
	.end_amdhsa_kernel

amdhsa.kernels:
  - .agpr_count:     0
    .args:
      - .offset:         0
        .size:           392
        .value_kind:     by_value
      - .offset:         392
        .size:           4
        .value_kind:     hidden_block_count_x
      - .offset:         396
        .size:           4
        .value_kind:     hidden_block_count_y
      - .offset:         400
        .size:           4
        .value_kind:     hidden_block_count_z
      - .offset:         404
        .size:           2
        .value_kind:     hidden_group_size_x
      - .offset:         406
        .size:           2
        .value_kind:     hidden_group_size_y
      - .offset:         408
        .size:           2
        .value_kind:     hidden_group_size_z
      - .offset:         410
        .size:           2
        .value_kind:     hidden_remainder_x
      - .offset:         412
        .size:           2
        .value_kind:     hidden_remainder_y
      - .offset:         414
        .size:           2
        .value_kind:     hidden_remainder_z
      - .offset:         432
        .size:           8
        .value_kind:     hidden_global_offset_x
      - .offset:         440
        .size:           8
        .value_kind:     hidden_global_offset_y
      - .offset:         448
        .size:           8
        .value_kind:     hidden_global_offset_z
      - .offset:         456
        .size:           2
        .value_kind:     hidden_grid_dims
      - .offset:         512
        .size:           4
        .value_kind:     hidden_dynamic_lds_size
    .group_segment_fixed_size: 0
    .kernarg_segment_align: 8
    .kernarg_segment_size: 648
    .language:       OpenCL C
    .language_version:
      - 2
      - 0
    .max_flat_workgroup_size: 512
    .name:           _Z10fwd_kernel6Params
    .private_segment_fixed_size: 0
    .sgpr_count:     108
    .sgpr_spill_count: 2244
    .symbol:         _Z10fwd_kernel6Params.kd
    .uniform_work_group_size: 1
    .uses_dynamic_stack: false
    .vgpr_count:     256
    .vgpr_spill_count: 0
    .wavefront_size: 64
